# P1: 72 converter workgroups + every in-projection epilogue store non-temporal
# speedup vs baseline: 1.0057x; 1.0057x over previous
; __device__ __forceinline__ unsigned cvt_pk_bf16(float lo, float hi) { f32x2 v = {lo, hi}; bf16x2_t b = __builtin_convertvector(v, bf16x2_t); return __builtin_bit_cast(unsigned, b); }
; __device__ __forceinline__ float sigmoid_f(float x) { return __builtin_amdgcn_rcpf(1.0f + __expf(-x)); }
;     __device__ __forceinline__ void operator()(const AccT& acc, const pg8::Unit& u, int wr, int wc, int fr, int fq) const {
;     ...
;             const int kind = (pn - 16) >> 3;
;             bf16_t* dst = (bf16_t*)(ws + (kind == 0 ? WS_RV : kind == 1 ? WS_RG : kind == 2 ? WS_GA : WS_GR)); const int col0 = ((pn - 16) & 7) * 256 + wc * 32 + 8 * fq;
; #pragma unroll
;             for (int ai = 0; ai < 2; ++ai)
; #pragma unroll
;                 for (int m = 0; m < 4; ++m) { const int row = row0 + ai * 128 + m * 16;
; #pragma unroll
;                     for (int bj = 0; bj < 2; ++bj) { f32x4 v0 = acc[ai][bj][m][0], v1 = acc[ai][bj][m][1];
;                         if (kind == 1) {
; #pragma unroll
;                             for (int j = 0; j < 4; ++j) { v0[j] = v0[j] * sigmoid_f(v0[j]); v1[j] = v1[j] * sigmoid_f(v1[j]); } }
;                         else if (kind >= 2) {
; #pragma unroll
;                             for (int j = 0; j < 4; ++j) { v0[j] = sigmoid_f(v0[j]); v1[j] = sigmoid_f(v1[j]); } }
;                         u32x4 w; w.x = cvt_pk_bf16(v0[0], v0[1]); w.y = cvt_pk_bf16(v0[2], v0[3]); w.z = cvt_pk_bf16(v1[0], v1[1]); w.w = cvt_pk_bf16(v1[2], v1[3]);
;                         if (kind >= 1) __builtin_nontemporal_store(w, (u32x4*)(dst + (size_t)row * D + col0 + bj * 128));
;                         else *(u32x4*)(dst + (size_t)row * D + col0 + bj * 128) = w; } }
.LBB0_152:
	s_cmp_eq_u32 s4, 2
	s_cselect_b32 s4, s76, 0x4c600000
	s_and_b64 s[54:55], s[54:55], exec
	s_cselect_b32 s4, 0x44600000, s4
	s_and_b64 s[12:13], s[12:13], exec
	s_cselect_b32 s4, 0x40600000, s4
	s_add_u32 s12, s94, s4
	s_addc_u32 s13, s95, 0
	s_lshl_b32 s4, s52, 8
	s_and_b32 s4, s4, 0x700
	v_or_b32_e32 v130, s4, v162
	v_lshlrev_b32_e32 v130, 1, v130
	v_ashrrev_i32_e32 v143, 31, v142
	v_lshl_add_u64 v[144:145], s[12:13], 0, v[130:131]
	v_lshlrev_b64 v[146:147], 12, v[142:143]
	v_cndmask_b32_e64 v130, 0, 1, s[0:1]
	v_lshl_add_u64 v[146:147], v[144:145], 0, v[146:147]
	v_cvt_pk_bf16_f32 v148, v148, v149
	v_cvt_pk_bf16_f32 v149, v152, v153
	v_cvt_pk_bf16_f32 v150, v150, v151
	v_cvt_pk_bf16_f32 v151, v154, v155
	v_cmp_ne_u32_e64 s[12:13], 1, v130
	s_andn2_b64 vcc, exec, s[0:1]
	s_mov_b64 s[0:1], -1
	global_store_dwordx4 v[146:147], v[148:151], off nt
	s_cbranch_vccnz .LBB0_156
	s_and_b64 vcc, exec, s[10:11]
	v_mov_b32_e32 v155, v117
	v_mov_b32_e32 v154, v116
	v_mov_b32_e32 v151, v115
	v_mov_b32_e32 v150, v114
	v_mov_b32_e32 v153, v121
	v_mov_b32_e32 v152, v120
	v_mov_b32_e32 v149, v119
	v_mov_b32_e32 v148, v118
	s_cbranch_vccnz .LBB0_155
	v_mul_f32_e32 v130, 0xbfb8aa3b, v118
	v_exp_f32_e32 v130, v130
	v_mul_f32_e32 v141, 0xbfb8aa3b, v114
	v_exp_f32_e32 v141, v141
	v_mul_f32_e32 v149, 0xbfb8aa3b, v115
	v_add_f32_e32 v130, 1.0, v130
	v_rcp_f32_e32 v148, v130
	v_mul_f32_e32 v130, 0xbfb8aa3b, v119
	v_exp_f32_e32 v130, v130
	v_exp_f32_e32 v151, v149
	v_add_f32_e32 v141, 1.0, v141
	v_rcp_f32_e32 v150, v141
	v_add_f32_e32 v130, 1.0, v130
	v_mul_f32_e32 v141, 0xbfb8aa3b, v120
	v_rcp_f32_e32 v149, v130
	v_add_f32_e32 v130, 1.0, v151
	v_exp_f32_e32 v141, v141
	v_mul_f32_e32 v151, 0xbfb8aa3b, v116
	v_exp_f32_e32 v153, v151
	v_rcp_f32_e32 v151, v130
	v_add_f32_e32 v130, 1.0, v141
	v_mul_f32_e32 v141, 0xbfb8aa3b, v121
	v_rcp_f32_e32 v152, v130
	v_add_f32_e32 v130, 1.0, v153
	v_exp_f32_e32 v141, v141
	v_mul_f32_e32 v153, 0xbfb8aa3b, v117
	v_exp_f32_e32 v155, v153
	v_rcp_f32_e32 v154, v130
	v_add_f32_e32 v130, 1.0, v141
	v_rcp_f32_e32 v153, v130
	v_add_f32_e32 v130, 1.0, v155
	v_rcp_f32_e32 v155, v130

; __device__ __forceinline__ unsigned cvt_pk_bf16(float lo, float hi) { f32x2 v = {lo, hi}; bf16x2_t b = __builtin_convertvector(v, bf16x2_t); return __builtin_bit_cast(unsigned, b); }
; __device__ __forceinline__ float sigmoid_f(float x) { return __builtin_amdgcn_rcpf(1.0f + __expf(-x)); }
;     __device__ __forceinline__ void operator()(const AccT& acc, const pg8::Unit& u, int wr, int wc, int fr, int fq) const {
;     ...
;                     for (int bj = 0; bj < 2; ++bj) { f32x4 v0 = acc[ai][bj][m][0], v1 = acc[ai][bj][m][1];
;                         if (kind == 1) {
; #pragma unroll
;                             for (int j = 0; j < 4; ++j) { v0[j] = v0[j] * sigmoid_f(v0[j]); v1[j] = v1[j] * sigmoid_f(v1[j]); } }
;                         else if (kind >= 2) {
; #pragma unroll
;                             for (int j = 0; j < 4; ++j) { v0[j] = sigmoid_f(v0[j]); v1[j] = sigmoid_f(v1[j]); } }
;                         u32x4 w; w.x = cvt_pk_bf16(v0[0], v0[1]); w.y = cvt_pk_bf16(v0[2], v0[3]); w.z = cvt_pk_bf16(v1[0], v1[1]); w.w = cvt_pk_bf16(v1[2], v1[3]);
;                         if (kind >= 1) __builtin_nontemporal_store(w, (u32x4*)(dst + (size_t)row * D + col0 + bj * 128));
;                         else *(u32x4*)(dst + (size_t)row * D + col0 + bj * 128) = w; } }
.LBB0_158:
	v_cvt_pk_bf16_f32 v148, v148, v149
	v_cvt_pk_bf16_f32 v149, v152, v153
	v_cvt_pk_bf16_f32 v150, v150, v151
	v_cvt_pk_bf16_f32 v151, v154, v155
	s_and_b64 vcc, exec, s[12:13]
	s_mov_b64 s[0:1], -1
	global_store_dwordx4 v[146:147], v[148:151], off offset:256 nt
	s_cbranch_vccnz .LBB0_162
	s_and_b64 vcc, exec, s[10:11]
	v_mov_b32_e32 v155, v109
	v_mov_b32_e32 v154, v108
	v_mov_b32_e32 v151, v107
	v_mov_b32_e32 v150, v106
	v_mov_b32_e32 v153, v113
	v_mov_b32_e32 v152, v112
	v_mov_b32_e32 v149, v111
	v_mov_b32_e32 v148, v110
	s_cbranch_vccnz .LBB0_161
	v_mul_f32_e32 v130, 0xbfb8aa3b, v110
	v_exp_f32_e32 v130, v130
	v_mul_f32_e32 v141, 0xbfb8aa3b, v106
	v_exp_f32_e32 v141, v141
	v_mul_f32_e32 v146, 0xbfb8aa3b, v107
	v_add_f32_e32 v130, 1.0, v130
	v_rcp_f32_e32 v148, v130
	v_mul_f32_e32 v130, 0xbfb8aa3b, v111
	v_exp_f32_e32 v130, v130
	v_exp_f32_e32 v146, v146
	v_add_f32_e32 v141, 1.0, v141
	v_rcp_f32_e32 v150, v141
	v_add_f32_e32 v130, 1.0, v130
	v_mul_f32_e32 v141, 0xbfb8aa3b, v112
	v_rcp_f32_e32 v149, v130
	v_add_f32_e32 v130, 1.0, v146
	v_exp_f32_e32 v141, v141
	v_mul_f32_e32 v146, 0xbfb8aa3b, v108
	v_exp_f32_e32 v146, v146
	v_rcp_f32_e32 v151, v130
	v_add_f32_e32 v130, 1.0, v141
	v_mul_f32_e32 v141, 0xbfb8aa3b, v113
	v_rcp_f32_e32 v152, v130
	v_add_f32_e32 v130, 1.0, v146
	v_exp_f32_e32 v141, v141
	v_mul_f32_e32 v146, 0xbfb8aa3b, v109
	v_exp_f32_e32 v146, v146
	v_rcp_f32_e32 v154, v130
	v_add_f32_e32 v130, 1.0, v141
	v_rcp_f32_e32 v153, v130
	v_add_f32_e32 v130, 1.0, v146
	v_rcp_f32_e32 v155, v130

; __device__ __forceinline__ unsigned cvt_pk_bf16(float lo, float hi) { f32x2 v = {lo, hi}; bf16x2_t b = __builtin_convertvector(v, bf16x2_t); return __builtin_bit_cast(unsigned, b); }
; __device__ __forceinline__ float sigmoid_f(float x) { return __builtin_amdgcn_rcpf(1.0f + __expf(-x)); }
;     __device__ __forceinline__ void operator()(const AccT& acc, const pg8::Unit& u, int wr, int wc, int fr, int fq) const {
;     ...
;                     for (int bj = 0; bj < 2; ++bj) { f32x4 v0 = acc[ai][bj][m][0], v1 = acc[ai][bj][m][1];
;                         if (kind == 1) {
; #pragma unroll
;                             for (int j = 0; j < 4; ++j) { v0[j] = v0[j] * sigmoid_f(v0[j]); v1[j] = v1[j] * sigmoid_f(v1[j]); } }
;                         else if (kind >= 2) {
; #pragma unroll
;                             for (int j = 0; j < 4; ++j) { v0[j] = sigmoid_f(v0[j]); v1[j] = sigmoid_f(v1[j]); } }
;                         u32x4 w; w.x = cvt_pk_bf16(v0[0], v0[1]); w.y = cvt_pk_bf16(v0[2], v0[3]); w.z = cvt_pk_bf16(v1[0], v1[1]); w.w = cvt_pk_bf16(v1[2], v1[3]);
;                         if (kind >= 1) __builtin_nontemporal_store(w, (u32x4*)(dst + (size_t)row * D + col0 + bj * 128));
;                         else *(u32x4*)(dst + (size_t)row * D + col0 + bj * 128) = w; } }
.LBB0_164:
	v_or_b32_e32 v146, 16, v142
	v_ashrrev_i32_e32 v147, 31, v146
	v_lshlrev_b64 v[146:147], 12, v[146:147]
	v_lshl_add_u64 v[146:147], v[144:145], 0, v[146:147]
	v_cvt_pk_bf16_f32 v148, v148, v149
	v_cvt_pk_bf16_f32 v149, v152, v153
	v_cvt_pk_bf16_f32 v150, v150, v151
	v_cvt_pk_bf16_f32 v151, v154, v155
	s_and_b64 vcc, exec, s[12:13]
	s_mov_b64 s[0:1], -1
	global_store_dwordx4 v[146:147], v[148:151], off nt
	s_cbranch_vccnz .LBB0_168
	s_and_b64 vcc, exec, s[10:11]
	v_mov_b32_e32 v155, v101
	v_mov_b32_e32 v154, v100
	v_mov_b32_e32 v151, v99
	v_mov_b32_e32 v150, v98
	v_mov_b32_e32 v153, v105
	v_mov_b32_e32 v152, v104
	v_mov_b32_e32 v149, v103
	v_mov_b32_e32 v148, v102
	s_cbranch_vccnz .LBB0_167
	v_mul_f32_e32 v130, 0xbfb8aa3b, v102
	v_exp_f32_e32 v130, v130
	v_mul_f32_e32 v141, 0xbfb8aa3b, v98
	v_exp_f32_e32 v141, v141
	v_mul_f32_e32 v149, 0xbfb8aa3b, v99
	v_add_f32_e32 v130, 1.0, v130
	v_rcp_f32_e32 v148, v130
	v_mul_f32_e32 v130, 0xbfb8aa3b, v103
	v_exp_f32_e32 v130, v130
	v_exp_f32_e32 v151, v149
	v_add_f32_e32 v141, 1.0, v141
	v_rcp_f32_e32 v150, v141
	v_add_f32_e32 v130, 1.0, v130
	v_mul_f32_e32 v141, 0xbfb8aa3b, v104
	v_rcp_f32_e32 v149, v130
	v_add_f32_e32 v130, 1.0, v151
	v_exp_f32_e32 v141, v141
	v_mul_f32_e32 v151, 0xbfb8aa3b, v100
	v_exp_f32_e32 v153, v151
	v_rcp_f32_e32 v151, v130
	v_add_f32_e32 v130, 1.0, v141
	v_mul_f32_e32 v141, 0xbfb8aa3b, v105
	v_rcp_f32_e32 v152, v130
	v_add_f32_e32 v130, 1.0, v153
	v_exp_f32_e32 v141, v141
	v_mul_f32_e32 v153, 0xbfb8aa3b, v101
	v_exp_f32_e32 v155, v153
	v_rcp_f32_e32 v154, v130
	v_add_f32_e32 v130, 1.0, v141
	v_rcp_f32_e32 v153, v130
	v_add_f32_e32 v130, 1.0, v155
	v_rcp_f32_e32 v155, v130

; __device__ __forceinline__ unsigned cvt_pk_bf16(float lo, float hi) { f32x2 v = {lo, hi}; bf16x2_t b = __builtin_convertvector(v, bf16x2_t); return __builtin_bit_cast(unsigned, b); }
; __device__ __forceinline__ float sigmoid_f(float x) { return __builtin_amdgcn_rcpf(1.0f + __expf(-x)); }
;     __device__ __forceinline__ void operator()(const AccT& acc, const pg8::Unit& u, int wr, int wc, int fr, int fq) const {
;     ...
;                     for (int bj = 0; bj < 2; ++bj) { f32x4 v0 = acc[ai][bj][m][0], v1 = acc[ai][bj][m][1];
;                         if (kind == 1) {
; #pragma unroll
;                             for (int j = 0; j < 4; ++j) { v0[j] = v0[j] * sigmoid_f(v0[j]); v1[j] = v1[j] * sigmoid_f(v1[j]); } }
;                         else if (kind >= 2) {
; #pragma unroll
;                             for (int j = 0; j < 4; ++j) { v0[j] = sigmoid_f(v0[j]); v1[j] = sigmoid_f(v1[j]); } }
;                         u32x4 w; w.x = cvt_pk_bf16(v0[0], v0[1]); w.y = cvt_pk_bf16(v0[2], v0[3]); w.z = cvt_pk_bf16(v1[0], v1[1]); w.w = cvt_pk_bf16(v1[2], v1[3]);
;                         if (kind >= 1) __builtin_nontemporal_store(w, (u32x4*)(dst + (size_t)row * D + col0 + bj * 128));
;                         else *(u32x4*)(dst + (size_t)row * D + col0 + bj * 128) = w; } }
.LBB0_170:
	v_cvt_pk_bf16_f32 v148, v148, v149
	v_cvt_pk_bf16_f32 v149, v152, v153
	v_cvt_pk_bf16_f32 v150, v150, v151
	v_cvt_pk_bf16_f32 v151, v154, v155
	s_and_b64 vcc, exec, s[12:13]
	s_mov_b64 s[0:1], -1
	global_store_dwordx4 v[146:147], v[148:151], off offset:256 nt
	s_cbranch_vccnz .LBB0_174
	s_and_b64 vcc, exec, s[10:11]
	v_mov_b32_e32 v155, v93
	v_mov_b32_e32 v154, v92
	v_mov_b32_e32 v151, v91
	v_mov_b32_e32 v150, v90
	v_mov_b32_e32 v153, v97
	v_mov_b32_e32 v152, v96
	v_mov_b32_e32 v149, v95
	v_mov_b32_e32 v148, v94
	s_cbranch_vccnz .LBB0_173
	v_mul_f32_e32 v130, 0xbfb8aa3b, v94
	v_exp_f32_e32 v130, v130
	v_mul_f32_e32 v141, 0xbfb8aa3b, v90
	v_exp_f32_e32 v141, v141
	v_mul_f32_e32 v146, 0xbfb8aa3b, v91
	v_add_f32_e32 v130, 1.0, v130
	v_rcp_f32_e32 v148, v130
	v_mul_f32_e32 v130, 0xbfb8aa3b, v95
	v_exp_f32_e32 v130, v130
	v_exp_f32_e32 v146, v146
	v_add_f32_e32 v141, 1.0, v141
	v_rcp_f32_e32 v150, v141
	v_add_f32_e32 v130, 1.0, v130
	v_mul_f32_e32 v141, 0xbfb8aa3b, v96
	v_rcp_f32_e32 v149, v130
	v_add_f32_e32 v130, 1.0, v146
	v_exp_f32_e32 v141, v141
	v_mul_f32_e32 v146, 0xbfb8aa3b, v92
	v_exp_f32_e32 v146, v146
	v_rcp_f32_e32 v151, v130
	v_add_f32_e32 v130, 1.0, v141
	v_mul_f32_e32 v141, 0xbfb8aa3b, v97
	v_rcp_f32_e32 v152, v130
	v_add_f32_e32 v130, 1.0, v146
	v_exp_f32_e32 v141, v141
	v_mul_f32_e32 v146, 0xbfb8aa3b, v93
	v_exp_f32_e32 v146, v146
	v_rcp_f32_e32 v154, v130
	v_add_f32_e32 v130, 1.0, v141
	v_rcp_f32_e32 v153, v130
	v_add_f32_e32 v130, 1.0, v146
	v_rcp_f32_e32 v155, v130

; __device__ __forceinline__ unsigned cvt_pk_bf16(float lo, float hi) { f32x2 v = {lo, hi}; bf16x2_t b = __builtin_convertvector(v, bf16x2_t); return __builtin_bit_cast(unsigned, b); }
; __device__ __forceinline__ float sigmoid_f(float x) { return __builtin_amdgcn_rcpf(1.0f + __expf(-x)); }
;     __device__ __forceinline__ void operator()(const AccT& acc, const pg8::Unit& u, int wr, int wc, int fr, int fq) const {
;     ...
;                     for (int bj = 0; bj < 2; ++bj) { f32x4 v0 = acc[ai][bj][m][0], v1 = acc[ai][bj][m][1];
;                         if (kind == 1) {
; #pragma unroll
;                             for (int j = 0; j < 4; ++j) { v0[j] = v0[j] * sigmoid_f(v0[j]); v1[j] = v1[j] * sigmoid_f(v1[j]); } }
;                         else if (kind >= 2) {
; #pragma unroll
;                             for (int j = 0; j < 4; ++j) { v0[j] = sigmoid_f(v0[j]); v1[j] = sigmoid_f(v1[j]); } }
;                         u32x4 w; w.x = cvt_pk_bf16(v0[0], v0[1]); w.y = cvt_pk_bf16(v0[2], v0[3]); w.z = cvt_pk_bf16(v1[0], v1[1]); w.w = cvt_pk_bf16(v1[2], v1[3]);
;                         if (kind >= 1) __builtin_nontemporal_store(w, (u32x4*)(dst + (size_t)row * D + col0 + bj * 128));
;                         else *(u32x4*)(dst + (size_t)row * D + col0 + bj * 128) = w; } }
.LBB0_176:
	v_or_b32_e32 v146, 32, v142
	v_ashrrev_i32_e32 v147, 31, v146
	v_lshlrev_b64 v[146:147], 12, v[146:147]
	v_lshl_add_u64 v[146:147], v[144:145], 0, v[146:147]
	v_cvt_pk_bf16_f32 v148, v148, v149
	v_cvt_pk_bf16_f32 v149, v152, v153
	v_cvt_pk_bf16_f32 v150, v150, v151
	v_cvt_pk_bf16_f32 v151, v154, v155
	s_and_b64 vcc, exec, s[12:13]
	s_mov_b64 s[0:1], -1
	global_store_dwordx4 v[146:147], v[148:151], off nt
	s_cbranch_vccnz .LBB0_180
	s_and_b64 vcc, exec, s[10:11]
	v_mov_b32_e32 v155, v85
	v_mov_b32_e32 v154, v84
	v_mov_b32_e32 v151, v83
	v_mov_b32_e32 v150, v82
	v_mov_b32_e32 v153, v89
	v_mov_b32_e32 v152, v88
	v_mov_b32_e32 v149, v87
	v_mov_b32_e32 v148, v86
	s_cbranch_vccnz .LBB0_179
	v_mul_f32_e32 v130, 0xbfb8aa3b, v86
	v_exp_f32_e32 v130, v130
	v_mul_f32_e32 v141, 0xbfb8aa3b, v82
	v_exp_f32_e32 v141, v141
	v_mul_f32_e32 v149, 0xbfb8aa3b, v83
	v_add_f32_e32 v130, 1.0, v130
	v_rcp_f32_e32 v148, v130
	v_mul_f32_e32 v130, 0xbfb8aa3b, v87
	v_exp_f32_e32 v130, v130
	v_exp_f32_e32 v151, v149
	v_add_f32_e32 v141, 1.0, v141
	v_rcp_f32_e32 v150, v141
	v_add_f32_e32 v130, 1.0, v130
	v_mul_f32_e32 v141, 0xbfb8aa3b, v88
	v_rcp_f32_e32 v149, v130
	v_add_f32_e32 v130, 1.0, v151
	v_exp_f32_e32 v141, v141
	v_mul_f32_e32 v151, 0xbfb8aa3b, v84
	v_exp_f32_e32 v153, v151
	v_rcp_f32_e32 v151, v130
	v_add_f32_e32 v130, 1.0, v141
	v_mul_f32_e32 v141, 0xbfb8aa3b, v89
	v_rcp_f32_e32 v152, v130
	v_add_f32_e32 v130, 1.0, v153
	v_exp_f32_e32 v141, v141
	v_mul_f32_e32 v153, 0xbfb8aa3b, v85
	v_exp_f32_e32 v155, v153
	v_rcp_f32_e32 v154, v130
	v_add_f32_e32 v130, 1.0, v141
	v_rcp_f32_e32 v153, v130
	v_add_f32_e32 v130, 1.0, v155
	v_rcp_f32_e32 v155, v130

; __device__ __forceinline__ unsigned cvt_pk_bf16(float lo, float hi) { f32x2 v = {lo, hi}; bf16x2_t b = __builtin_convertvector(v, bf16x2_t); return __builtin_bit_cast(unsigned, b); }
; __device__ __forceinline__ float sigmoid_f(float x) { return __builtin_amdgcn_rcpf(1.0f + __expf(-x)); }
;     __device__ __forceinline__ void operator()(const AccT& acc, const pg8::Unit& u, int wr, int wc, int fr, int fq) const {
;     ...
;                     for (int bj = 0; bj < 2; ++bj) { f32x4 v0 = acc[ai][bj][m][0], v1 = acc[ai][bj][m][1];
;                         if (kind == 1) {
; #pragma unroll
;                             for (int j = 0; j < 4; ++j) { v0[j] = v0[j] * sigmoid_f(v0[j]); v1[j] = v1[j] * sigmoid_f(v1[j]); } }
;                         else if (kind >= 2) {
; #pragma unroll
;                             for (int j = 0; j < 4; ++j) { v0[j] = sigmoid_f(v0[j]); v1[j] = sigmoid_f(v1[j]); } }
;                         u32x4 w; w.x = cvt_pk_bf16(v0[0], v0[1]); w.y = cvt_pk_bf16(v0[2], v0[3]); w.z = cvt_pk_bf16(v1[0], v1[1]); w.w = cvt_pk_bf16(v1[2], v1[3]);
;                         if (kind >= 1) __builtin_nontemporal_store(w, (u32x4*)(dst + (size_t)row * D + col0 + bj * 128));
;                         else *(u32x4*)(dst + (size_t)row * D + col0 + bj * 128) = w; } }
.LBB0_182:
	v_cvt_pk_bf16_f32 v148, v148, v149
	v_cvt_pk_bf16_f32 v149, v152, v153
	v_cvt_pk_bf16_f32 v150, v150, v151
	v_cvt_pk_bf16_f32 v151, v154, v155
	s_and_b64 vcc, exec, s[12:13]
	s_mov_b64 s[0:1], -1
	global_store_dwordx4 v[146:147], v[148:151], off offset:256 nt
	s_cbranch_vccnz .LBB0_186
	s_and_b64 vcc, exec, s[10:11]
	v_mov_b32_e32 v155, v77
	v_mov_b32_e32 v154, v76
	v_mov_b32_e32 v151, v75
	v_mov_b32_e32 v150, v74
	v_mov_b32_e32 v153, v81
	v_mov_b32_e32 v152, v80
	v_mov_b32_e32 v149, v79
	v_mov_b32_e32 v148, v78
	s_cbranch_vccnz .LBB0_185
	v_mul_f32_e32 v130, 0xbfb8aa3b, v78
	v_exp_f32_e32 v130, v130
	v_mul_f32_e32 v141, 0xbfb8aa3b, v74
	v_exp_f32_e32 v141, v141
	v_mul_f32_e32 v146, 0xbfb8aa3b, v75
	v_add_f32_e32 v130, 1.0, v130
	v_rcp_f32_e32 v148, v130
	v_mul_f32_e32 v130, 0xbfb8aa3b, v79
	v_exp_f32_e32 v130, v130
	v_exp_f32_e32 v146, v146
	v_add_f32_e32 v141, 1.0, v141
	v_rcp_f32_e32 v150, v141
	v_add_f32_e32 v130, 1.0, v130
	v_mul_f32_e32 v141, 0xbfb8aa3b, v80
	v_rcp_f32_e32 v149, v130
	v_add_f32_e32 v130, 1.0, v146
	v_exp_f32_e32 v141, v141
	v_mul_f32_e32 v146, 0xbfb8aa3b, v76
	v_exp_f32_e32 v146, v146
	v_rcp_f32_e32 v151, v130
	v_add_f32_e32 v130, 1.0, v141
	v_mul_f32_e32 v141, 0xbfb8aa3b, v81
	v_rcp_f32_e32 v152, v130
	v_add_f32_e32 v130, 1.0, v146
	v_exp_f32_e32 v141, v141
	v_mul_f32_e32 v146, 0xbfb8aa3b, v77
	v_exp_f32_e32 v146, v146
	v_rcp_f32_e32 v154, v130
	v_add_f32_e32 v130, 1.0, v141
	v_rcp_f32_e32 v153, v130
	v_add_f32_e32 v130, 1.0, v146
	v_rcp_f32_e32 v155, v130

; __device__ __forceinline__ unsigned cvt_pk_bf16(float lo, float hi) { f32x2 v = {lo, hi}; bf16x2_t b = __builtin_convertvector(v, bf16x2_t); return __builtin_bit_cast(unsigned, b); }
; __device__ __forceinline__ float sigmoid_f(float x) { return __builtin_amdgcn_rcpf(1.0f + __expf(-x)); }
;     __device__ __forceinline__ void operator()(const AccT& acc, const pg8::Unit& u, int wr, int wc, int fr, int fq) const {
;     ...
;                     for (int bj = 0; bj < 2; ++bj) { f32x4 v0 = acc[ai][bj][m][0], v1 = acc[ai][bj][m][1];
;                         if (kind == 1) {
; #pragma unroll
;                             for (int j = 0; j < 4; ++j) { v0[j] = v0[j] * sigmoid_f(v0[j]); v1[j] = v1[j] * sigmoid_f(v1[j]); } }
;                         else if (kind >= 2) {
; #pragma unroll
;                             for (int j = 0; j < 4; ++j) { v0[j] = sigmoid_f(v0[j]); v1[j] = sigmoid_f(v1[j]); } }
;                         u32x4 w; w.x = cvt_pk_bf16(v0[0], v0[1]); w.y = cvt_pk_bf16(v0[2], v0[3]); w.z = cvt_pk_bf16(v1[0], v1[1]); w.w = cvt_pk_bf16(v1[2], v1[3]);
;                         if (kind >= 1) __builtin_nontemporal_store(w, (u32x4*)(dst + (size_t)row * D + col0 + bj * 128));
;                         else *(u32x4*)(dst + (size_t)row * D + col0 + bj * 128) = w; } }
.LBB0_188:
	v_or_b32_e32 v146, 48, v142
	v_ashrrev_i32_e32 v147, 31, v146
	v_lshlrev_b64 v[146:147], 12, v[146:147]
	v_lshl_add_u64 v[146:147], v[144:145], 0, v[146:147]
	v_cvt_pk_bf16_f32 v148, v148, v149
	v_cvt_pk_bf16_f32 v149, v152, v153
	v_cvt_pk_bf16_f32 v150, v150, v151
	v_cvt_pk_bf16_f32 v151, v154, v155
	s_and_b64 vcc, exec, s[12:13]
	s_mov_b64 s[0:1], -1
	global_store_dwordx4 v[146:147], v[148:151], off nt
	s_cbranch_vccnz .LBB0_192
	s_and_b64 vcc, exec, s[10:11]
	v_mov_b32_e32 v155, v69
	v_mov_b32_e32 v154, v68
	v_mov_b32_e32 v151, v67
	v_mov_b32_e32 v150, v66
	v_mov_b32_e32 v153, v73
	v_mov_b32_e32 v152, v72
	v_mov_b32_e32 v149, v71
	v_mov_b32_e32 v148, v70
	s_cbranch_vccnz .LBB0_191
	v_mul_f32_e32 v130, 0xbfb8aa3b, v70
	v_exp_f32_e32 v130, v130
	v_mul_f32_e32 v141, 0xbfb8aa3b, v66
	v_exp_f32_e32 v141, v141
	v_mul_f32_e32 v149, 0xbfb8aa3b, v67
	v_add_f32_e32 v130, 1.0, v130
	v_rcp_f32_e32 v148, v130
	v_mul_f32_e32 v130, 0xbfb8aa3b, v71
	v_exp_f32_e32 v130, v130
	v_exp_f32_e32 v151, v149
	v_add_f32_e32 v141, 1.0, v141
	v_rcp_f32_e32 v150, v141
	v_add_f32_e32 v130, 1.0, v130
	v_mul_f32_e32 v141, 0xbfb8aa3b, v72
	v_rcp_f32_e32 v149, v130
	v_add_f32_e32 v130, 1.0, v151
	v_exp_f32_e32 v141, v141
	v_mul_f32_e32 v151, 0xbfb8aa3b, v68
	v_exp_f32_e32 v153, v151
	v_rcp_f32_e32 v151, v130
	v_add_f32_e32 v130, 1.0, v141
	v_mul_f32_e32 v141, 0xbfb8aa3b, v73
	v_rcp_f32_e32 v152, v130
	v_add_f32_e32 v130, 1.0, v153
	v_exp_f32_e32 v141, v141
	v_mul_f32_e32 v153, 0xbfb8aa3b, v69
	v_exp_f32_e32 v155, v153
	v_rcp_f32_e32 v154, v130
	v_add_f32_e32 v130, 1.0, v141
	v_rcp_f32_e32 v153, v130
	v_add_f32_e32 v130, 1.0, v155
	v_rcp_f32_e32 v155, v130

; __device__ __forceinline__ unsigned cvt_pk_bf16(float lo, float hi) { f32x2 v = {lo, hi}; bf16x2_t b = __builtin_convertvector(v, bf16x2_t); return __builtin_bit_cast(unsigned, b); }
; __device__ __forceinline__ float sigmoid_f(float x) { return __builtin_amdgcn_rcpf(1.0f + __expf(-x)); }
;     __device__ __forceinline__ void operator()(const AccT& acc, const pg8::Unit& u, int wr, int wc, int fr, int fq) const {
;     ...
;                     for (int bj = 0; bj < 2; ++bj) { f32x4 v0 = acc[ai][bj][m][0], v1 = acc[ai][bj][m][1];
;                         if (kind == 1) {
; #pragma unroll
;                             for (int j = 0; j < 4; ++j) { v0[j] = v0[j] * sigmoid_f(v0[j]); v1[j] = v1[j] * sigmoid_f(v1[j]); } }
;                         else if (kind >= 2) {
; #pragma unroll
;                             for (int j = 0; j < 4; ++j) { v0[j] = sigmoid_f(v0[j]); v1[j] = sigmoid_f(v1[j]); } }
;                         u32x4 w; w.x = cvt_pk_bf16(v0[0], v0[1]); w.y = cvt_pk_bf16(v0[2], v0[3]); w.z = cvt_pk_bf16(v1[0], v1[1]); w.w = cvt_pk_bf16(v1[2], v1[3]);
;                         if (kind >= 1) __builtin_nontemporal_store(w, (u32x4*)(dst + (size_t)row * D + col0 + bj * 128));
;                         else *(u32x4*)(dst + (size_t)row * D + col0 + bj * 128) = w; } }
.LBB0_194:
	v_cvt_pk_bf16_f32 v148, v148, v149
	v_cvt_pk_bf16_f32 v149, v152, v153
	v_cvt_pk_bf16_f32 v150, v150, v151
	v_cvt_pk_bf16_f32 v151, v154, v155
	s_and_b64 vcc, exec, s[12:13]
	s_mov_b64 s[0:1], -1
	global_store_dwordx4 v[146:147], v[148:151], off offset:256 nt
	s_cbranch_vccnz .LBB0_198
	s_and_b64 vcc, exec, s[10:11]
	v_mov_b32_e32 v155, v61
	v_mov_b32_e32 v154, v60
	v_mov_b32_e32 v151, v59
	v_mov_b32_e32 v150, v58
	v_mov_b32_e32 v153, v65
	v_mov_b32_e32 v152, v64
	v_mov_b32_e32 v149, v63
	v_mov_b32_e32 v148, v62
	s_cbranch_vccnz .LBB0_197
	v_mul_f32_e32 v130, 0xbfb8aa3b, v62
	v_exp_f32_e32 v130, v130
	v_mul_f32_e32 v141, 0xbfb8aa3b, v58
	v_exp_f32_e32 v141, v141
	v_mul_f32_e32 v146, 0xbfb8aa3b, v59
	v_add_f32_e32 v130, 1.0, v130
	v_rcp_f32_e32 v148, v130
	v_mul_f32_e32 v130, 0xbfb8aa3b, v63
	v_exp_f32_e32 v130, v130
	v_exp_f32_e32 v146, v146
	v_add_f32_e32 v141, 1.0, v141
	v_rcp_f32_e32 v150, v141
	v_add_f32_e32 v130, 1.0, v130
	v_mul_f32_e32 v141, 0xbfb8aa3b, v64
	v_rcp_f32_e32 v149, v130
	v_add_f32_e32 v130, 1.0, v146
	v_exp_f32_e32 v141, v141
	v_mul_f32_e32 v146, 0xbfb8aa3b, v60
	v_exp_f32_e32 v146, v146
	v_rcp_f32_e32 v151, v130
	v_add_f32_e32 v130, 1.0, v141
	v_mul_f32_e32 v141, 0xbfb8aa3b, v65
	v_rcp_f32_e32 v152, v130
	v_add_f32_e32 v130, 1.0, v146
	v_exp_f32_e32 v141, v141
	v_mul_f32_e32 v146, 0xbfb8aa3b, v61
	v_exp_f32_e32 v146, v146
	v_rcp_f32_e32 v154, v130
	v_add_f32_e32 v130, 1.0, v141
	v_rcp_f32_e32 v153, v130
	v_add_f32_e32 v130, 1.0, v146
	v_rcp_f32_e32 v155, v130

; __device__ __forceinline__ unsigned cvt_pk_bf16(float lo, float hi) { f32x2 v = {lo, hi}; bf16x2_t b = __builtin_convertvector(v, bf16x2_t); return __builtin_bit_cast(unsigned, b); }
; __device__ __forceinline__ float sigmoid_f(float x) { return __builtin_amdgcn_rcpf(1.0f + __expf(-x)); }
;     __device__ __forceinline__ void operator()(const AccT& acc, const pg8::Unit& u, int wr, int wc, int fr, int fq) const {
;     ...
;                     for (int bj = 0; bj < 2; ++bj) { f32x4 v0 = acc[ai][bj][m][0], v1 = acc[ai][bj][m][1];
;                         if (kind == 1) {
; #pragma unroll
;                             for (int j = 0; j < 4; ++j) { v0[j] = v0[j] * sigmoid_f(v0[j]); v1[j] = v1[j] * sigmoid_f(v1[j]); } }
;                         else if (kind >= 2) {
; #pragma unroll
;                             for (int j = 0; j < 4; ++j) { v0[j] = sigmoid_f(v0[j]); v1[j] = sigmoid_f(v1[j]); } }
;                         u32x4 w; w.x = cvt_pk_bf16(v0[0], v0[1]); w.y = cvt_pk_bf16(v0[2], v0[3]); w.z = cvt_pk_bf16(v1[0], v1[1]); w.w = cvt_pk_bf16(v1[2], v1[3]);
;                         if (kind >= 1) __builtin_nontemporal_store(w, (u32x4*)(dst + (size_t)row * D + col0 + bj * 128));
;                         else *(u32x4*)(dst + (size_t)row * D + col0 + bj * 128) = w; } }
.LBB0_200:
	v_lshlrev_b64 v[146:147], 12, v[142:143]
	v_lshl_add_u64 v[146:147], v[144:145], 0, v[146:147]
	v_cvt_pk_bf16_f32 v148, v148, v149
	v_cvt_pk_bf16_f32 v149, v152, v153
	v_add_co_u32_e32 v152, vcc, 0x80000, v146
	v_cvt_pk_bf16_f32 v150, v150, v151
	s_nop 0
	v_addc_co_u32_e32 v153, vcc, 0, v147, vcc
	v_cvt_pk_bf16_f32 v151, v154, v155
	s_and_b64 vcc, exec, s[12:13]
	s_mov_b64 s[0:1], -1
	global_store_dwordx4 v[152:153], v[148:151], off nt
	s_cbranch_vccnz .LBB0_204
	s_and_b64 vcc, exec, s[10:11]
	v_mov_b32_e32 v155, v53
	v_mov_b32_e32 v154, v52
	v_mov_b32_e32 v151, v51
	v_mov_b32_e32 v150, v50
	v_mov_b32_e32 v153, v57
	v_mov_b32_e32 v152, v56
	v_mov_b32_e32 v149, v55
	v_mov_b32_e32 v148, v54
	s_cbranch_vccnz .LBB0_203
	v_mul_f32_e32 v130, 0xbfb8aa3b, v54
	v_exp_f32_e32 v130, v130
	v_mul_f32_e32 v141, 0xbfb8aa3b, v50
	v_exp_f32_e32 v141, v141
	v_mul_f32_e32 v149, 0xbfb8aa3b, v51
	v_add_f32_e32 v130, 1.0, v130
	v_rcp_f32_e32 v148, v130
	v_mul_f32_e32 v130, 0xbfb8aa3b, v55
	v_exp_f32_e32 v130, v130
	v_exp_f32_e32 v151, v149
	v_add_f32_e32 v141, 1.0, v141
	v_rcp_f32_e32 v150, v141
	v_add_f32_e32 v130, 1.0, v130
	v_mul_f32_e32 v141, 0xbfb8aa3b, v56
	v_rcp_f32_e32 v149, v130
	v_add_f32_e32 v130, 1.0, v151
	v_exp_f32_e32 v141, v141
	v_mul_f32_e32 v151, 0xbfb8aa3b, v52
	v_exp_f32_e32 v153, v151
	v_rcp_f32_e32 v151, v130
	v_add_f32_e32 v130, 1.0, v141
	v_mul_f32_e32 v141, 0xbfb8aa3b, v57
	v_rcp_f32_e32 v152, v130
	v_add_f32_e32 v130, 1.0, v153
	v_exp_f32_e32 v141, v141
	v_mul_f32_e32 v153, 0xbfb8aa3b, v53
	v_exp_f32_e32 v155, v153
	v_rcp_f32_e32 v154, v130
	v_add_f32_e32 v130, 1.0, v141
	v_rcp_f32_e32 v153, v130
	v_add_f32_e32 v130, 1.0, v155
	v_rcp_f32_e32 v155, v130

; __device__ __forceinline__ unsigned cvt_pk_bf16(float lo, float hi) { f32x2 v = {lo, hi}; bf16x2_t b = __builtin_convertvector(v, bf16x2_t); return __builtin_bit_cast(unsigned, b); }
; __device__ __forceinline__ float sigmoid_f(float x) { return __builtin_amdgcn_rcpf(1.0f + __expf(-x)); }
;     __device__ __forceinline__ void operator()(const AccT& acc, const pg8::Unit& u, int wr, int wc, int fr, int fq) const {
;     ...
;                     for (int bj = 0; bj < 2; ++bj) { f32x4 v0 = acc[ai][bj][m][0], v1 = acc[ai][bj][m][1];
;                         if (kind == 1) {
; #pragma unroll
;                             for (int j = 0; j < 4; ++j) { v0[j] = v0[j] * sigmoid_f(v0[j]); v1[j] = v1[j] * sigmoid_f(v1[j]); } }
;                         else if (kind >= 2) {
; #pragma unroll
;                             for (int j = 0; j < 4; ++j) { v0[j] = sigmoid_f(v0[j]); v1[j] = sigmoid_f(v1[j]); } }
;                         u32x4 w; w.x = cvt_pk_bf16(v0[0], v0[1]); w.y = cvt_pk_bf16(v0[2], v0[3]); w.z = cvt_pk_bf16(v1[0], v1[1]); w.w = cvt_pk_bf16(v1[2], v1[3]);
;                         if (kind >= 1) __builtin_nontemporal_store(w, (u32x4*)(dst + (size_t)row * D + col0 + bj * 128));
;                         else *(u32x4*)(dst + (size_t)row * D + col0 + bj * 128) = w; } }
.LBB0_206:
	v_lshl_add_u64 v[170:171], v[146:147], 0, s[16:17]
	v_cvt_pk_bf16_f32 v146, v148, v149
	v_cvt_pk_bf16_f32 v147, v152, v153
	v_cvt_pk_bf16_f32 v148, v150, v151
	v_cvt_pk_bf16_f32 v149, v154, v155
	s_and_b64 vcc, exec, s[12:13]
	s_mov_b64 s[0:1], -1
	global_store_dwordx4 v[170:171], v[146:149], off offset:256 nt
	s_cbranch_vccnz .LBB0_210
	s_and_b64 vcc, exec, s[10:11]
	v_mov_b32_e32 v155, v45
	v_mov_b32_e32 v154, v44
	v_mov_b32_e32 v151, v43
	v_mov_b32_e32 v150, v42
	v_mov_b32_e32 v153, v49
	v_mov_b32_e32 v152, v48
	v_mov_b32_e32 v149, v47
	v_mov_b32_e32 v148, v46
	s_cbranch_vccnz .LBB0_209
	v_mul_f32_e32 v130, 0xbfb8aa3b, v46
	v_exp_f32_e32 v130, v130
	v_mul_f32_e32 v141, 0xbfb8aa3b, v42
	v_exp_f32_e32 v141, v141
	v_mul_f32_e32 v146, 0xbfb8aa3b, v43
	v_add_f32_e32 v130, 1.0, v130
	v_rcp_f32_e32 v148, v130
	v_mul_f32_e32 v130, 0xbfb8aa3b, v47
	v_exp_f32_e32 v130, v130
	v_exp_f32_e32 v146, v146
	v_add_f32_e32 v141, 1.0, v141
	v_rcp_f32_e32 v150, v141
	v_add_f32_e32 v130, 1.0, v130
	v_mul_f32_e32 v141, 0xbfb8aa3b, v48
	v_rcp_f32_e32 v149, v130
	v_add_f32_e32 v130, 1.0, v146
	v_exp_f32_e32 v141, v141
	v_mul_f32_e32 v146, 0xbfb8aa3b, v44
	v_exp_f32_e32 v146, v146
	v_rcp_f32_e32 v151, v130
	v_add_f32_e32 v130, 1.0, v141
	v_mul_f32_e32 v141, 0xbfb8aa3b, v49
	v_rcp_f32_e32 v152, v130
	v_add_f32_e32 v130, 1.0, v146
	v_exp_f32_e32 v141, v141
	v_mul_f32_e32 v146, 0xbfb8aa3b, v45
	v_exp_f32_e32 v146, v146
	v_rcp_f32_e32 v154, v130
	v_add_f32_e32 v130, 1.0, v141
	v_rcp_f32_e32 v153, v130
	v_add_f32_e32 v130, 1.0, v146
	v_rcp_f32_e32 v155, v130

; __device__ __forceinline__ unsigned cvt_pk_bf16(float lo, float hi) { f32x2 v = {lo, hi}; bf16x2_t b = __builtin_convertvector(v, bf16x2_t); return __builtin_bit_cast(unsigned, b); }
; __device__ __forceinline__ float sigmoid_f(float x) { return __builtin_amdgcn_rcpf(1.0f + __expf(-x)); }
;     __device__ __forceinline__ void operator()(const AccT& acc, const pg8::Unit& u, int wr, int wc, int fr, int fq) const {
;     ...
;                     for (int bj = 0; bj < 2; ++bj) { f32x4 v0 = acc[ai][bj][m][0], v1 = acc[ai][bj][m][1];
;                         if (kind == 1) {
; #pragma unroll
;                             for (int j = 0; j < 4; ++j) { v0[j] = v0[j] * sigmoid_f(v0[j]); v1[j] = v1[j] * sigmoid_f(v1[j]); } }
;                         else if (kind >= 2) {
; #pragma unroll
;                             for (int j = 0; j < 4; ++j) { v0[j] = sigmoid_f(v0[j]); v1[j] = sigmoid_f(v1[j]); } }
;                         u32x4 w; w.x = cvt_pk_bf16(v0[0], v0[1]); w.y = cvt_pk_bf16(v0[2], v0[3]); w.z = cvt_pk_bf16(v1[0], v1[1]); w.w = cvt_pk_bf16(v1[2], v1[3]);
;                         if (kind >= 1) __builtin_nontemporal_store(w, (u32x4*)(dst + (size_t)row * D + col0 + bj * 128));
;                         else *(u32x4*)(dst + (size_t)row * D + col0 + bj * 128) = w; } }
.LBB0_212:
	v_lshlrev_b64 v[146:147], 12, v[142:143]
	v_lshl_add_u64 v[146:147], v[144:145], 0, v[146:147]
	v_cvt_pk_bf16_f32 v148, v148, v149
	v_cvt_pk_bf16_f32 v149, v152, v153
	v_add_co_u32_e32 v152, vcc, 0x90000, v146
	v_cvt_pk_bf16_f32 v150, v150, v151
	s_nop 0
	v_addc_co_u32_e32 v153, vcc, 0, v147, vcc
	v_cvt_pk_bf16_f32 v151, v154, v155
	s_and_b64 vcc, exec, s[12:13]
	s_mov_b64 s[0:1], -1
	global_store_dwordx4 v[152:153], v[148:151], off nt
	s_cbranch_vccnz .LBB0_216
	s_and_b64 vcc, exec, s[10:11]
	v_mov_b32_e32 v155, v37
	v_mov_b32_e32 v154, v36
	v_mov_b32_e32 v151, v35
	v_mov_b32_e32 v150, v34
	v_mov_b32_e32 v153, v41
	v_mov_b32_e32 v152, v40
	v_mov_b32_e32 v149, v39
	v_mov_b32_e32 v148, v38
	s_cbranch_vccnz .LBB0_215
	v_mul_f32_e32 v130, 0xbfb8aa3b, v38
	v_exp_f32_e32 v130, v130
	v_mul_f32_e32 v141, 0xbfb8aa3b, v34
	v_exp_f32_e32 v141, v141
	v_mul_f32_e32 v149, 0xbfb8aa3b, v35
	v_add_f32_e32 v130, 1.0, v130
	v_rcp_f32_e32 v148, v130
	v_mul_f32_e32 v130, 0xbfb8aa3b, v39
	v_exp_f32_e32 v130, v130
	v_exp_f32_e32 v151, v149
	v_add_f32_e32 v141, 1.0, v141
	v_rcp_f32_e32 v150, v141
	v_add_f32_e32 v130, 1.0, v130
	v_mul_f32_e32 v141, 0xbfb8aa3b, v40
	v_rcp_f32_e32 v149, v130
	v_add_f32_e32 v130, 1.0, v151
	v_exp_f32_e32 v141, v141
	v_mul_f32_e32 v151, 0xbfb8aa3b, v36
	v_exp_f32_e32 v153, v151
	v_rcp_f32_e32 v151, v130
	v_add_f32_e32 v130, 1.0, v141
	v_mul_f32_e32 v141, 0xbfb8aa3b, v41
	v_rcp_f32_e32 v152, v130
	v_add_f32_e32 v130, 1.0, v153
	v_exp_f32_e32 v141, v141
	v_mul_f32_e32 v153, 0xbfb8aa3b, v37
	v_exp_f32_e32 v155, v153
	v_rcp_f32_e32 v154, v130
	v_add_f32_e32 v130, 1.0, v141
	v_rcp_f32_e32 v153, v130
	v_add_f32_e32 v130, 1.0, v155
	v_rcp_f32_e32 v155, v130

; __device__ __forceinline__ unsigned cvt_pk_bf16(float lo, float hi) { f32x2 v = {lo, hi}; bf16x2_t b = __builtin_convertvector(v, bf16x2_t); return __builtin_bit_cast(unsigned, b); }
; __device__ __forceinline__ float sigmoid_f(float x) { return __builtin_amdgcn_rcpf(1.0f + __expf(-x)); }
;     __device__ __forceinline__ void operator()(const AccT& acc, const pg8::Unit& u, int wr, int wc, int fr, int fq) const {
;     ...
;                     for (int bj = 0; bj < 2; ++bj) { f32x4 v0 = acc[ai][bj][m][0], v1 = acc[ai][bj][m][1];
;                         if (kind == 1) {
; #pragma unroll
;                             for (int j = 0; j < 4; ++j) { v0[j] = v0[j] * sigmoid_f(v0[j]); v1[j] = v1[j] * sigmoid_f(v1[j]); } }
;                         else if (kind >= 2) {
; #pragma unroll
;                             for (int j = 0; j < 4; ++j) { v0[j] = sigmoid_f(v0[j]); v1[j] = sigmoid_f(v1[j]); } }
;                         u32x4 w; w.x = cvt_pk_bf16(v0[0], v0[1]); w.y = cvt_pk_bf16(v0[2], v0[3]); w.z = cvt_pk_bf16(v1[0], v1[1]); w.w = cvt_pk_bf16(v1[2], v1[3]);
;                         if (kind >= 1) __builtin_nontemporal_store(w, (u32x4*)(dst + (size_t)row * D + col0 + bj * 128));
;                         else *(u32x4*)(dst + (size_t)row * D + col0 + bj * 128) = w; } }
.LBB0_218:
	v_lshl_add_u64 v[170:171], v[146:147], 0, s[22:23]
	v_cvt_pk_bf16_f32 v146, v148, v149
	v_cvt_pk_bf16_f32 v147, v152, v153
	v_cvt_pk_bf16_f32 v148, v150, v151
	v_cvt_pk_bf16_f32 v149, v154, v155
	s_and_b64 vcc, exec, s[12:13]
	s_mov_b64 s[0:1], -1
	global_store_dwordx4 v[170:171], v[146:149], off offset:256 nt
	s_cbranch_vccnz .LBB0_222
	s_and_b64 vcc, exec, s[10:11]
	v_mov_b32_e32 v155, v29
	v_mov_b32_e32 v154, v28
	v_mov_b32_e32 v151, v27
	v_mov_b32_e32 v150, v26
	v_mov_b32_e32 v153, v33
	v_mov_b32_e32 v152, v32
	v_mov_b32_e32 v149, v31
	v_mov_b32_e32 v148, v30
	s_cbranch_vccnz .LBB0_221
	v_mul_f32_e32 v130, 0xbfb8aa3b, v30
	v_exp_f32_e32 v130, v130
	v_mul_f32_e32 v141, 0xbfb8aa3b, v26
	v_exp_f32_e32 v141, v141
	v_mul_f32_e32 v146, 0xbfb8aa3b, v27
	v_add_f32_e32 v130, 1.0, v130
	v_rcp_f32_e32 v148, v130
	v_mul_f32_e32 v130, 0xbfb8aa3b, v31
	v_exp_f32_e32 v130, v130
	v_exp_f32_e32 v146, v146
	v_add_f32_e32 v141, 1.0, v141
	v_rcp_f32_e32 v150, v141
	v_add_f32_e32 v130, 1.0, v130
	v_mul_f32_e32 v141, 0xbfb8aa3b, v32
	v_rcp_f32_e32 v149, v130
	v_add_f32_e32 v130, 1.0, v146
	v_exp_f32_e32 v141, v141
	v_mul_f32_e32 v146, 0xbfb8aa3b, v28
	v_exp_f32_e32 v146, v146
	v_rcp_f32_e32 v151, v130
	v_add_f32_e32 v130, 1.0, v141
	v_mul_f32_e32 v141, 0xbfb8aa3b, v33
	v_rcp_f32_e32 v152, v130
	v_add_f32_e32 v130, 1.0, v146
	v_exp_f32_e32 v141, v141
	v_mul_f32_e32 v146, 0xbfb8aa3b, v29
	v_exp_f32_e32 v146, v146
	v_rcp_f32_e32 v154, v130
	v_add_f32_e32 v130, 1.0, v141
	v_rcp_f32_e32 v153, v130
	v_add_f32_e32 v130, 1.0, v146
	v_rcp_f32_e32 v155, v130

; __device__ __forceinline__ unsigned cvt_pk_bf16(float lo, float hi) { f32x2 v = {lo, hi}; bf16x2_t b = __builtin_convertvector(v, bf16x2_t); return __builtin_bit_cast(unsigned, b); }
; __device__ __forceinline__ float sigmoid_f(float x) { return __builtin_amdgcn_rcpf(1.0f + __expf(-x)); }
;     __device__ __forceinline__ void operator()(const AccT& acc, const pg8::Unit& u, int wr, int wc, int fr, int fq) const {
;     ...
;                     for (int bj = 0; bj < 2; ++bj) { f32x4 v0 = acc[ai][bj][m][0], v1 = acc[ai][bj][m][1];
;                         if (kind == 1) {
; #pragma unroll
;                             for (int j = 0; j < 4; ++j) { v0[j] = v0[j] * sigmoid_f(v0[j]); v1[j] = v1[j] * sigmoid_f(v1[j]); } }
;                         else if (kind >= 2) {
; #pragma unroll
;                             for (int j = 0; j < 4; ++j) { v0[j] = sigmoid_f(v0[j]); v1[j] = sigmoid_f(v1[j]); } }
;                         u32x4 w; w.x = cvt_pk_bf16(v0[0], v0[1]); w.y = cvt_pk_bf16(v0[2], v0[3]); w.z = cvt_pk_bf16(v1[0], v1[1]); w.w = cvt_pk_bf16(v1[2], v1[3]);
;                         if (kind >= 1) __builtin_nontemporal_store(w, (u32x4*)(dst + (size_t)row * D + col0 + bj * 128));
;                         else *(u32x4*)(dst + (size_t)row * D + col0 + bj * 128) = w; } }
.LBB0_224:
	v_lshlrev_b64 v[146:147], 12, v[142:143]
	v_lshl_add_u64 v[146:147], v[144:145], 0, v[146:147]
	v_cvt_pk_bf16_f32 v148, v148, v149
	v_cvt_pk_bf16_f32 v149, v152, v153
	v_add_co_u32_e32 v152, vcc, 0xa0000, v146
	v_cvt_pk_bf16_f32 v150, v150, v151
	s_nop 0
	v_addc_co_u32_e32 v153, vcc, 0, v147, vcc
	v_cvt_pk_bf16_f32 v151, v154, v155
	s_and_b64 vcc, exec, s[12:13]
	s_mov_b64 s[0:1], -1
	global_store_dwordx4 v[152:153], v[148:151], off nt
	s_cbranch_vccnz .LBB0_228
	s_and_b64 vcc, exec, s[10:11]
	v_mov_b32_e32 v155, v21
	v_mov_b32_e32 v154, v20
	v_mov_b32_e32 v151, v19
	v_mov_b32_e32 v150, v18
	v_mov_b32_e32 v153, v25
	v_mov_b32_e32 v152, v24
	v_mov_b32_e32 v149, v23
	v_mov_b32_e32 v148, v22
	s_cbranch_vccnz .LBB0_227
	v_mul_f32_e32 v130, 0xbfb8aa3b, v22
	v_exp_f32_e32 v130, v130
	v_mul_f32_e32 v141, 0xbfb8aa3b, v18
	v_exp_f32_e32 v141, v141
	v_mul_f32_e32 v149, 0xbfb8aa3b, v19
	v_add_f32_e32 v130, 1.0, v130
	v_rcp_f32_e32 v148, v130
	v_mul_f32_e32 v130, 0xbfb8aa3b, v23
	v_exp_f32_e32 v130, v130
	v_exp_f32_e32 v151, v149
	v_add_f32_e32 v141, 1.0, v141
	v_rcp_f32_e32 v150, v141
	v_add_f32_e32 v130, 1.0, v130
	v_mul_f32_e32 v141, 0xbfb8aa3b, v24
	v_rcp_f32_e32 v149, v130
	v_add_f32_e32 v130, 1.0, v151
	v_exp_f32_e32 v141, v141
	v_mul_f32_e32 v151, 0xbfb8aa3b, v20
	v_exp_f32_e32 v153, v151
	v_rcp_f32_e32 v151, v130
	v_add_f32_e32 v130, 1.0, v141
	v_mul_f32_e32 v141, 0xbfb8aa3b, v25
	v_rcp_f32_e32 v152, v130
	v_add_f32_e32 v130, 1.0, v153
	v_exp_f32_e32 v141, v141
	v_mul_f32_e32 v153, 0xbfb8aa3b, v21
	v_exp_f32_e32 v155, v153
	v_rcp_f32_e32 v154, v130
	v_add_f32_e32 v130, 1.0, v141
	v_rcp_f32_e32 v153, v130
	v_add_f32_e32 v130, 1.0, v155
	v_rcp_f32_e32 v155, v130

; __device__ __forceinline__ unsigned cvt_pk_bf16(float lo, float hi) { f32x2 v = {lo, hi}; bf16x2_t b = __builtin_convertvector(v, bf16x2_t); return __builtin_bit_cast(unsigned, b); }
; __device__ __forceinline__ float sigmoid_f(float x) { return __builtin_amdgcn_rcpf(1.0f + __expf(-x)); }
;     __device__ __forceinline__ void operator()(const AccT& acc, const pg8::Unit& u, int wr, int wc, int fr, int fq) const {
;     ...
;                     for (int bj = 0; bj < 2; ++bj) { f32x4 v0 = acc[ai][bj][m][0], v1 = acc[ai][bj][m][1];
;                         if (kind == 1) {
; #pragma unroll
;                             for (int j = 0; j < 4; ++j) { v0[j] = v0[j] * sigmoid_f(v0[j]); v1[j] = v1[j] * sigmoid_f(v1[j]); } }
;                         else if (kind >= 2) {
; #pragma unroll
;                             for (int j = 0; j < 4; ++j) { v0[j] = sigmoid_f(v0[j]); v1[j] = sigmoid_f(v1[j]); } }
;                         u32x4 w; w.x = cvt_pk_bf16(v0[0], v0[1]); w.y = cvt_pk_bf16(v0[2], v0[3]); w.z = cvt_pk_bf16(v1[0], v1[1]); w.w = cvt_pk_bf16(v1[2], v1[3]);
;                         if (kind >= 1) __builtin_nontemporal_store(w, (u32x4*)(dst + (size_t)row * D + col0 + bj * 128));
;                         else *(u32x4*)(dst + (size_t)row * D + col0 + bj * 128) = w; } }
.LBB0_230:
	v_lshl_add_u64 v[170:171], v[146:147], 0, s[24:25]
	v_cvt_pk_bf16_f32 v146, v148, v149
	v_cvt_pk_bf16_f32 v147, v152, v153
	v_cvt_pk_bf16_f32 v148, v150, v151
	v_cvt_pk_bf16_f32 v149, v154, v155
	s_and_b64 vcc, exec, s[12:13]
	s_mov_b64 s[0:1], -1
	global_store_dwordx4 v[170:171], v[146:149], off offset:256 nt
	s_cbranch_vccnz .LBB0_234
	s_and_b64 vcc, exec, s[10:11]
	v_mov_b32_e32 v153, v13
	v_mov_b32_e32 v152, v12
	v_mov_b32_e32 v149, v11
	v_mov_b32_e32 v148, v10
	v_mov_b32_e32 v151, v17
	v_mov_b32_e32 v150, v16
	v_mov_b32_e32 v147, v15
	v_mov_b32_e32 v146, v14
	s_cbranch_vccnz .LBB0_233
	v_mul_f32_e32 v130, 0xbfb8aa3b, v14
	v_exp_f32_e32 v130, v130
	v_mul_f32_e32 v141, 0xbfb8aa3b, v10
	v_exp_f32_e32 v141, v141
	v_mul_f32_e32 v147, 0xbfb8aa3b, v11
	v_add_f32_e32 v130, 1.0, v130
	v_rcp_f32_e32 v146, v130
	v_mul_f32_e32 v130, 0xbfb8aa3b, v15
	v_exp_f32_e32 v130, v130
	v_exp_f32_e32 v149, v147
	v_add_f32_e32 v141, 1.0, v141
	v_rcp_f32_e32 v148, v141
	v_add_f32_e32 v130, 1.0, v130
	v_mul_f32_e32 v141, 0xbfb8aa3b, v16
	v_rcp_f32_e32 v147, v130
	v_add_f32_e32 v130, 1.0, v149
	v_exp_f32_e32 v141, v141
	v_mul_f32_e32 v149, 0xbfb8aa3b, v12
	v_exp_f32_e32 v151, v149
	v_rcp_f32_e32 v149, v130
	v_add_f32_e32 v130, 1.0, v141
	v_mul_f32_e32 v141, 0xbfb8aa3b, v17
	v_rcp_f32_e32 v150, v130
	v_add_f32_e32 v130, 1.0, v151
	v_exp_f32_e32 v141, v141
	v_mul_f32_e32 v151, 0xbfb8aa3b, v13
	v_exp_f32_e32 v153, v151
	v_rcp_f32_e32 v152, v130
	v_add_f32_e32 v130, 1.0, v141
	v_rcp_f32_e32 v151, v130
	v_add_f32_e32 v130, 1.0, v153
	v_rcp_f32_e32 v153, v130

; __device__ __forceinline__ unsigned cvt_pk_bf16(float lo, float hi) { f32x2 v = {lo, hi}; bf16x2_t b = __builtin_convertvector(v, bf16x2_t); return __builtin_bit_cast(unsigned, b); }
; __device__ __forceinline__ float sigmoid_f(float x) { return __builtin_amdgcn_rcpf(1.0f + __expf(-x)); }
;     __device__ __forceinline__ void operator()(const AccT& acc, const pg8::Unit& u, int wr, int wc, int fr, int fq) const {
;     ...
;                     for (int bj = 0; bj < 2; ++bj) { f32x4 v0 = acc[ai][bj][m][0], v1 = acc[ai][bj][m][1];
;                         if (kind == 1) {
; #pragma unroll
;                             for (int j = 0; j < 4; ++j) { v0[j] = v0[j] * sigmoid_f(v0[j]); v1[j] = v1[j] * sigmoid_f(v1[j]); } }
;                         else if (kind >= 2) {
; #pragma unroll
;                             for (int j = 0; j < 4; ++j) { v0[j] = sigmoid_f(v0[j]); v1[j] = sigmoid_f(v1[j]); } }
;                         u32x4 w; w.x = cvt_pk_bf16(v0[0], v0[1]); w.y = cvt_pk_bf16(v0[2], v0[3]); w.z = cvt_pk_bf16(v1[0], v1[1]); w.w = cvt_pk_bf16(v1[2], v1[3]);
;                         if (kind >= 1) __builtin_nontemporal_store(w, (u32x4*)(dst + (size_t)row * D + col0 + bj * 128));
;                         else *(u32x4*)(dst + (size_t)row * D + col0 + bj * 128) = w; } }
.LBB0_236:
	v_lshlrev_b64 v[154:155], 12, v[142:143]
	v_lshl_add_u64 v[144:145], v[144:145], 0, v[154:155]
	v_cvt_pk_bf16_f32 v146, v146, v147
	v_cvt_pk_bf16_f32 v147, v150, v151
	v_add_co_u32_e32 v150, vcc, 0xb0000, v144
	v_cvt_pk_bf16_f32 v148, v148, v149
	s_nop 0
	v_addc_co_u32_e32 v151, vcc, 0, v145, vcc
	v_cvt_pk_bf16_f32 v149, v152, v153
	s_and_b64 vcc, exec, s[12:13]
	s_mov_b64 s[0:1], -1
	global_store_dwordx4 v[150:151], v[146:149], off nt
	s_cbranch_vccnz .LBB0_240
	s_and_b64 vcc, exec, s[10:11]
	v_mov_b32_e32 v153, v5
	v_mov_b32_e32 v152, v4
	v_mov_b32_e32 v149, v3
	v_mov_b32_e32 v148, v2
	v_mov_b32_e32 v151, v9
	v_mov_b32_e32 v150, v8
	v_mov_b32_e32 v147, v7
	v_mov_b32_e32 v146, v6
	s_cbranch_vccnz .LBB0_239
	v_mul_f32_e32 v130, 0xbfb8aa3b, v6
	v_exp_f32_e32 v130, v130
	v_mul_f32_e32 v141, 0xbfb8aa3b, v2
	v_exp_f32_e32 v141, v141
	v_mul_f32_e32 v143, 0xbfb8aa3b, v3
	v_add_f32_e32 v130, 1.0, v130
	v_rcp_f32_e32 v146, v130
	v_mul_f32_e32 v130, 0xbfb8aa3b, v7
	v_exp_f32_e32 v130, v130
	v_exp_f32_e32 v143, v143
	v_add_f32_e32 v141, 1.0, v141
	v_rcp_f32_e32 v148, v141
	v_add_f32_e32 v130, 1.0, v130
	v_mul_f32_e32 v141, 0xbfb8aa3b, v8
	v_rcp_f32_e32 v147, v130
	v_add_f32_e32 v130, 1.0, v143
	v_exp_f32_e32 v141, v141
	v_mul_f32_e32 v143, 0xbfb8aa3b, v4
	v_exp_f32_e32 v143, v143
	v_rcp_f32_e32 v149, v130
	v_add_f32_e32 v130, 1.0, v141
	v_mul_f32_e32 v141, 0xbfb8aa3b, v9
	v_rcp_f32_e32 v150, v130
	v_add_f32_e32 v130, 1.0, v143
	v_exp_f32_e32 v141, v141
	v_mul_f32_e32 v143, 0xbfb8aa3b, v5
	v_exp_f32_e32 v143, v143
	v_rcp_f32_e32 v152, v130
	v_add_f32_e32 v130, 1.0, v141
	v_rcp_f32_e32 v151, v130
	v_add_f32_e32 v130, 1.0, v143
	v_rcp_f32_e32 v153, v130

; __device__ __forceinline__ unsigned cvt_pk_bf16(float lo, float hi) { f32x2 v = {lo, hi}; bf16x2_t b = __builtin_convertvector(v, bf16x2_t); return __builtin_bit_cast(unsigned, b); }
;     __device__ __forceinline__ void operator()(const AccT& acc, const pg8::Unit& u, int wr, int wc, int fr, int fq) const {
;     ...
;             bf16_t* dst = (bf16_t*)(ws + (pn < 12 ? WS_Q : WS_K)); const float sc = pn < 12 ? 1.0f : 0.08838834764831845f;
;             const float* rc = (const float*)(ws + WS_ROPEC); const float* rs = (const float*)(ws + WS_ROPES);
;             const int dd = 16 * wc + 4 * fq;
; #pragma unroll
;             for (int ai = 0; ai < 2; ++ai) {
;                 f32x4 cc[4], ss[4];
; #pragma unroll
;                 for (int m = 0; m < 4; ++m) { const int row = row0 + ai * 128 + m * 16; cc[m] = *(const f32x4*)(rc + (size_t)row * 64 + dd); ss[m] = *(const f32x4*)(rs + (size_t)row * 64 + dd); }
; #pragma unroll
;                 for (int m = 0; m < 4; ++m) { const int row = row0 + ai * 128 + m * 16;
;                     const f32x4 c = cc[m] * sc, s = ss[m] * sc;
; #pragma unroll
;                     for (int bj = 0; bj < 2; ++bj) { const f32x4 t1 = acc[ai][bj][m][0], t2 = acc[ai][bj][m][1];
;                         const f32x4 o1 = t1 * c - t2 * s, o2 = t2 * c + t1 * s;
;                         bf16_t* p = dst + (size_t)row * QKW + (pn & 3) * 256 + bj * 128 + dd;
;                         u32x2 w1, w2; w1.x = cvt_pk_bf16(o1[0], o1[1]); w1.y = cvt_pk_bf16(o1[2], o1[3]); w2.x = cvt_pk_bf16(o2[0], o2[1]); w2.y = cvt_pk_bf16(o2[2], o2[3]);
;                         if (pn < 12) { __builtin_nontemporal_store(w1, (u32x2*)p); __builtin_nontemporal_store(w2, (u32x2*)(p + 64)); }
;                         else { *(u32x2*)p = w1; *(u32x2*)(p + 64) = w2; } } } }
;     ...
;                         u32x4 w; w.x = cvt_pk_bf16(v0[0], v0[1]); w.y = cvt_pk_bf16(v0[2], v0[3]); w.z = cvt_pk_bf16(v1[0], v1[1]); w.w = cvt_pk_bf16(v1[2], v1[3]);
;                         if (kind >= 1) __builtin_nontemporal_store(w, (u32x4*)(dst + (size_t)row * D + col0 + bj * 128));
;                         else *(u32x4*)(dst + (size_t)row * D + col0 + bj * 128) = w; } }
.LBB0_242:
	v_lshl_add_u64 v[154:155], v[144:145], 0, s[26:27]
	v_cvt_pk_bf16_f32 v144, v146, v147
	v_cvt_pk_bf16_f32 v145, v150, v151
	v_cvt_pk_bf16_f32 v146, v148, v149
	v_cvt_pk_bf16_f32 v147, v152, v153
	global_store_dwordx4 v[154:155], v[144:147], off offset:256 nt
	s_mov_b64 s[0:1], 0
.LBB0_243:
	s_and_b64 vcc, exec, s[0:1]
	s_cbranch_vccz .LBB0_245
	v_ashrrev_i32_e32 v143, 31, v142
	v_lshlrev_b64 v[144:145], 8, v[142:143]
	v_lshl_add_u64 v[146:147], v[132:133], 0, v[144:145]
	v_lshl_add_u64 v[144:145], v[134:135], 0, v[144:145]
	global_load_dwordx4 v[146:149], v[146:147], off
	v_or_b32_e32 v194, 48, v142
	global_load_dwordx4 v[150:153], v[144:145], off
	v_or_b32_e32 v144, 16, v142
	v_ashrrev_i32_e32 v145, 31, v144
	v_lshlrev_b64 v[154:155], 8, v[144:145]
	v_lshl_add_u64 v[170:171], v[132:133], 0, v[154:155]
	v_lshl_add_u64 v[154:155], v[134:135], 0, v[154:155]
	global_load_dwordx4 v[174:177], v[154:155], off
	v_or_b32_e32 v154, 32, v142
	global_load_dwordx4 v[170:173], v[170:171], off
	v_ashrrev_i32_e32 v155, 31, v154
	v_lshlrev_b64 v[182:183], 8, v[154:155]
	v_lshlrev_b64 v[198:199], 11, v[144:145]
	v_lshl_add_u64 v[144:145], v[132:133], 0, v[182:183]
	global_load_dwordx4 v[178:181], v[144:145], off
	v_lshl_add_u64 v[144:145], v[134:135], 0, v[182:183]
	global_load_dwordx4 v[182:185], v[144:145], off
	v_ashrrev_i32_e32 v195, 31, v194
	v_lshlrev_b64 v[186:187], 8, v[194:195]
	v_lshl_add_u64 v[144:145], v[132:133], 0, v[186:187]
	v_lshl_add_u64 v[190:191], v[134:135], 0, v[186:187]
	global_load_dwordx4 v[186:189], v[144:145], off
	s_nop 0
	global_load_dwordx4 v[190:193], v[190:191], off
	s_cmp_lt_u32 s52, 12
	s_cselect_b64 s[0:1], -1, 0
	v_cndmask_b32_e64 v130, v168, 1.0, s[0:1]
	s_and_b64 s[0:1], s[0:1], exec
	s_cselect_b32 s0, s77, 0x3e600000
	s_add_u32 s0, s94, s0
	s_addc_u32 s1, s95, 0
	s_lshl_b32 s4, s52, 9
	s_and_b32 s4, s4, 0x600
	s_add_u32 s0, s0, s4
	v_mov_b32_e32 v141, v131
	s_addc_u32 s1, s1, 0
	v_lshlrev_b64 v[196:197], 11, v[142:143]
	v_lshl_add_u64 v[144:145], s[0:1], 0, v[140:141]
	v_lshl_add_u64 v[196:197], v[144:145], 0, v[196:197]
	v_lshl_add_u64 v[198:199], v[144:145], 0, v[198:199]
	v_lshlrev_b64 v[154:155], 11, v[154:155]
	v_lshl_add_u64 v[154:155], v[144:145], 0, v[154:155]
	s_waitcnt vmcnt(7)
	v_pk_mul_f32 v[146:147], v[130:131], v[146:147] op_sel_hi:[0,1]
	v_pk_mul_f32 v[148:149], v[130:131], v[148:149] op_sel_hi:[0,1]
	s_waitcnt vmcnt(6)
	v_pk_mul_f32 v[152:153], v[130:131], v[152:153] op_sel_hi:[0,1]
	v_pk_mul_f32 v[150:151], v[130:131], v[150:151] op_sel_hi:[0,1]
	v_pk_mul_f32 v[200:201], v[122:123], v[150:151]
	v_pk_mul_f32 v[202:203], v[124:125], v[152:153]
	v_pk_mul_f32 v[204:205], v[126:127], v[150:151]
	v_pk_mul_f32 v[206:207], v[128:129], v[152:153]
	v_pk_mul_f32 v[208:209], v[114:115], v[150:151]
	v_pk_mul_f32 v[210:211], v[116:117], v[152:153]
	v_pk_mul_f32 v[150:151], v[118:119], v[150:151]
	v_pk_mul_f32 v[152:153], v[120:121], v[152:153]
	s_waitcnt vmcnt(5)
	v_pk_mul_f32 v[176:177], v[130:131], v[176:177] op_sel_hi:[0,1]
	v_pk_mul_f32 v[174:175], v[130:131], v[174:175] op_sel_hi:[0,1]
	s_waitcnt vmcnt(4)
	v_pk_mul_f32 v[172:173], v[130:131], v[172:173] op_sel_hi:[0,1]
	v_pk_mul_f32 v[170:171], v[130:131], v[170:171] op_sel_hi:[0,1]
	v_pk_fma_f32 v[202:203], v[128:129], v[148:149], v[202:203] neg_lo:[0,0,1] neg_hi:[0,0,1]
	v_pk_fma_f32 v[200:201], v[126:127], v[146:147], v[200:201] neg_lo:[0,0,1] neg_hi:[0,0,1]
	v_pk_fma_f32 v[206:207], v[124:125], v[148:149], v[206:207]
	v_pk_fma_f32 v[204:205], v[122:123], v[146:147], v[204:205]
	v_pk_fma_f32 v[210:211], v[120:121], v[148:149], v[210:211] neg_lo:[0,0,1] neg_hi:[0,0,1]
	v_pk_fma_f32 v[208:209], v[118:119], v[146:147], v[208:209] neg_lo:[0,0,1] neg_hi:[0,0,1]
	v_pk_fma_f32 v[148:149], v[116:117], v[148:149], v[152:153]
	v_pk_fma_f32 v[146:147], v[114:115], v[146:147], v[150:151]
	v_pk_mul_f32 v[150:151], v[108:109], v[176:177]
	v_pk_mul_f32 v[152:153], v[106:107], v[174:175]
	v_pk_mul_f32 v[212:213], v[112:113], v[176:177]
	v_pk_mul_f32 v[214:215], v[110:111], v[174:175]
	v_cvt_pk_bf16_f32 v200, v200, v201
	v_cvt_pk_bf16_f32 v201, v202, v203
	v_cvt_pk_bf16_f32 v203, v206, v207
	v_cvt_pk_bf16_f32 v146, v146, v147
	v_cvt_pk_bf16_f32 v147, v148, v149
	v_pk_fma_f32 v[148:149], v[112:113], v[172:173], v[150:151] neg_lo:[0,0,1] neg_hi:[0,0,1]
	v_pk_fma_f32 v[150:151], v[110:111], v[170:171], v[152:153] neg_lo:[0,0,1] neg_hi:[0,0,1]
	v_pk_fma_f32 v[152:153], v[108:109], v[172:173], v[212:213]
	v_pk_fma_f32 v[206:207], v[106:107], v[170:171], v[214:215]
	v_cvt_pk_bf16_f32 v202, v204, v205
	v_cvt_pk_bf16_f32 v204, v208, v209
	v_cvt_pk_bf16_f32 v205, v210, v211
	global_store_dwordx2 v[196:197], v[200:201], off nt
	global_store_dwordx2 v[196:197], v[202:203], off offset:128 nt
	global_store_dwordx2 v[196:197], v[204:205], off offset:256 nt
	global_store_dwordx2 v[196:197], v[146:147], off offset:384 nt
	v_cvt_pk_bf16_f32 v146, v150, v151
	v_cvt_pk_bf16_f32 v147, v148, v149
	v_cvt_pk_bf16_f32 v148, v206, v207
	v_cvt_pk_bf16_f32 v149, v152, v153
	global_store_dwordx2 v[198:199], v[146:147], off nt
	global_store_dwordx2 v[198:199], v[148:149], off offset:128 nt
	v_pk_mul_f32 v[146:147], v[100:101], v[176:177]
	v_pk_mul_f32 v[148:149], v[98:99], v[174:175]
	v_pk_mul_f32 v[150:151], v[104:105], v[176:177]
	v_pk_mul_f32 v[152:153], v[102:103], v[174:175]
	v_pk_fma_f32 v[146:147], v[104:105], v[172:173], v[146:147] neg_lo:[0,0,1] neg_hi:[0,0,1]
	v_pk_fma_f32 v[148:149], v[102:103], v[170:171], v[148:149] neg_lo:[0,0,1] neg_hi:[0,0,1]
	v_pk_fma_f32 v[150:151], v[100:101], v[172:173], v[150:151]
	v_pk_fma_f32 v[152:153], v[98:99], v[170:171], v[152:153]
	v_cvt_pk_bf16_f32 v148, v148, v149
	v_cvt_pk_bf16_f32 v149, v146, v147
	v_cvt_pk_bf16_f32 v146, v152, v153
	v_cvt_pk_bf16_f32 v147, v150, v151
	s_waitcnt vmcnt(8)
; __device__ __forceinline__ unsigned cvt_pk_bf16(float lo, float hi) { f32x2 v = {lo, hi}; bf16x2_t b = __builtin_convertvector(v, bf16x2_t); return __builtin_bit_cast(unsigned, b); }
;     __device__ __forceinline__ void operator()(const AccT& acc, const pg8::Unit& u, int wr, int wc, int fr, int fq) const {
;     ...
;                 f32x4 cc[4], ss[4];
; #pragma unroll
;                 for (int m = 0; m < 4; ++m) { const int row = row0 + ai * 128 + m * 16; cc[m] = *(const f32x4*)(rc + (size_t)row * 64 + dd); ss[m] = *(const f32x4*)(rs + (size_t)row * 64 + dd); }
; #pragma unroll
;                 for (int m = 0; m < 4; ++m) { const int row = row0 + ai * 128 + m * 16;
;                     const f32x4 c = cc[m] * sc, s = ss[m] * sc;
; #pragma unroll
;                     for (int bj = 0; bj < 2; ++bj) { const f32x4 t1 = acc[ai][bj][m][0], t2 = acc[ai][bj][m][1];
;                         const f32x4 o1 = t1 * c - t2 * s, o2 = t2 * c + t1 * s;
;                         bf16_t* p = dst + (size_t)row * QKW + (pn & 3) * 256 + bj * 128 + dd;
;                         u32x2 w1, w2; w1.x = cvt_pk_bf16(o1[0], o1[1]); w1.y = cvt_pk_bf16(o1[2], o1[3]); w2.x = cvt_pk_bf16(o2[0], o2[1]); w2.y = cvt_pk_bf16(o2[2], o2[3]);
;                         if (pn < 12) { __builtin_nontemporal_store(w1, (u32x2*)p); __builtin_nontemporal_store(w2, (u32x2*)(p + 64)); }
;                         else { *(u32x2*)p = w1; *(u32x2*)(p + 64) = w2; } } } }
	v_pk_mul_f32 v[150:151], v[130:131], v[184:185] op_sel_hi:[0,1]
	v_pk_mul_f32 v[152:153], v[130:131], v[182:183] op_sel_hi:[0,1]
	global_store_dwordx2 v[198:199], v[148:149], off offset:256 nt
	global_store_dwordx2 v[198:199], v[146:147], off offset:384 nt
	v_pk_mul_f32 v[146:147], v[130:131], v[180:181] op_sel_hi:[0,1]
	v_pk_mul_f32 v[148:149], v[130:131], v[178:179] op_sel_hi:[0,1]
	v_pk_mul_f32 v[170:171], v[92:93], v[150:151]
	v_pk_mul_f32 v[172:173], v[90:91], v[152:153]
	v_pk_mul_f32 v[174:175], v[96:97], v[150:151]
	v_pk_mul_f32 v[176:177], v[94:95], v[152:153]
	v_pk_fma_f32 v[170:171], v[96:97], v[146:147], v[170:171] neg_lo:[0,0,1] neg_hi:[0,0,1]
	v_pk_fma_f32 v[172:173], v[94:95], v[148:149], v[172:173] neg_lo:[0,0,1] neg_hi:[0,0,1]
	v_pk_fma_f32 v[174:175], v[92:93], v[146:147], v[174:175]
	v_pk_fma_f32 v[176:177], v[90:91], v[148:149], v[176:177]
	v_cvt_pk_bf16_f32 v172, v172, v173
	v_cvt_pk_bf16_f32 v173, v170, v171
	v_cvt_pk_bf16_f32 v170, v176, v177
	v_cvt_pk_bf16_f32 v171, v174, v175
	global_store_dwordx2 v[154:155], v[172:173], off nt
	global_store_dwordx2 v[154:155], v[170:171], off offset:128 nt
	v_pk_mul_f32 v[170:171], v[84:85], v[150:151]
	v_pk_mul_f32 v[172:173], v[82:83], v[152:153]
	v_pk_fma_f32 v[170:171], v[88:89], v[146:147], v[170:171] neg_lo:[0,0,1] neg_hi:[0,0,1]
	v_pk_fma_f32 v[172:173], v[86:87], v[148:149], v[172:173] neg_lo:[0,0,1] neg_hi:[0,0,1]
	v_pk_mul_f32 v[150:151], v[88:89], v[150:151]
	v_pk_mul_f32 v[152:153], v[86:87], v[152:153]
	v_pk_fma_f32 v[146:147], v[84:85], v[146:147], v[150:151]
	v_pk_fma_f32 v[148:149], v[82:83], v[148:149], v[152:153]
	v_cvt_pk_bf16_f32 v150, v172, v173
	v_cvt_pk_bf16_f32 v151, v170, v171
	v_cvt_pk_bf16_f32 v148, v148, v149
	v_cvt_pk_bf16_f32 v149, v146, v147
	global_store_dwordx2 v[154:155], v[150:151], off offset:256 nt
	global_store_dwordx2 v[154:155], v[148:149], off offset:384 nt
	s_waitcnt vmcnt(12)
	v_pk_mul_f32 v[150:151], v[130:131], v[192:193] op_sel_hi:[0,1]
	v_pk_mul_f32 v[152:153], v[130:131], v[190:191] op_sel_hi:[0,1]
	v_pk_mul_f32 v[146:147], v[130:131], v[188:189] op_sel_hi:[0,1]
	v_pk_mul_f32 v[148:149], v[130:131], v[186:187] op_sel_hi:[0,1]
	v_pk_mul_f32 v[170:171], v[76:77], v[150:151]
	v_pk_mul_f32 v[172:173], v[74:75], v[152:153]
	v_pk_mul_f32 v[174:175], v[80:81], v[150:151]
	v_pk_mul_f32 v[176:177], v[78:79], v[152:153]
	v_lshlrev_b64 v[154:155], 11, v[194:195]
	v_pk_fma_f32 v[170:171], v[80:81], v[146:147], v[170:171] neg_lo:[0,0,1] neg_hi:[0,0,1]
	v_pk_fma_f32 v[172:173], v[78:79], v[148:149], v[172:173] neg_lo:[0,0,1] neg_hi:[0,0,1]
	v_pk_fma_f32 v[174:175], v[76:77], v[146:147], v[174:175]
	v_pk_fma_f32 v[176:177], v[74:75], v[148:149], v[176:177]
	v_lshl_add_u64 v[154:155], v[144:145], 0, v[154:155]
	v_cvt_pk_bf16_f32 v172, v172, v173
	v_cvt_pk_bf16_f32 v173, v170, v171
	v_cvt_pk_bf16_f32 v170, v176, v177
	v_cvt_pk_bf16_f32 v171, v174, v175
	global_store_dwordx2 v[154:155], v[172:173], off nt
	global_store_dwordx2 v[154:155], v[170:171], off offset:128 nt
	v_pk_mul_f32 v[170:171], v[68:69], v[150:151]
	v_pk_mul_f32 v[172:173], v[66:67], v[152:153]
	v_pk_fma_f32 v[170:171], v[72:73], v[146:147], v[170:171] neg_lo:[0,0,1] neg_hi:[0,0,1]
	v_pk_fma_f32 v[172:173], v[70:71], v[148:149], v[172:173] neg_lo:[0,0,1] neg_hi:[0,0,1]
	v_pk_mul_f32 v[150:151], v[72:73], v[150:151]
	v_pk_mul_f32 v[152:153], v[70:71], v[152:153]
	v_pk_fma_f32 v[146:147], v[68:69], v[146:147], v[150:151]
	v_pk_fma_f32 v[148:149], v[66:67], v[148:149], v[152:153]
	v_cvt_pk_bf16_f32 v150, v172, v173
	v_cvt_pk_bf16_f32 v151, v170, v171
	v_cvt_pk_bf16_f32 v148, v148, v149
	v_cvt_pk_bf16_f32 v149, v146, v147
	global_store_dwordx2 v[154:155], v[150:151], off offset:256 nt
	global_store_dwordx2 v[154:155], v[148:149], off offset:384 nt
	v_add_u32_e32 v154, 0x80, v142
	v_ashrrev_i32_e32 v155, 31, v154
	v_lshlrev_b64 v[150:151], 8, v[154:155]
	v_lshl_add_u64 v[146:147], v[132:133], 0, v[150:151]
	v_lshl_add_u64 v[150:151], v[134:135], 0, v[150:151]
	global_load_dwordx4 v[146:149], v[146:147], off
	v_add_u32_e32 v194, 0x90, v142
	global_load_dwordx4 v[150:153], v[150:151], off
	v_ashrrev_i32_e32 v195, 31, v194
	v_lshlrev_b64 v[174:175], 8, v[194:195]
	v_lshl_add_u64 v[170:171], v[132:133], 0, v[174:175]
	v_lshl_add_u64 v[174:175], v[134:135], 0, v[174:175]
	global_load_dwordx4 v[170:173], v[170:171], off
	v_add_u32_e32 v196, 0xa0, v142
	global_load_dwordx4 v[174:177], v[174:175], off
	v_ashrrev_i32_e32 v197, 31, v196
	v_lshlrev_b64 v[182:183], 8, v[196:197]
	v_lshl_add_u64 v[178:179], v[132:133], 0, v[182:183]
	v_lshl_add_u64 v[182:183], v[134:135], 0, v[182:183]
	global_load_dwordx4 v[178:181], v[178:179], off
	v_add_u32_e32 v198, 0xb0, v142
	global_load_dwordx4 v[182:185], v[182:183], off
	v_ashrrev_i32_e32 v199, 31, v198
	v_lshlrev_b64 v[186:187], 8, v[198:199]
	v_lshl_add_u64 v[188:189], v[132:133], 0, v[186:187]
	v_lshl_add_u64 v[190:191], v[134:135], 0, v[186:187]
	global_load_dwordx4 v[186:189], v[188:189], off
	s_nop 0
	global_load_dwordx4 v[190:193], v[190:191], off
	v_lshlrev_b64 v[154:155], 11, v[154:155]
	v_lshl_add_u64 v[154:155], v[144:145], 0, v[154:155]
	s_waitcnt vmcnt(7)
	v_pk_mul_f32 v[148:149], v[130:131], v[148:149] op_sel_hi:[0,1]
	v_pk_mul_f32 v[146:147], v[130:131], v[146:147] op_sel_hi:[0,1]
	s_waitcnt vmcnt(6)
; __device__ __forceinline__ unsigned cvt_pk_bf16(float lo, float hi) { f32x2 v = {lo, hi}; bf16x2_t b = __builtin_convertvector(v, bf16x2_t); return __builtin_bit_cast(unsigned, b); }
;     __device__ __forceinline__ void operator()(const AccT& acc, const pg8::Unit& u, int wr, int wc, int fr, int fq) const {
;     ...
;                 for (int m = 0; m < 4; ++m) { const int row = row0 + ai * 128 + m * 16;
;                     const f32x4 c = cc[m] * sc, s = ss[m] * sc;
; #pragma unroll
;                     for (int bj = 0; bj < 2; ++bj) { const f32x4 t1 = acc[ai][bj][m][0], t2 = acc[ai][bj][m][1];
;                         const f32x4 o1 = t1 * c - t2 * s, o2 = t2 * c + t1 * s;
;                         bf16_t* p = dst + (size_t)row * QKW + (pn & 3) * 256 + bj * 128 + dd;
;                         u32x2 w1, w2; w1.x = cvt_pk_bf16(o1[0], o1[1]); w1.y = cvt_pk_bf16(o1[2], o1[3]); w2.x = cvt_pk_bf16(o2[0], o2[1]); w2.y = cvt_pk_bf16(o2[2], o2[3]);
;                         if (pn < 12) { __builtin_nontemporal_store(w1, (u32x2*)p); __builtin_nontemporal_store(w2, (u32x2*)(p + 64)); }
;                         else { *(u32x2*)p = w1; *(u32x2*)(p + 64) = w2; } } } }
	v_pk_mul_f32 v[152:153], v[130:131], v[152:153] op_sel_hi:[0,1]
	v_pk_mul_f32 v[150:151], v[130:131], v[150:151] op_sel_hi:[0,1]
	v_pk_mul_f32 v[200:201], v[60:61], v[152:153]
	v_pk_mul_f32 v[202:203], v[58:59], v[150:151]
	v_pk_mul_f32 v[204:205], v[64:65], v[152:153]
	v_pk_mul_f32 v[206:207], v[62:63], v[150:151]
	v_pk_fma_f32 v[200:201], v[64:65], v[148:149], v[200:201] neg_lo:[0,0,1] neg_hi:[0,0,1]
	v_pk_fma_f32 v[202:203], v[62:63], v[146:147], v[202:203] neg_lo:[0,0,1] neg_hi:[0,0,1]
	v_pk_fma_f32 v[204:205], v[60:61], v[148:149], v[204:205]
	v_pk_fma_f32 v[206:207], v[58:59], v[146:147], v[206:207]
	v_cvt_pk_bf16_f32 v202, v202, v203
	v_cvt_pk_bf16_f32 v203, v200, v201
	v_cvt_pk_bf16_f32 v200, v206, v207
	v_cvt_pk_bf16_f32 v201, v204, v205
	global_store_dwordx2 v[154:155], v[202:203], off nt
	global_store_dwordx2 v[154:155], v[200:201], off offset:128 nt
	v_pk_mul_f32 v[200:201], v[52:53], v[152:153]
	v_pk_mul_f32 v[202:203], v[50:51], v[150:151]
	v_pk_fma_f32 v[200:201], v[56:57], v[148:149], v[200:201] neg_lo:[0,0,1] neg_hi:[0,0,1]
	v_pk_fma_f32 v[202:203], v[54:55], v[146:147], v[202:203] neg_lo:[0,0,1] neg_hi:[0,0,1]
	v_pk_mul_f32 v[152:153], v[56:57], v[152:153]
	v_pk_mul_f32 v[150:151], v[54:55], v[150:151]
	v_pk_fma_f32 v[148:149], v[52:53], v[148:149], v[152:153]
	v_pk_fma_f32 v[146:147], v[50:51], v[146:147], v[150:151]
	v_cvt_pk_bf16_f32 v150, v202, v203
	v_cvt_pk_bf16_f32 v151, v200, v201
	v_cvt_pk_bf16_f32 v146, v146, v147
	v_cvt_pk_bf16_f32 v147, v148, v149
	global_store_dwordx2 v[154:155], v[150:151], off offset:256 nt
	global_store_dwordx2 v[154:155], v[146:147], off offset:384 nt
	s_waitcnt vmcnt(8)
	v_pk_mul_f32 v[150:151], v[130:131], v[176:177] op_sel_hi:[0,1]
	v_pk_mul_f32 v[152:153], v[130:131], v[174:175] op_sel_hi:[0,1]
	v_pk_mul_f32 v[146:147], v[130:131], v[172:173] op_sel_hi:[0,1]
	v_pk_mul_f32 v[148:149], v[130:131], v[170:171] op_sel_hi:[0,1]
	v_pk_mul_f32 v[170:171], v[44:45], v[150:151]
	v_pk_mul_f32 v[172:173], v[42:43], v[152:153]
	v_pk_mul_f32 v[174:175], v[48:49], v[150:151]
	v_pk_mul_f32 v[176:177], v[46:47], v[152:153]
	v_lshlrev_b64 v[154:155], 11, v[194:195]
	v_pk_fma_f32 v[170:171], v[48:49], v[146:147], v[170:171] neg_lo:[0,0,1] neg_hi:[0,0,1]
	v_pk_fma_f32 v[172:173], v[46:47], v[148:149], v[172:173] neg_lo:[0,0,1] neg_hi:[0,0,1]
	v_pk_fma_f32 v[174:175], v[44:45], v[146:147], v[174:175]
	v_pk_fma_f32 v[176:177], v[42:43], v[148:149], v[176:177]
	v_lshl_add_u64 v[154:155], v[144:145], 0, v[154:155]
	v_cvt_pk_bf16_f32 v172, v172, v173
	v_cvt_pk_bf16_f32 v173, v170, v171
	v_cvt_pk_bf16_f32 v170, v176, v177
	v_cvt_pk_bf16_f32 v171, v174, v175
	global_store_dwordx2 v[154:155], v[172:173], off nt
	global_store_dwordx2 v[154:155], v[170:171], off offset:128 nt
	v_pk_mul_f32 v[170:171], v[36:37], v[150:151]
	v_pk_mul_f32 v[172:173], v[34:35], v[152:153]
	v_pk_fma_f32 v[170:171], v[40:41], v[146:147], v[170:171] neg_lo:[0,0,1] neg_hi:[0,0,1]
	v_pk_fma_f32 v[172:173], v[38:39], v[148:149], v[172:173] neg_lo:[0,0,1] neg_hi:[0,0,1]
	v_pk_mul_f32 v[150:151], v[40:41], v[150:151]
	v_pk_mul_f32 v[152:153], v[38:39], v[152:153]
	v_pk_fma_f32 v[146:147], v[36:37], v[146:147], v[150:151]
	v_pk_fma_f32 v[148:149], v[34:35], v[148:149], v[152:153]
	v_cvt_pk_bf16_f32 v150, v172, v173
	v_cvt_pk_bf16_f32 v151, v170, v171
	v_cvt_pk_bf16_f32 v148, v148, v149
	v_cvt_pk_bf16_f32 v149, v146, v147
	global_store_dwordx2 v[154:155], v[150:151], off offset:256 nt
	global_store_dwordx2 v[154:155], v[148:149], off offset:384 nt
	s_waitcnt vmcnt(10)
; __device__ __forceinline__ unsigned cvt_pk_bf16(float lo, float hi) { f32x2 v = {lo, hi}; bf16x2_t b = __builtin_convertvector(v, bf16x2_t); return __builtin_bit_cast(unsigned, b); }
;     __device__ __forceinline__ void operator()(const AccT& acc, const pg8::Unit& u, int wr, int wc, int fr, int fq) const {
;     ...
;                 for (int m = 0; m < 4; ++m) { const int row = row0 + ai * 128 + m * 16;
;                     const f32x4 c = cc[m] * sc, s = ss[m] * sc;
; #pragma unroll
;                     for (int bj = 0; bj < 2; ++bj) { const f32x4 t1 = acc[ai][bj][m][0], t2 = acc[ai][bj][m][1];
;                         const f32x4 o1 = t1 * c - t2 * s, o2 = t2 * c + t1 * s;
;                         bf16_t* p = dst + (size_t)row * QKW + (pn & 3) * 256 + bj * 128 + dd;
;                         u32x2 w1, w2; w1.x = cvt_pk_bf16(o1[0], o1[1]); w1.y = cvt_pk_bf16(o1[2], o1[3]); w2.x = cvt_pk_bf16(o2[0], o2[1]); w2.y = cvt_pk_bf16(o2[2], o2[3]);
;                         if (pn < 12) { __builtin_nontemporal_store(w1, (u32x2*)p); __builtin_nontemporal_store(w2, (u32x2*)(p + 64)); }
;                         else { *(u32x2*)p = w1; *(u32x2*)(p + 64) = w2; } } } }
	v_pk_mul_f32 v[150:151], v[130:131], v[184:185] op_sel_hi:[0,1]
	v_pk_mul_f32 v[152:153], v[130:131], v[182:183] op_sel_hi:[0,1]
	v_pk_mul_f32 v[146:147], v[130:131], v[180:181] op_sel_hi:[0,1]
	v_pk_mul_f32 v[148:149], v[130:131], v[178:179] op_sel_hi:[0,1]
	v_pk_mul_f32 v[170:171], v[28:29], v[150:151]
	v_pk_mul_f32 v[172:173], v[26:27], v[152:153]
	v_pk_mul_f32 v[174:175], v[32:33], v[150:151]
	v_pk_mul_f32 v[176:177], v[30:31], v[152:153]
	v_lshlrev_b64 v[154:155], 11, v[196:197]
	v_pk_fma_f32 v[170:171], v[32:33], v[146:147], v[170:171] neg_lo:[0,0,1] neg_hi:[0,0,1]
	v_pk_fma_f32 v[172:173], v[30:31], v[148:149], v[172:173] neg_lo:[0,0,1] neg_hi:[0,0,1]
	v_pk_fma_f32 v[174:175], v[28:29], v[146:147], v[174:175]
	v_pk_fma_f32 v[176:177], v[26:27], v[148:149], v[176:177]
	v_lshl_add_u64 v[154:155], v[144:145], 0, v[154:155]
	v_cvt_pk_bf16_f32 v172, v172, v173
	v_cvt_pk_bf16_f32 v173, v170, v171
	v_cvt_pk_bf16_f32 v170, v176, v177
	v_cvt_pk_bf16_f32 v171, v174, v175
	global_store_dwordx2 v[154:155], v[172:173], off nt
	global_store_dwordx2 v[154:155], v[170:171], off offset:128 nt
	v_pk_mul_f32 v[170:171], v[20:21], v[150:151]
	v_pk_mul_f32 v[172:173], v[18:19], v[152:153]
	v_pk_fma_f32 v[170:171], v[24:25], v[146:147], v[170:171] neg_lo:[0,0,1] neg_hi:[0,0,1]
	v_pk_fma_f32 v[172:173], v[22:23], v[148:149], v[172:173] neg_lo:[0,0,1] neg_hi:[0,0,1]
	v_pk_mul_f32 v[150:151], v[24:25], v[150:151]
	v_pk_mul_f32 v[152:153], v[22:23], v[152:153]
	v_pk_fma_f32 v[146:147], v[20:21], v[146:147], v[150:151]
	v_pk_fma_f32 v[148:149], v[18:19], v[148:149], v[152:153]
	v_cvt_pk_bf16_f32 v150, v172, v173
	v_cvt_pk_bf16_f32 v151, v170, v171
	v_cvt_pk_bf16_f32 v148, v148, v149
	v_cvt_pk_bf16_f32 v149, v146, v147
	global_store_dwordx2 v[154:155], v[150:151], off offset:256 nt
	global_store_dwordx2 v[154:155], v[148:149], off offset:384 nt
	s_waitcnt vmcnt(12)
	v_pk_mul_f32 v[150:151], v[130:131], v[192:193] op_sel_hi:[0,1]
	v_pk_mul_f32 v[152:153], v[130:131], v[190:191] op_sel_hi:[0,1]
	v_lshlrev_b64 v[154:155], 11, v[198:199]
	v_pk_mul_f32 v[146:147], v[130:131], v[188:189] op_sel_hi:[0,1]
	v_pk_mul_f32 v[148:149], v[130:131], v[186:187] op_sel_hi:[0,1]
	v_lshl_add_u64 v[144:145], v[144:145], 0, v[154:155]
	v_pk_mul_f32 v[154:155], v[12:13], v[150:151]
	v_pk_mul_f32 v[170:171], v[10:11], v[152:153]
	v_pk_mul_f32 v[172:173], v[16:17], v[150:151]
	v_pk_mul_f32 v[174:175], v[14:15], v[152:153]
	v_pk_fma_f32 v[154:155], v[16:17], v[146:147], v[154:155] neg_lo:[0,0,1] neg_hi:[0,0,1]
	v_pk_fma_f32 v[170:171], v[14:15], v[148:149], v[170:171] neg_lo:[0,0,1] neg_hi:[0,0,1]
	v_pk_fma_f32 v[172:173], v[12:13], v[146:147], v[172:173]
	v_pk_fma_f32 v[174:175], v[10:11], v[148:149], v[174:175]
	v_cvt_pk_bf16_f32 v170, v170, v171
	v_cvt_pk_bf16_f32 v171, v154, v155
	v_cvt_pk_bf16_f32 v154, v174, v175
	v_cvt_pk_bf16_f32 v155, v172, v173
	global_store_dwordx2 v[144:145], v[170:171], off nt
	global_store_dwordx2 v[144:145], v[154:155], off offset:128 nt
	v_pk_mul_f32 v[154:155], v[4:5], v[150:151]
	v_pk_mul_f32 v[170:171], v[2:3], v[152:153]
	v_pk_fma_f32 v[154:155], v[8:9], v[146:147], v[154:155] neg_lo:[0,0,1] neg_hi:[0,0,1]
	v_pk_fma_f32 v[170:171], v[6:7], v[148:149], v[170:171] neg_lo:[0,0,1] neg_hi:[0,0,1]
	v_pk_mul_f32 v[150:151], v[8:9], v[150:151]
	v_pk_mul_f32 v[152:153], v[6:7], v[152:153]
	v_pk_fma_f32 v[146:147], v[4:5], v[146:147], v[150:151]
	v_pk_fma_f32 v[148:149], v[2:3], v[148:149], v[152:153]
	v_cvt_pk_bf16_f32 v150, v170, v171
	v_cvt_pk_bf16_f32 v151, v154, v155
	v_cvt_pk_bf16_f32 v148, v148, v149
	v_cvt_pk_bf16_f32 v149, v146, v147
	global_store_dwordx2 v[144:145], v[150:151], off offset:256 nt
	global_store_dwordx2 v[144:145], v[148:149], off offset:384 nt

; __device__ __forceinline__ f32x2 gelu_pk(f32x2 v) {
;     const f32x2 av = __builtin_elementwise_abs(v), d = av * 0.2316418882f + 1.0f;
;     f32x2 t; t.x = __builtin_amdgcn_rcpf(d.x); t.y = __builtin_amdgcn_rcpf(d.y);
;     f32x2 q = t * 0.5307027145f + (-0.7265760135f); q = q * t + 0.7107068705f; q = q * t + (-0.142248368f); q = q * t + 0.127414796f; q = q * t;
;     const f32x2 s = (v * v) * (-0.72134752044f);
;     f32x2 e; e.x = __builtin_amdgcn_exp2f(s.x); e.y = __builtin_amdgcn_exp2f(s.y);
;     const f32x2 m = v * (q * e), r = v - m;
;     f32x2 o; o.x = v.x < 0.f ? m.x : r.x; o.y = v.y < 0.f ? m.y : r.y; return o;
; }
; __device__ __forceinline__ f32x4 gelu4(f32x4 v) { f32x2 a = gelu_pk((f32x2){v[0], v[1]}), b = gelu_pk((f32x2){v[2], v[3]}); return (f32x4){a.x, a.y, b.x, b.y}; }
;     __device__ __forceinline__ void operator()(const AccT& acc, const pg8::Unit& u, int wr, int wc, int fr, int fq) const {
;     ...
;         if (pn < 8) {
;             bf16_t* dst = (bf16_t*)(ws + (pn < 4 ? WS_U : WS_V)); const int col0 = (pn & 3) * 256 + wc * 32 + 8 * fq;
;             float* vstat = (float*)(ws + WS_VSTAT);
; #pragma unroll
;             for (int ai = 0; ai < 2; ++ai)
; #pragma unroll
;                 for (int m = 0; m < 4; ++m) { const int row = row0 + ai * 128 + m * 16; float s = 0.f, q = 0.f;
; #pragma unroll
;                     for (int bj = 0; bj < 2; ++bj) { const f32x4 v0 = gelu4(acc[ai][bj][m][0]), v1 = gelu4(acc[ai][bj][m][1]);
.LBB0_246:
	v_and_b32_e32 v147, 0x7fffffff, v127
	v_and_b32_e32 v146, 0x7fffffff, v126
	v_pk_fma_f32 v[146:147], v[146:147], s[28:29], 1.0 op_sel_hi:[1,0,0]
	v_mov_b64_e32 v[148:149], s[34:35]
	v_rcp_f32_e32 v150, v146
	v_rcp_f32_e32 v151, v147
	v_pk_mul_f32 v[154:155], v[126:127], v[126:127]
	v_and_b32_e32 v171, 0x7fffffff, v129
	v_pk_mul_f32 v[154:155], v[154:155], s[42:43] op_sel_hi:[1,0]
	v_pk_fma_f32 v[152:153], v[150:151], s[30:31], v[148:149] op_sel_hi:[1,0,0]
	v_and_b32_e32 v170, 0x7fffffff, v128
	v_pk_fma_f32 v[152:153], v[150:151], v[152:153], s[36:37] op_sel_hi:[1,1,0]
	v_exp_f32_e32 v154, v154
	v_exp_f32_e32 v155, v155
	v_pk_fma_f32 v[170:171], v[170:171], s[28:29], 1.0 op_sel_hi:[1,0,0]
	v_pk_fma_f32 v[152:153], v[150:151], v[152:153], s[38:39] op_sel_hi:[1,1,0]
	v_rcp_f32_e32 v170, v170
	v_rcp_f32_e32 v171, v171
	v_pk_fma_f32 v[152:153], v[150:151], v[152:153], s[40:41] op_sel_hi:[1,1,0]
	s_cmp_lt_i32 s52, 4
	v_pk_mul_f32 v[150:151], v[150:151], v[152:153]
	v_pk_mul_f32 v[152:153], v[128:129], v[128:129]
	v_pk_mul_f32 v[150:151], v[154:155], v[150:151]
	s_cselect_b64 s[0:1], -1, 0
	v_pk_mul_f32 v[154:155], v[126:127], v[150:151]
	v_pk_fma_f32 v[174:175], v[126:127], v[150:151], v[126:127] neg_lo:[1,0,0] neg_hi:[1,0,0]
	v_pk_fma_f32 v[150:151], v[170:171], s[30:31], v[148:149] op_sel_hi:[1,0,0]
	v_pk_mul_f32 v[152:153], v[152:153], s[42:43] op_sel_hi:[1,0]
	v_pk_fma_f32 v[150:151], v[170:171], v[150:151], s[36:37] op_sel_hi:[1,1,0]
	s_and_b64 vcc, s[0:1], exec
	v_pk_fma_f32 v[150:151], v[170:171], v[150:151], s[38:39] op_sel_hi:[1,1,0]
	v_exp_f32_e32 v152, v152
	v_pk_fma_f32 v[150:151], v[170:171], v[150:151], s[40:41] op_sel_hi:[1,1,0]
	v_exp_f32_e32 v153, v153
	v_pk_mul_f32 v[150:151], v[170:171], v[150:151]
	v_and_b32_e32 v171, 0x7fffffff, v123
	v_and_b32_e32 v170, 0x7fffffff, v122
	v_pk_fma_f32 v[170:171], v[170:171], s[28:29], 1.0 op_sel_hi:[1,0,0]
	s_cselect_b32 s0, s78, 0x3a600000
	v_rcp_f32_e32 v170, v170
	v_rcp_f32_e32 v171, v171
	s_add_u32 s0, s94, s0
	s_addc_u32 s1, s95, 0
	s_lshl_b32 s4, s52, 8
	s_and_b32 s4, s4, 0x300
	v_pk_mul_f32 v[150:151], v[152:153], v[150:151]
	v_pk_mul_f32 v[152:153], v[122:123], v[122:123]
	v_or_b32_e32 v130, s4, v162
	v_pk_mul_f32 v[176:177], v[128:129], v[150:151]
	v_pk_fma_f32 v[178:179], v[128:129], v[150:151], v[128:129] neg_lo:[1,0,0] neg_hi:[1,0,0]
	v_pk_fma_f32 v[150:151], v[170:171], s[30:31], v[148:149] op_sel_hi:[1,0,0]
	v_pk_mul_f32 v[152:153], v[152:153], s[42:43] op_sel_hi:[1,0]
	v_lshlrev_b32_e32 v130, 1, v130
	s_cmp_gt_i32 s52, 3
	v_pk_fma_f32 v[150:151], v[170:171], v[150:151], s[36:37] op_sel_hi:[1,1,0]
	v_exp_f32_e32 v152, v152
	v_exp_f32_e32 v153, v153
	v_lshl_add_u64 v[144:145], s[0:1], 0, v[130:131]
	s_cselect_b64 s[54:55], -1, 0
	s_lshl_b32 s0, s52, 3
	v_pk_fma_f32 v[150:151], v[170:171], v[150:151], s[38:39] op_sel_hi:[1,1,0]
	v_and_b32_e32 v173, 0x7fffffff, v125
	v_and_b32_e32 v172, 0x7fffffff, v124
	s_add_i32 s4, s74, s0
	v_pk_fma_f32 v[150:151], v[170:171], v[150:151], s[40:41] op_sel_hi:[1,1,0]
	v_pk_fma_f32 v[172:173], v[172:173], s[28:29], 1.0 op_sel_hi:[1,0,0]
	s_lshl_b64 s[0:1], s[4:5], 2
	v_pk_mul_f32 v[150:151], v[170:171], v[150:151]
	v_rcp_f32_e32 v172, v172
	v_rcp_f32_e32 v173, v173
	s_add_u32 s12, s62, s0
	v_pk_mul_f32 v[150:151], v[152:153], v[150:151]
	s_addc_u32 s13, s63, s1
	v_pk_mul_f32 v[152:153], v[122:123], v[150:151]
	v_pk_fma_f32 v[150:151], v[122:123], v[150:151], v[122:123] neg_lo:[1,0,0] neg_hi:[1,0,0]
	v_cmp_gt_f32_e64 s[0:1], 0, v123
	v_pk_mul_f32 v[170:171], v[124:125], v[124:125]
	v_pk_mul_f32 v[180:181], v[118:119], v[118:119]
	v_cndmask_b32_e64 v123, v151, v153, s[0:1]
	v_cmp_gt_f32_e64 s[0:1], 0, v122
	v_pk_mul_f32 v[180:181], v[180:181], s[42:43] op_sel_hi:[1,0]
	v_and_b32_e32 v183, 0x7fffffff, v121
	v_cndmask_b32_e64 v122, v150, v152, s[0:1]
	v_pk_fma_f32 v[150:151], v[172:173], s[30:31], v[148:149] op_sel_hi:[1,0,0]
	v_pk_mul_f32 v[152:153], v[170:171], s[42:43] op_sel_hi:[1,0]
	v_pk_fma_f32 v[150:151], v[172:173], v[150:151], s[36:37] op_sel_hi:[1,1,0]
	v_exp_f32_e32 v152, v152
	v_exp_f32_e32 v153, v153
	v_pk_fma_f32 v[150:151], v[172:173], v[150:151], s[38:39] op_sel_hi:[1,1,0]
	v_and_b32_e32 v182, 0x7fffffff, v120
	v_pk_fma_f32 v[150:151], v[172:173], v[150:151], s[40:41] op_sel_hi:[1,1,0]
	v_exp_f32_e32 v180, v180
	v_pk_mul_f32 v[150:151], v[172:173], v[150:151]
	v_exp_f32_e32 v181, v181
	v_pk_mul_f32 v[150:151], v[152:153], v[150:151]
	v_pk_fma_f32 v[182:183], v[182:183], s[28:29], 1.0 op_sel_hi:[1,0,0]
	v_pk_mul_f32 v[170:171], v[124:125], v[150:151]
	v_pk_fma_f32 v[172:173], v[124:125], v[150:151], v[124:125] neg_lo:[1,0,0] neg_hi:[1,0,0]
	v_and_b32_e32 v151, 0x7fffffff, v119
	v_and_b32_e32 v150, 0x7fffffff, v118
	v_pk_fma_f32 v[150:151], v[150:151], s[28:29], 1.0 op_sel_hi:[1,0,0]
	v_rcp_f32_e32 v182, v182
	v_rcp_f32_e32 v150, v150
	v_rcp_f32_e32 v151, v151
	v_rcp_f32_e32 v183, v183
	v_cmp_gt_f32_e64 s[0:1], 0, v124
	v_ashrrev_i32_e32 v143, 31, v142
	v_pk_fma_f32 v[152:153], v[150:151], s[30:31], v[148:149] op_sel_hi:[1,0,0]
	v_cndmask_b32_e64 v124, v172, v170, s[0:1]
	v_pk_fma_f32 v[152:153], v[150:151], v[152:153], s[36:37] op_sel_hi:[1,1,0]
	v_cmp_gt_f32_e64 s[0:1], 0, v120
	v_pk_fma_f32 v[152:153], v[150:151], v[152:153], s[38:39] op_sel_hi:[1,1,0]
	v_lshlrev_b64 v[146:147], 11, v[142:143]
	v_pk_fma_f32 v[152:153], v[150:151], v[152:153], s[40:41] op_sel_hi:[1,1,0]
	v_lshl_add_u64 v[146:147], v[144:145], 0, v[146:147]
	v_pk_mul_f32 v[150:151], v[150:151], v[152:153]
	v_pk_mul_f32 v[152:153], v[120:121], v[120:121]
	v_pk_mul_f32 v[150:151], v[180:181], v[150:151]
	v_pk_mul_f32 v[152:153], v[152:153], s[42:43] op_sel_hi:[1,0]
; __device__ __forceinline__ unsigned cvt_pk_bf16(float lo, float hi) { f32x2 v = {lo, hi}; bf16x2_t b = __builtin_convertvector(v, bf16x2_t); return __builtin_bit_cast(unsigned, b); }
; __device__ __forceinline__ f32x2 gelu_pk(f32x2 v) {
;     const f32x2 av = __builtin_elementwise_abs(v), d = av * 0.2316418882f + 1.0f;
;     f32x2 t; t.x = __builtin_amdgcn_rcpf(d.x); t.y = __builtin_amdgcn_rcpf(d.y);
;     f32x2 q = t * 0.5307027145f + (-0.7265760135f); q = q * t + 0.7107068705f; q = q * t + (-0.142248368f); q = q * t + 0.127414796f; q = q * t;
;     const f32x2 s = (v * v) * (-0.72134752044f);
;     f32x2 e; e.x = __builtin_amdgcn_exp2f(s.x); e.y = __builtin_amdgcn_exp2f(s.y);
;     const f32x2 m = v * (q * e), r = v - m;
;     f32x2 o; o.x = v.x < 0.f ? m.x : r.x; o.y = v.y < 0.f ? m.y : r.y; return o;
; }
; __device__ __forceinline__ f32x4 gelu4(f32x4 v) { f32x2 a = gelu_pk((f32x2){v[0], v[1]}), b = gelu_pk((f32x2){v[2], v[3]}); return (f32x4){a.x, a.y, b.x, b.y}; }
;     __device__ __forceinline__ void operator()(const AccT& acc, const pg8::Unit& u, int wr, int wc, int fr, int fq) const {
;     ...
;                 for (int m = 0; m < 4; ++m) { const int row = row0 + ai * 128 + m * 16; float s = 0.f, q = 0.f;
; #pragma unroll
;                     for (int bj = 0; bj < 2; ++bj) { const f32x4 v0 = gelu4(acc[ai][bj][m][0]), v1 = gelu4(acc[ai][bj][m][1]);
;                         s += (v0[0] + v0[1]) + (v0[2] + v0[3]) + (v1[0] + v1[1]) + (v1[2] + v1[3]);
;                         q += (v0[0] * v0[0] + v0[1] * v0[1]) + (v0[2] * v0[2] + v0[3] * v0[3]) + (v1[0] * v1[0] + v1[1] * v1[1]) + (v1[2] * v1[2] + v1[3] * v1[3]);
;                         u32x4 w; w.x = cvt_pk_bf16(v0[0], v0[1]); w.y = cvt_pk_bf16(v0[2], v0[3]); w.z = cvt_pk_bf16(v1[0], v1[1]); w.w = cvt_pk_bf16(v1[2], v1[3]);
;                         *(u32x4*)(dst + (size_t)row * GW + col0 + bj * 128) = w; }
;                     if (pn >= 4) { s += __shfl_xor(s, 16); s += __shfl_xor(s, 32); q += __shfl_xor(q, 16); q += __shfl_xor(q, 32);
;                         if (fq == 0) *(f32x2*)(vstat + (size_t)row * 32 + ((pn - 4) * 4 + wc) * 2) = (f32x2){s, q}; } }
	v_pk_mul_f32 v[180:181], v[118:119], v[150:151]
	v_pk_fma_f32 v[184:185], v[118:119], v[150:151], v[118:119] neg_lo:[1,0,0] neg_hi:[1,0,0]
	v_pk_fma_f32 v[150:151], v[182:183], s[30:31], v[148:149] op_sel_hi:[1,0,0]
	v_exp_f32_e32 v152, v152
	v_pk_fma_f32 v[150:151], v[182:183], v[150:151], s[36:37] op_sel_hi:[1,1,0]
	v_exp_f32_e32 v153, v153
	v_pk_fma_f32 v[150:151], v[182:183], v[150:151], s[38:39] op_sel_hi:[1,1,0]
	v_cvt_pk_bf16_f32 v172, v122, v123
	v_pk_fma_f32 v[150:151], v[182:183], v[150:151], s[40:41] op_sel_hi:[1,1,0]
	s_nop 0
	v_pk_mul_f32 v[150:151], v[182:183], v[150:151]
	s_nop 0
	v_pk_mul_f32 v[150:151], v[152:153], v[150:151]
	s_nop 0
	v_pk_mul_f32 v[152:153], v[120:121], v[150:151]
	v_pk_fma_f32 v[182:183], v[120:121], v[150:151], v[120:121] neg_lo:[1,0,0] neg_hi:[1,0,0]
	v_and_b32_e32 v151, 0x7fffffff, v115
	v_and_b32_e32 v150, 0x7fffffff, v114
	v_pk_fma_f32 v[150:151], v[150:151], s[28:29], 1.0 op_sel_hi:[1,0,0]
	s_nop 0
	v_rcp_f32_e32 v186, v150
	v_rcp_f32_e32 v187, v151
	v_cndmask_b32_e64 v151, v182, v152, s[0:1]
	v_cmp_gt_f32_e64 s[0:1], 0, v121
	s_nop 1
	v_cndmask_b32_e64 v121, v183, v153, s[0:1]
	v_pk_mul_f32 v[182:183], v[114:115], v[114:115]
	v_pk_fma_f32 v[152:153], v[186:187], s[30:31], v[148:149] op_sel_hi:[1,0,0]
	v_pk_mul_f32 v[182:183], v[182:183], s[42:43] op_sel_hi:[1,0]
	v_pk_fma_f32 v[152:153], v[186:187], v[152:153], s[36:37] op_sel_hi:[1,1,0]
	v_exp_f32_e32 v182, v182
	v_exp_f32_e32 v183, v183
	v_pk_fma_f32 v[152:153], v[186:187], v[152:153], s[38:39] op_sel_hi:[1,1,0]
	v_cmp_gt_f32_e64 s[0:1], 0, v126
	v_pk_fma_f32 v[152:153], v[186:187], v[152:153], s[40:41] op_sel_hi:[1,1,0]
	s_nop 0
	v_pk_mul_f32 v[152:153], v[186:187], v[152:153]
	v_pk_mul_f32 v[186:187], v[116:117], v[116:117]
	v_pk_mul_f32 v[152:153], v[182:183], v[152:153]
	s_nop 0
	v_pk_mul_f32 v[182:183], v[114:115], v[152:153]
	v_pk_fma_f32 v[188:189], v[114:115], v[152:153], v[114:115] neg_lo:[1,0,0] neg_hi:[1,0,0]
	v_cndmask_b32_e64 v152, v174, v154, s[0:1]
	v_cmp_gt_f32_e64 s[0:1], 0, v118
	v_and_b32_e32 v174, 0x7fffffff, v116
	s_nop 0
	v_cndmask_b32_e64 v153, v184, v180, s[0:1]
	v_cmp_gt_f32_e64 s[0:1], 0, v127
	s_nop 1
	v_cndmask_b32_e64 v154, v175, v155, s[0:1]
	v_cmp_gt_f32_e64 s[0:1], 0, v128
	v_and_b32_e32 v175, 0x7fffffff, v117
	v_pk_fma_f32 v[174:175], v[174:175], s[28:29], 1.0 op_sel_hi:[1,0,0]
	v_cndmask_b32_e64 v126, v178, v176, s[0:1]
	v_cmp_gt_f32_e64 s[0:1], 0, v119
	v_rcp_f32_e32 v174, v174
	v_rcp_f32_e32 v175, v175
	v_cndmask_b32_e64 v127, v185, v181, s[0:1]
	v_cmp_gt_f32_e64 s[0:1], 0, v129
	v_cvt_pk_bf16_f32 v170, v152, v154
	v_pk_fma_f32 v[148:149], v[174:175], s[30:31], v[148:149] op_sel_hi:[1,0,0]
	v_cndmask_b32_e64 v128, v179, v177, s[0:1]
	v_cmp_gt_f32_e64 s[0:1], 0, v114
	v_pk_fma_f32 v[148:149], v[174:175], v[148:149], s[36:37] op_sel_hi:[1,1,0]
	s_nop 0
	v_cndmask_b32_e64 v118, v188, v182, s[0:1]
	v_cmp_gt_f32_e64 s[0:1], 0, v125
	v_pk_fma_f32 v[148:149], v[174:175], v[148:149], s[38:39] op_sel_hi:[1,1,0]
	s_nop 0
	v_cndmask_b32_e64 v119, v173, v171, s[0:1]
	v_cvt_pk_bf16_f32 v171, v126, v128
	v_cvt_pk_bf16_f32 v173, v124, v119
	global_store_dwordx4 v[146:147], v[170:173], off nt
	v_pk_fma_f32 v[148:149], v[174:175], v[148:149], s[40:41] op_sel_hi:[1,1,0]
	v_cmp_gt_f32_e64 s[0:1], 0, v115
	v_pk_mul_f32 v[170:171], v[186:187], s[42:43] op_sel_hi:[1,0]
	v_pk_mul_f32 v[148:149], v[174:175], v[148:149]
	v_exp_f32_e32 v170, v170
	v_exp_f32_e32 v171, v171
	v_cndmask_b32_e64 v114, v189, v183, s[0:1]
	v_cmp_gt_f32_e64 s[0:1], 0, v117
	v_cvt_pk_bf16_f32 v172, v118, v114
	v_pk_mul_f32 v[148:149], v[170:171], v[148:149]
	s_nop 0
	v_pk_mul_f32 v[170:171], v[116:117], v[148:149]
	v_pk_fma_f32 v[148:149], v[116:117], v[148:149], v[116:117] neg_lo:[1,0,0] neg_hi:[1,0,0]
	s_nop 0
	v_cndmask_b32_e64 v117, v149, v171, s[0:1]
	v_cmp_gt_f32_e64 s[0:1], 0, v116
	v_cvt_pk_bf16_f32 v171, v151, v121
	s_nop 0
	v_cndmask_b32_e64 v116, v148, v170, s[0:1]
	v_cvt_pk_bf16_f32 v170, v153, v127
	v_cvt_pk_bf16_f32 v173, v116, v117
	global_store_dwordx4 v[146:147], v[170:173], off offset:256 nt
	s_cbranch_vccnz .LBB0_250
	v_mov_b32_e32 v155, v153
	v_mov_b32_e32 v115, v119
	v_mov_b32_e32 v129, v127
	v_pk_add_f32 v[146:147], v[118:119], v[114:115]
	v_pk_mul_f32 v[148:149], v[118:119], v[114:115]
	v_mov_b32_e32 v170, v154
	v_pk_add_f32 v[174:175], v[152:153], v[154:155]
	v_pk_mul_f32 v[154:155], v[152:153], v[154:155]
	v_mov_b32_e32 v147, v149
	v_mov_b32_e32 v149, v126
	v_mov_b32_e32 v171, v128
	v_mov_b32_e32 v175, v155
	v_pk_add_f32 v[154:155], v[126:127], v[128:129]
	v_pk_mul_f32 v[128:129], v[126:127], v[128:129]
	v_and_b32_e32 v126, 64, v169
	v_xor_b32_e32 v125, 16, v169
	v_add_u32_e32 v126, 64, v126
	v_mov_b32_e32 v148, v152
	v_pk_mul_f32 v[170:171], v[170:171], v[170:171]
	v_mul_f32_e32 v120, v122, v122
	v_cmp_lt_i32_e32 vcc, v125, v126
	v_pk_fma_f32 v[148:149], v[148:149], v[148:149], v[170:171]
	v_pk_fma_f32 v[170:171], v[122:123], v[122:123], v[120:121] op_sel_hi:[1,1,0]
	v_mul_f32_e32 v120, v116, v116
	v_mov_b32_e32 v155, v129
	v_mul_f32_e32 v129, v151, v151
	v_mul_f32_e32 v177, v121, v121
	v_pk_mul_f32 v[178:179], v[118:119], v[118:119]
	v_pk_mul_f32 v[114:115], v[114:115], v[114:115]
	v_cndmask_b32_e32 v125, v169, v125, vcc
	v_mov_b32_e32 v128, v122
	v_mov_b32_e32 v176, v123
	v_pk_fma_f32 v[172:173], v[116:117], v[116:117], v[120:121] op_sel_hi:[1,1,0]
	v_mov_b32_e32 v150, v153
	v_mov_b32_e32 v120, v127
	v_lshlrev_b32_e32 v127, 2, v125
	v_mov_b32_e32 v125, v178
	v_pk_mov_b32 v[114:115], v[118:119], v[114:115] op_sel:[1,0]
	v_pk_add_f32 v[118:119], v[174:175], v[154:155]
	v_pk_add_f32 v[122:123], v[128:129], v[176:177]
	v_pk_add_f32 v[120:121], v[150:151], v[120:121]
	v_pk_add_f32 v[114:115], v[124:125], v[114:115]
	v_pk_add_f32 v[118:119], v[118:119], v[122:123]
	v_mul_f32_e32 v130, v124, v124
	v_pk_add_f32 v[148:149], v[148:149], v[148:149] op_sel_hi:[0,1]
	v_pk_add_f32 v[114:115], v[118:119], v[114:115]
	v_pk_add_f32 v[118:119], v[120:121], v[120:121] op_sel:[0,1] op_sel_hi:[1,0]
	v_mov_b32_e32 v148, v116
	v_mov_b32_e32 v170, v117
	v_mov_b32_e32 v119, v130
	v_mov_b32_e32 v172, v131
	v_pk_add_f32 v[116:117], v[148:149], v[170:171]
	v_pk_add_f32 v[118:119], v[118:119], v[146:147]
	v_pk_add_f32 v[114:115], v[114:115], v[172:173]
	v_pk_add_f32 v[116:117], v[118:119], v[116:117]
	v_xor_b32_e32 v118, 32, v169
	v_pk_add_f32 v[114:115], v[116:117], v[114:115]
	ds_bpermute_b32 v116, v127, v114
	ds_bpermute_b32 v117, v127, v115
	v_cmp_lt_i32_e32 vcc, v118, v126
	s_waitcnt lgkmcnt(0)
	v_pk_add_f32 v[114:115], v[114:115], v[116:117]
	v_cndmask_b32_e32 v118, v169, v118, vcc
	v_lshlrev_b32_e32 v118, 2, v118
	ds_bpermute_b32 v116, v118, v114
	ds_bpermute_b32 v117, v118, v115
	s_and_saveexec_b64 s[0:1], s[6:7]
	s_cbranch_execz .LBB0_249
	s_waitcnt lgkmcnt(0)
	v_pk_add_f32 v[114:115], v[114:115], v[116:117]
	v_lshlrev_b64 v[116:117], 7, v[142:143]
	v_lshl_add_u64 v[116:117], s[12:13], 0, v[116:117]
	global_store_dwordx2 v[116:117], v[114:115], off nt

; __device__ __forceinline__ unsigned cvt_pk_bf16(float lo, float hi) { f32x2 v = {lo, hi}; bf16x2_t b = __builtin_convertvector(v, bf16x2_t); return __builtin_bit_cast(unsigned, b); }
; __device__ __forceinline__ f32x2 gelu_pk(f32x2 v) {
;     const f32x2 av = __builtin_elementwise_abs(v), d = av * 0.2316418882f + 1.0f;
;     f32x2 t; t.x = __builtin_amdgcn_rcpf(d.x); t.y = __builtin_amdgcn_rcpf(d.y);
;     f32x2 q = t * 0.5307027145f + (-0.7265760135f); q = q * t + 0.7107068705f; q = q * t + (-0.142248368f); q = q * t + 0.127414796f; q = q * t;
;     const f32x2 s = (v * v) * (-0.72134752044f);
;     f32x2 e; e.x = __builtin_amdgcn_exp2f(s.x); e.y = __builtin_amdgcn_exp2f(s.y);
;     const f32x2 m = v * (q * e), r = v - m;
;     f32x2 o; o.x = v.x < 0.f ? m.x : r.x; o.y = v.y < 0.f ? m.y : r.y; return o;
; }
; __device__ __forceinline__ f32x4 gelu4(f32x4 v) { f32x2 a = gelu_pk((f32x2){v[0], v[1]}), b = gelu_pk((f32x2){v[2], v[3]}); return (f32x4){a.x, a.y, b.x, b.y}; }
;     __device__ __forceinline__ void operator()(const AccT& acc, const pg8::Unit& u, int wr, int wc, int fr, int fq) const {
;     ...
;                 for (int m = 0; m < 4; ++m) { const int row = row0 + ai * 128 + m * 16; float s = 0.f, q = 0.f;
; #pragma unroll
;                     for (int bj = 0; bj < 2; ++bj) { const f32x4 v0 = gelu4(acc[ai][bj][m][0]), v1 = gelu4(acc[ai][bj][m][1]);
;                         s += (v0[0] + v0[1]) + (v0[2] + v0[3]) + (v1[0] + v1[1]) + (v1[2] + v1[3]);
;                         q += (v0[0] * v0[0] + v0[1] * v0[1]) + (v0[2] * v0[2] + v0[3] * v0[3]) + (v1[0] * v1[0] + v1[1] * v1[1]) + (v1[2] * v1[2] + v1[3] * v1[3]);
;                         u32x4 w; w.x = cvt_pk_bf16(v0[0], v0[1]); w.y = cvt_pk_bf16(v0[2], v0[3]); w.z = cvt_pk_bf16(v1[0], v1[1]); w.w = cvt_pk_bf16(v1[2], v1[3]);
;                         *(u32x4*)(dst + (size_t)row * GW + col0 + bj * 128) = w; }
.LBB0_250:
	s_waitcnt lgkmcnt(0)
	v_and_b32_e32 v117, 0x7fffffff, v111
	v_and_b32_e32 v116, 0x7fffffff, v110
	v_pk_fma_f32 v[116:117], v[116:117], s[28:29], 1.0 op_sel_hi:[1,0,0]
	v_mov_b64_e32 v[118:119], s[34:35]
	v_rcp_f32_e32 v120, v116
	v_rcp_f32_e32 v121, v117
	v_pk_mul_f32 v[124:125], v[110:111], v[110:111]
	v_and_b32_e32 v127, 0x7fffffff, v113
	v_pk_mul_f32 v[124:125], v[124:125], s[42:43] op_sel_hi:[1,0]
	v_pk_fma_f32 v[122:123], v[120:121], s[30:31], v[118:119] op_sel_hi:[1,0,0]
	v_and_b32_e32 v126, 0x7fffffff, v112
	v_pk_fma_f32 v[122:123], v[120:121], v[122:123], s[36:37] op_sel_hi:[1,1,0]
	v_exp_f32_e32 v124, v124
	v_exp_f32_e32 v125, v125
	v_pk_fma_f32 v[126:127], v[126:127], s[28:29], 1.0 op_sel_hi:[1,0,0]
	v_pk_fma_f32 v[122:123], v[120:121], v[122:123], s[38:39] op_sel_hi:[1,1,0]
	v_rcp_f32_e32 v126, v126
	v_rcp_f32_e32 v127, v127
	v_pk_fma_f32 v[122:123], v[120:121], v[122:123], s[40:41] op_sel_hi:[1,1,0]
	v_and_b32_e32 v129, 0x7fffffff, v109
	v_pk_mul_f32 v[120:121], v[120:121], v[122:123]
	v_pk_mul_f32 v[122:123], v[112:113], v[112:113]
	v_pk_mul_f32 v[120:121], v[124:125], v[120:121]
	v_pk_mul_f32 v[122:123], v[122:123], s[42:43] op_sel_hi:[1,0]
	v_pk_mul_f32 v[124:125], v[110:111], v[120:121]
	v_pk_fma_f32 v[146:147], v[110:111], v[120:121], v[110:111] neg_lo:[1,0,0] neg_hi:[1,0,0]
	v_pk_fma_f32 v[120:121], v[126:127], s[30:31], v[118:119] op_sel_hi:[1,0,0]
	v_exp_f32_e32 v122, v122
	v_pk_fma_f32 v[120:121], v[126:127], v[120:121], s[36:37] op_sel_hi:[1,1,0]
	v_exp_f32_e32 v123, v123
	v_pk_fma_f32 v[120:121], v[126:127], v[120:121], s[38:39] op_sel_hi:[1,1,0]
	v_and_b32_e32 v128, 0x7fffffff, v108
	v_pk_fma_f32 v[120:121], v[126:127], v[120:121], s[40:41] op_sel_hi:[1,1,0]
	v_pk_fma_f32 v[128:129], v[128:129], s[28:29], 1.0 op_sel_hi:[1,0,0]
	v_pk_mul_f32 v[120:121], v[126:127], v[120:121]
	v_and_b32_e32 v127, 0x7fffffff, v107
	v_and_b32_e32 v126, 0x7fffffff, v106
	v_pk_fma_f32 v[126:127], v[126:127], s[28:29], 1.0 op_sel_hi:[1,0,0]
	v_pk_mul_f32 v[120:121], v[122:123], v[120:121]
	v_rcp_f32_e32 v126, v126
	v_rcp_f32_e32 v127, v127
	v_pk_mul_f32 v[122:123], v[106:107], v[106:107]
	v_pk_mul_f32 v[148:149], v[112:113], v[120:121]
	v_pk_fma_f32 v[150:151], v[112:113], v[120:121], v[112:113] neg_lo:[1,0,0] neg_hi:[1,0,0]
	v_pk_fma_f32 v[120:121], v[126:127], s[30:31], v[118:119] op_sel_hi:[1,0,0]
	v_pk_mul_f32 v[122:123], v[122:123], s[42:43] op_sel_hi:[1,0]
	v_pk_fma_f32 v[120:121], v[126:127], v[120:121], s[36:37] op_sel_hi:[1,1,0]
	v_exp_f32_e32 v122, v122
	v_exp_f32_e32 v123, v123
	v_pk_fma_f32 v[120:121], v[126:127], v[120:121], s[38:39] op_sel_hi:[1,1,0]
	v_rcp_f32_e32 v128, v128
	v_pk_fma_f32 v[120:121], v[126:127], v[120:121], s[40:41] op_sel_hi:[1,1,0]
	v_rcp_f32_e32 v129, v129
	v_pk_mul_f32 v[120:121], v[126:127], v[120:121]
	v_cmp_gt_f32_e32 vcc, 0, v107
	v_pk_mul_f32 v[120:121], v[122:123], v[120:121]
	v_pk_mul_f32 v[126:127], v[108:109], v[108:109]
	v_pk_mul_f32 v[122:123], v[106:107], v[120:121]
	v_pk_fma_f32 v[120:121], v[106:107], v[120:121], v[106:107] neg_lo:[1,0,0] neg_hi:[1,0,0]
	v_pk_mul_f32 v[152:153], v[102:103], v[102:103]
	v_cndmask_b32_e32 v107, v121, v123, vcc
	v_cmp_gt_f32_e32 vcc, 0, v106
	v_pk_mul_f32 v[152:153], v[152:153], s[42:43] op_sel_hi:[1,0]
	v_and_b32_e32 v155, 0x7fffffff, v105
	v_cndmask_b32_e32 v106, v120, v122, vcc
	v_pk_fma_f32 v[120:121], v[128:129], s[30:31], v[118:119] op_sel_hi:[1,0,0]
	v_pk_mul_f32 v[122:123], v[126:127], s[42:43] op_sel_hi:[1,0]
	v_pk_fma_f32 v[120:121], v[128:129], v[120:121], s[36:37] op_sel_hi:[1,1,0]
	v_exp_f32_e32 v122, v122
	v_exp_f32_e32 v123, v123
	v_pk_fma_f32 v[120:121], v[128:129], v[120:121], s[38:39] op_sel_hi:[1,1,0]
	v_and_b32_e32 v154, 0x7fffffff, v104
	v_pk_fma_f32 v[120:121], v[128:129], v[120:121], s[40:41] op_sel_hi:[1,1,0]
	v_exp_f32_e32 v152, v152
	v_pk_mul_f32 v[120:121], v[128:129], v[120:121]
	v_exp_f32_e32 v153, v153
	v_pk_mul_f32 v[120:121], v[122:123], v[120:121]
	v_pk_fma_f32 v[154:155], v[154:155], s[28:29], 1.0 op_sel_hi:[1,0,0]
	v_pk_mul_f32 v[126:127], v[108:109], v[120:121]
	v_pk_fma_f32 v[128:129], v[108:109], v[120:121], v[108:109] neg_lo:[1,0,0] neg_hi:[1,0,0]
	v_and_b32_e32 v121, 0x7fffffff, v103
	v_and_b32_e32 v120, 0x7fffffff, v102
	v_pk_fma_f32 v[120:121], v[120:121], s[28:29], 1.0 op_sel_hi:[1,0,0]
	v_rcp_f32_e32 v154, v154
	v_rcp_f32_e32 v120, v120
	v_rcp_f32_e32 v121, v121
	v_rcp_f32_e32 v155, v155
	v_cmp_gt_f32_e32 vcc, 0, v108
	v_or_b32_e32 v114, 16, v142
	v_pk_fma_f32 v[122:123], v[120:121], s[30:31], v[118:119] op_sel_hi:[1,0,0]
	v_cndmask_b32_e32 v108, v128, v126, vcc
	v_pk_fma_f32 v[122:123], v[120:121], v[122:123], s[36:37] op_sel_hi:[1,1,0]
	v_cmp_gt_f32_e32 vcc, 0, v104
	v_pk_fma_f32 v[122:123], v[120:121], v[122:123], s[38:39] op_sel_hi:[1,1,0]
	v_ashrrev_i32_e32 v115, 31, v114
	v_pk_fma_f32 v[122:123], v[120:121], v[122:123], s[40:41] op_sel_hi:[1,1,0]
	v_lshlrev_b64 v[116:117], 11, v[114:115]
	v_pk_mul_f32 v[120:121], v[120:121], v[122:123]
	v_pk_mul_f32 v[122:123], v[104:105], v[104:105]
	v_pk_mul_f32 v[120:121], v[152:153], v[120:121]
	v_pk_mul_f32 v[122:123], v[122:123], s[42:43] op_sel_hi:[1,0]
	v_pk_mul_f32 v[152:153], v[102:103], v[120:121]
	v_pk_fma_f32 v[170:171], v[102:103], v[120:121], v[102:103] neg_lo:[1,0,0] neg_hi:[1,0,0]
	v_pk_fma_f32 v[120:121], v[154:155], s[30:31], v[118:119] op_sel_hi:[1,0,0]
	v_exp_f32_e32 v122, v122
	v_pk_fma_f32 v[120:121], v[154:155], v[120:121], s[36:37] op_sel_hi:[1,1,0]
	v_exp_f32_e32 v123, v123
	v_pk_fma_f32 v[120:121], v[154:155], v[120:121], s[38:39] op_sel_hi:[1,1,0]
	v_lshl_add_u64 v[116:117], v[144:145], 0, v[116:117]
; __device__ __forceinline__ unsigned cvt_pk_bf16(float lo, float hi) { f32x2 v = {lo, hi}; bf16x2_t b = __builtin_convertvector(v, bf16x2_t); return __builtin_bit_cast(unsigned, b); }
; __device__ __forceinline__ f32x2 gelu_pk(f32x2 v) {
;     const f32x2 av = __builtin_elementwise_abs(v), d = av * 0.2316418882f + 1.0f;
;     f32x2 t; t.x = __builtin_amdgcn_rcpf(d.x); t.y = __builtin_amdgcn_rcpf(d.y);
;     f32x2 q = t * 0.5307027145f + (-0.7265760135f); q = q * t + 0.7107068705f; q = q * t + (-0.142248368f); q = q * t + 0.127414796f; q = q * t;
;     const f32x2 s = (v * v) * (-0.72134752044f);
;     f32x2 e; e.x = __builtin_amdgcn_exp2f(s.x); e.y = __builtin_amdgcn_exp2f(s.y);
;     const f32x2 m = v * (q * e), r = v - m;
;     f32x2 o; o.x = v.x < 0.f ? m.x : r.x; o.y = v.y < 0.f ? m.y : r.y; return o;
; }
; __device__ __forceinline__ f32x4 gelu4(f32x4 v) { f32x2 a = gelu_pk((f32x2){v[0], v[1]}), b = gelu_pk((f32x2){v[2], v[3]}); return (f32x4){a.x, a.y, b.x, b.y}; }
;     __device__ __forceinline__ void operator()(const AccT& acc, const pg8::Unit& u, int wr, int wc, int fr, int fq) const {
;     ...
;                 for (int m = 0; m < 4; ++m) { const int row = row0 + ai * 128 + m * 16; float s = 0.f, q = 0.f;
; #pragma unroll
;                     for (int bj = 0; bj < 2; ++bj) { const f32x4 v0 = gelu4(acc[ai][bj][m][0]), v1 = gelu4(acc[ai][bj][m][1]);
;                         s += (v0[0] + v0[1]) + (v0[2] + v0[3]) + (v1[0] + v1[1]) + (v1[2] + v1[3]);
;                         q += (v0[0] * v0[0] + v0[1] * v0[1]) + (v0[2] * v0[2] + v0[3] * v0[3]) + (v1[0] * v1[0] + v1[1] * v1[1]) + (v1[2] * v1[2] + v1[3] * v1[3]);
;                         u32x4 w; w.x = cvt_pk_bf16(v0[0], v0[1]); w.y = cvt_pk_bf16(v0[2], v0[3]); w.z = cvt_pk_bf16(v1[0], v1[1]); w.w = cvt_pk_bf16(v1[2], v1[3]);
;                         *(u32x4*)(dst + (size_t)row * GW + col0 + bj * 128) = w; }
;                     if (pn >= 4) { s += __shfl_xor(s, 16); s += __shfl_xor(s, 32); q += __shfl_xor(q, 16); q += __shfl_xor(q, 32);
;                         if (fq == 0) *(f32x2*)(vstat + (size_t)row * 32 + ((pn - 4) * 4 + wc) * 2) = (f32x2){s, q}; } }
	v_pk_fma_f32 v[120:121], v[154:155], v[120:121], s[40:41] op_sel_hi:[1,1,0]
	v_cvt_pk_bf16_f32 v128, v106, v107
	v_pk_mul_f32 v[120:121], v[154:155], v[120:121]
	s_nop 0
	v_pk_mul_f32 v[120:121], v[122:123], v[120:121]
	s_nop 0
	v_pk_mul_f32 v[122:123], v[104:105], v[120:121]
	v_pk_fma_f32 v[154:155], v[104:105], v[120:121], v[104:105] neg_lo:[1,0,0] neg_hi:[1,0,0]
	v_and_b32_e32 v121, 0x7fffffff, v99
	v_and_b32_e32 v120, 0x7fffffff, v98
	v_pk_fma_f32 v[120:121], v[120:121], s[28:29], 1.0 op_sel_hi:[1,0,0]
	v_cndmask_b32_e64 v104, 0, 1, s[54:55]
	v_rcp_f32_e32 v172, v120
	v_rcp_f32_e32 v173, v121
	v_cndmask_b32_e32 v121, v154, v122, vcc
	v_cmp_gt_f32_e32 vcc, 0, v105
	v_cmp_ne_u32_e64 s[10:11], 1, v104
	s_nop 0
	v_cndmask_b32_e32 v105, v155, v123, vcc
	v_pk_mul_f32 v[154:155], v[98:99], v[98:99]
	v_pk_fma_f32 v[122:123], v[172:173], s[30:31], v[118:119] op_sel_hi:[1,0,0]
	v_pk_mul_f32 v[154:155], v[154:155], s[42:43] op_sel_hi:[1,0]
	v_pk_fma_f32 v[122:123], v[172:173], v[122:123], s[36:37] op_sel_hi:[1,1,0]
	v_exp_f32_e32 v154, v154
	v_exp_f32_e32 v155, v155
	v_pk_fma_f32 v[122:123], v[172:173], v[122:123], s[38:39] op_sel_hi:[1,1,0]
	v_cmp_gt_f32_e32 vcc, 0, v110
	v_pk_fma_f32 v[122:123], v[172:173], v[122:123], s[40:41] op_sel_hi:[1,1,0]
	s_nop 0
	v_pk_mul_f32 v[122:123], v[172:173], v[122:123]
	v_pk_mul_f32 v[172:173], v[100:101], v[100:101]
	v_pk_mul_f32 v[122:123], v[154:155], v[122:123]
	s_nop 0
	v_pk_mul_f32 v[154:155], v[98:99], v[122:123]
	v_pk_fma_f32 v[174:175], v[98:99], v[122:123], v[98:99] neg_lo:[1,0,0] neg_hi:[1,0,0]
	v_cndmask_b32_e32 v122, v146, v124, vcc
	v_cmp_gt_f32_e32 vcc, 0, v102
	v_and_b32_e32 v146, 0x7fffffff, v100
	s_nop 0
	v_cndmask_b32_e32 v123, v170, v152, vcc
	v_cmp_gt_f32_e32 vcc, 0, v111
	s_nop 1
	v_cndmask_b32_e32 v124, v147, v125, vcc
	v_cmp_gt_f32_e32 vcc, 0, v112
	v_and_b32_e32 v147, 0x7fffffff, v101
	v_pk_fma_f32 v[146:147], v[146:147], s[28:29], 1.0 op_sel_hi:[1,0,0]
	v_cndmask_b32_e32 v110, v150, v148, vcc
	v_cmp_gt_f32_e32 vcc, 0, v103
	v_rcp_f32_e32 v146, v146
	v_rcp_f32_e32 v147, v147
	v_cndmask_b32_e32 v111, v171, v153, vcc
	v_cmp_gt_f32_e32 vcc, 0, v113
	v_cvt_pk_bf16_f32 v126, v122, v124
	v_pk_fma_f32 v[118:119], v[146:147], s[30:31], v[118:119] op_sel_hi:[1,0,0]
	v_cndmask_b32_e32 v112, v151, v149, vcc
	v_cmp_gt_f32_e32 vcc, 0, v98
	v_pk_fma_f32 v[118:119], v[146:147], v[118:119], s[36:37] op_sel_hi:[1,1,0]
	s_nop 0
	v_cndmask_b32_e32 v102, v174, v154, vcc
	v_cmp_gt_f32_e32 vcc, 0, v109
	v_pk_fma_f32 v[118:119], v[146:147], v[118:119], s[38:39] op_sel_hi:[1,1,0]
	s_nop 0
	v_cndmask_b32_e32 v103, v129, v127, vcc
	v_cvt_pk_bf16_f32 v127, v110, v112
	v_cvt_pk_bf16_f32 v129, v108, v103
	global_store_dwordx4 v[116:117], v[126:129], off nt
	v_pk_fma_f32 v[118:119], v[146:147], v[118:119], s[40:41] op_sel_hi:[1,1,0]
	v_cmp_gt_f32_e32 vcc, 0, v99
	v_pk_mul_f32 v[126:127], v[172:173], s[42:43] op_sel_hi:[1,0]
	v_pk_mul_f32 v[118:119], v[146:147], v[118:119]
	v_exp_f32_e32 v126, v126
	v_exp_f32_e32 v127, v127
	v_cndmask_b32_e32 v98, v175, v155, vcc
	v_cmp_gt_f32_e32 vcc, 0, v101
	v_cvt_pk_bf16_f32 v128, v102, v98
	v_pk_mul_f32 v[118:119], v[126:127], v[118:119]
	s_nop 0
	v_pk_mul_f32 v[126:127], v[100:101], v[118:119]
	v_pk_fma_f32 v[118:119], v[100:101], v[118:119], v[100:101] neg_lo:[1,0,0] neg_hi:[1,0,0]
	s_nop 0
	v_cndmask_b32_e32 v101, v119, v127, vcc
	v_cmp_gt_f32_e32 vcc, 0, v100
	v_cvt_pk_bf16_f32 v127, v121, v105
	s_nop 0
	v_cndmask_b32_e32 v100, v118, v126, vcc
	v_cvt_pk_bf16_f32 v126, v123, v111
	v_cvt_pk_bf16_f32 v129, v100, v101
	s_andn2_b64 vcc, exec, s[54:55]
	global_store_dwordx4 v[116:117], v[126:129], off offset:256 nt
	s_cbranch_vccnz .LBB0_254
	v_mov_b32_e32 v125, v123
	v_mov_b32_e32 v99, v103
	v_mov_b32_e32 v113, v111
	v_pk_add_f32 v[116:117], v[102:103], v[98:99]
	v_pk_mul_f32 v[118:119], v[102:103], v[98:99]
	v_mov_b32_e32 v126, v124
	v_pk_add_f32 v[146:147], v[122:123], v[124:125]
	v_pk_mul_f32 v[124:125], v[122:123], v[124:125]
	v_mov_b32_e32 v117, v119
	v_mov_b32_e32 v119, v110
	v_mov_b32_e32 v127, v112
	v_mov_b32_e32 v147, v125
	v_pk_add_f32 v[124:125], v[110:111], v[112:113]
	v_pk_mul_f32 v[112:113], v[110:111], v[112:113]
	v_and_b32_e32 v110, 64, v169
	v_xor_b32_e32 v109, 16, v169
	v_add_u32_e32 v110, 64, v110
	v_mov_b32_e32 v118, v122
	v_pk_mul_f32 v[126:127], v[126:127], v[126:127]
	v_mul_f32_e32 v104, v106, v106
	v_cmp_lt_i32_e32 vcc, v109, v110
	v_pk_fma_f32 v[118:119], v[118:119], v[118:119], v[126:127]
	v_pk_fma_f32 v[126:127], v[106:107], v[106:107], v[104:105] op_sel_hi:[1,1,0]
	v_mul_f32_e32 v104, v100, v100
	v_mov_b32_e32 v125, v113
	v_mul_f32_e32 v113, v121, v121
	v_mul_f32_e32 v149, v105, v105
	v_pk_mul_f32 v[150:151], v[102:103], v[102:103]
	v_pk_mul_f32 v[98:99], v[98:99], v[98:99]
	v_cndmask_b32_e32 v109, v169, v109, vcc
	v_mov_b32_e32 v112, v106
	v_mov_b32_e32 v148, v107
	v_pk_fma_f32 v[128:129], v[100:101], v[100:101], v[104:105] op_sel_hi:[1,1,0]
	v_mov_b32_e32 v120, v123
	v_mov_b32_e32 v104, v111
	v_lshlrev_b32_e32 v111, 2, v109
	v_mov_b32_e32 v109, v150
	v_pk_mov_b32 v[98:99], v[102:103], v[98:99] op_sel:[1,0]
	v_pk_add_f32 v[102:103], v[146:147], v[124:125]
	v_pk_add_f32 v[106:107], v[112:113], v[148:149]
	v_pk_add_f32 v[104:105], v[120:121], v[104:105]
	v_pk_add_f32 v[98:99], v[108:109], v[98:99]
	v_pk_add_f32 v[102:103], v[102:103], v[106:107]
	v_mul_f32_e32 v130, v108, v108
	v_pk_add_f32 v[118:119], v[118:119], v[118:119] op_sel_hi:[0,1]
	v_pk_add_f32 v[98:99], v[102:103], v[98:99]
	v_pk_add_f32 v[102:103], v[104:105], v[104:105] op_sel:[0,1] op_sel_hi:[1,0]
	v_mov_b32_e32 v118, v100
	v_mov_b32_e32 v126, v101
	v_mov_b32_e32 v103, v130
	v_mov_b32_e32 v128, v131
	v_pk_add_f32 v[100:101], v[118:119], v[126:127]
	v_pk_add_f32 v[102:103], v[102:103], v[116:117]
	v_pk_add_f32 v[98:99], v[98:99], v[128:129]
	v_pk_add_f32 v[100:101], v[102:103], v[100:101]
	v_xor_b32_e32 v102, 32, v169
	v_pk_add_f32 v[98:99], v[100:101], v[98:99]
	ds_bpermute_b32 v100, v111, v98
	ds_bpermute_b32 v101, v111, v99
	v_cmp_lt_i32_e32 vcc, v102, v110
	s_waitcnt lgkmcnt(0)
	v_pk_add_f32 v[98:99], v[98:99], v[100:101]
	v_cndmask_b32_e32 v102, v169, v102, vcc
	v_lshlrev_b32_e32 v102, 2, v102
	ds_bpermute_b32 v100, v102, v98
	ds_bpermute_b32 v101, v102, v99
	s_and_saveexec_b64 s[0:1], s[6:7]
	s_cbranch_execz .LBB0_253
	s_waitcnt lgkmcnt(0)
	v_pk_add_f32 v[98:99], v[98:99], v[100:101]
	v_lshlrev_b64 v[100:101], 7, v[114:115]
	v_lshl_add_u64 v[100:101], s[12:13], 0, v[100:101]
	global_store_dwordx2 v[100:101], v[98:99], off nt

; __device__ __forceinline__ unsigned cvt_pk_bf16(float lo, float hi) { f32x2 v = {lo, hi}; bf16x2_t b = __builtin_convertvector(v, bf16x2_t); return __builtin_bit_cast(unsigned, b); }
; __device__ __forceinline__ f32x2 gelu_pk(f32x2 v) {
;     const f32x2 av = __builtin_elementwise_abs(v), d = av * 0.2316418882f + 1.0f;
;     f32x2 t; t.x = __builtin_amdgcn_rcpf(d.x); t.y = __builtin_amdgcn_rcpf(d.y);
;     f32x2 q = t * 0.5307027145f + (-0.7265760135f); q = q * t + 0.7107068705f; q = q * t + (-0.142248368f); q = q * t + 0.127414796f; q = q * t;
;     const f32x2 s = (v * v) * (-0.72134752044f);
;     f32x2 e; e.x = __builtin_amdgcn_exp2f(s.x); e.y = __builtin_amdgcn_exp2f(s.y);
;     const f32x2 m = v * (q * e), r = v - m;
;     f32x2 o; o.x = v.x < 0.f ? m.x : r.x; o.y = v.y < 0.f ? m.y : r.y; return o;
; }
; __device__ __forceinline__ f32x4 gelu4(f32x4 v) { f32x2 a = gelu_pk((f32x2){v[0], v[1]}), b = gelu_pk((f32x2){v[2], v[3]}); return (f32x4){a.x, a.y, b.x, b.y}; }
;     __device__ __forceinline__ void operator()(const AccT& acc, const pg8::Unit& u, int wr, int wc, int fr, int fq) const {
;     ...
;                 for (int m = 0; m < 4; ++m) { const int row = row0 + ai * 128 + m * 16; float s = 0.f, q = 0.f;
; #pragma unroll
;                     for (int bj = 0; bj < 2; ++bj) { const f32x4 v0 = gelu4(acc[ai][bj][m][0]), v1 = gelu4(acc[ai][bj][m][1]);
;                         s += (v0[0] + v0[1]) + (v0[2] + v0[3]) + (v1[0] + v1[1]) + (v1[2] + v1[3]);
;                         q += (v0[0] * v0[0] + v0[1] * v0[1]) + (v0[2] * v0[2] + v0[3] * v0[3]) + (v1[0] * v1[0] + v1[1] * v1[1]) + (v1[2] * v1[2] + v1[3] * v1[3]);
;                         u32x4 w; w.x = cvt_pk_bf16(v0[0], v0[1]); w.y = cvt_pk_bf16(v0[2], v0[3]); w.z = cvt_pk_bf16(v1[0], v1[1]); w.w = cvt_pk_bf16(v1[2], v1[3]);
;                         *(u32x4*)(dst + (size_t)row * GW + col0 + bj * 128) = w; }
.LBB0_254:
	s_waitcnt lgkmcnt(0)
	v_and_b32_e32 v101, 0x7fffffff, v95
	v_and_b32_e32 v100, 0x7fffffff, v94
	v_pk_fma_f32 v[100:101], v[100:101], s[28:29], 1.0 op_sel_hi:[1,0,0]
	v_mov_b64_e32 v[102:103], s[34:35]
	v_rcp_f32_e32 v104, v100
	v_rcp_f32_e32 v105, v101
	v_pk_mul_f32 v[108:109], v[94:95], v[94:95]
	v_and_b32_e32 v111, 0x7fffffff, v97
	v_pk_mul_f32 v[108:109], v[108:109], s[42:43] op_sel_hi:[1,0]
	v_pk_fma_f32 v[106:107], v[104:105], s[30:31], v[102:103] op_sel_hi:[1,0,0]
	v_and_b32_e32 v110, 0x7fffffff, v96
	v_pk_fma_f32 v[106:107], v[104:105], v[106:107], s[36:37] op_sel_hi:[1,1,0]
	v_exp_f32_e32 v108, v108
	v_exp_f32_e32 v109, v109
	v_pk_fma_f32 v[110:111], v[110:111], s[28:29], 1.0 op_sel_hi:[1,0,0]
	v_pk_fma_f32 v[106:107], v[104:105], v[106:107], s[38:39] op_sel_hi:[1,1,0]
	v_rcp_f32_e32 v110, v110
	v_rcp_f32_e32 v111, v111
	v_pk_fma_f32 v[106:107], v[104:105], v[106:107], s[40:41] op_sel_hi:[1,1,0]
	v_and_b32_e32 v113, 0x7fffffff, v93
	v_pk_mul_f32 v[104:105], v[104:105], v[106:107]
	v_pk_mul_f32 v[106:107], v[96:97], v[96:97]
	v_pk_mul_f32 v[104:105], v[108:109], v[104:105]
	v_pk_mul_f32 v[106:107], v[106:107], s[42:43] op_sel_hi:[1,0]
	v_pk_mul_f32 v[108:109], v[94:95], v[104:105]
	v_pk_fma_f32 v[114:115], v[94:95], v[104:105], v[94:95] neg_lo:[1,0,0] neg_hi:[1,0,0]
	v_pk_fma_f32 v[104:105], v[110:111], s[30:31], v[102:103] op_sel_hi:[1,0,0]
	v_exp_f32_e32 v106, v106
	v_pk_fma_f32 v[104:105], v[110:111], v[104:105], s[36:37] op_sel_hi:[1,1,0]
	v_exp_f32_e32 v107, v107
	v_pk_fma_f32 v[104:105], v[110:111], v[104:105], s[38:39] op_sel_hi:[1,1,0]
	v_and_b32_e32 v112, 0x7fffffff, v92
	v_pk_fma_f32 v[104:105], v[110:111], v[104:105], s[40:41] op_sel_hi:[1,1,0]
	v_pk_fma_f32 v[112:113], v[112:113], s[28:29], 1.0 op_sel_hi:[1,0,0]
	v_pk_mul_f32 v[104:105], v[110:111], v[104:105]
	v_and_b32_e32 v111, 0x7fffffff, v91
	v_and_b32_e32 v110, 0x7fffffff, v90
	v_pk_fma_f32 v[110:111], v[110:111], s[28:29], 1.0 op_sel_hi:[1,0,0]
	v_pk_mul_f32 v[104:105], v[106:107], v[104:105]
	v_rcp_f32_e32 v110, v110
	v_rcp_f32_e32 v111, v111
	v_pk_mul_f32 v[106:107], v[90:91], v[90:91]
	v_pk_mul_f32 v[116:117], v[96:97], v[104:105]
	v_pk_fma_f32 v[118:119], v[96:97], v[104:105], v[96:97] neg_lo:[1,0,0] neg_hi:[1,0,0]
	v_pk_fma_f32 v[104:105], v[110:111], s[30:31], v[102:103] op_sel_hi:[1,0,0]
	v_pk_mul_f32 v[106:107], v[106:107], s[42:43] op_sel_hi:[1,0]
	v_pk_fma_f32 v[104:105], v[110:111], v[104:105], s[36:37] op_sel_hi:[1,1,0]
	v_exp_f32_e32 v106, v106
	v_exp_f32_e32 v107, v107
	v_pk_fma_f32 v[104:105], v[110:111], v[104:105], s[38:39] op_sel_hi:[1,1,0]
	v_rcp_f32_e32 v112, v112
	v_pk_fma_f32 v[104:105], v[110:111], v[104:105], s[40:41] op_sel_hi:[1,1,0]
	v_rcp_f32_e32 v113, v113
	v_pk_mul_f32 v[104:105], v[110:111], v[104:105]
	v_cmp_gt_f32_e32 vcc, 0, v91
	v_pk_mul_f32 v[104:105], v[106:107], v[104:105]
	v_pk_mul_f32 v[110:111], v[92:93], v[92:93]
	v_pk_mul_f32 v[106:107], v[90:91], v[104:105]
	v_pk_fma_f32 v[104:105], v[90:91], v[104:105], v[90:91] neg_lo:[1,0,0] neg_hi:[1,0,0]
	v_pk_mul_f32 v[120:121], v[86:87], v[86:87]
	v_cndmask_b32_e32 v91, v105, v107, vcc
	v_cmp_gt_f32_e32 vcc, 0, v90
	v_pk_mul_f32 v[120:121], v[120:121], s[42:43] op_sel_hi:[1,0]
	v_and_b32_e32 v123, 0x7fffffff, v89
	v_cndmask_b32_e32 v90, v104, v106, vcc
	v_pk_fma_f32 v[104:105], v[112:113], s[30:31], v[102:103] op_sel_hi:[1,0,0]
	v_pk_mul_f32 v[106:107], v[110:111], s[42:43] op_sel_hi:[1,0]
	v_pk_fma_f32 v[104:105], v[112:113], v[104:105], s[36:37] op_sel_hi:[1,1,0]
	v_exp_f32_e32 v106, v106
	v_exp_f32_e32 v107, v107
	v_pk_fma_f32 v[104:105], v[112:113], v[104:105], s[38:39] op_sel_hi:[1,1,0]
	v_and_b32_e32 v122, 0x7fffffff, v88
	v_pk_fma_f32 v[104:105], v[112:113], v[104:105], s[40:41] op_sel_hi:[1,1,0]
	v_exp_f32_e32 v120, v120
	v_pk_mul_f32 v[104:105], v[112:113], v[104:105]
	v_exp_f32_e32 v121, v121
	v_pk_mul_f32 v[104:105], v[106:107], v[104:105]
	v_pk_fma_f32 v[122:123], v[122:123], s[28:29], 1.0 op_sel_hi:[1,0,0]
	v_pk_mul_f32 v[110:111], v[92:93], v[104:105]
	v_pk_fma_f32 v[112:113], v[92:93], v[104:105], v[92:93] neg_lo:[1,0,0] neg_hi:[1,0,0]
	v_and_b32_e32 v105, 0x7fffffff, v87
	v_and_b32_e32 v104, 0x7fffffff, v86
	v_pk_fma_f32 v[104:105], v[104:105], s[28:29], 1.0 op_sel_hi:[1,0,0]
	v_rcp_f32_e32 v122, v122
	v_rcp_f32_e32 v104, v104
	v_rcp_f32_e32 v105, v105
	v_rcp_f32_e32 v123, v123
	v_cmp_gt_f32_e32 vcc, 0, v92
	v_or_b32_e32 v98, 32, v142
	v_pk_fma_f32 v[106:107], v[104:105], s[30:31], v[102:103] op_sel_hi:[1,0,0]
	v_cndmask_b32_e32 v92, v112, v110, vcc
	v_pk_fma_f32 v[106:107], v[104:105], v[106:107], s[36:37] op_sel_hi:[1,1,0]
	v_cmp_gt_f32_e32 vcc, 0, v88
	v_pk_fma_f32 v[106:107], v[104:105], v[106:107], s[38:39] op_sel_hi:[1,1,0]
	v_ashrrev_i32_e32 v99, 31, v98
	v_pk_fma_f32 v[106:107], v[104:105], v[106:107], s[40:41] op_sel_hi:[1,1,0]
	v_lshlrev_b64 v[100:101], 11, v[98:99]
	v_pk_mul_f32 v[104:105], v[104:105], v[106:107]
	v_pk_mul_f32 v[106:107], v[88:89], v[88:89]
	v_pk_mul_f32 v[104:105], v[120:121], v[104:105]
	v_pk_mul_f32 v[106:107], v[106:107], s[42:43] op_sel_hi:[1,0]
	v_pk_mul_f32 v[120:121], v[86:87], v[104:105]
	v_pk_fma_f32 v[124:125], v[86:87], v[104:105], v[86:87] neg_lo:[1,0,0] neg_hi:[1,0,0]
	v_pk_fma_f32 v[104:105], v[122:123], s[30:31], v[102:103] op_sel_hi:[1,0,0]
	v_exp_f32_e32 v106, v106
	v_pk_fma_f32 v[104:105], v[122:123], v[104:105], s[36:37] op_sel_hi:[1,1,0]
	v_exp_f32_e32 v107, v107
	v_pk_fma_f32 v[104:105], v[122:123], v[104:105], s[38:39] op_sel_hi:[1,1,0]
	v_lshl_add_u64 v[100:101], v[144:145], 0, v[100:101]
	v_pk_fma_f32 v[104:105], v[122:123], v[104:105], s[40:41] op_sel_hi:[1,1,0]
	v_cvt_pk_bf16_f32 v112, v90, v91
; __device__ __forceinline__ unsigned cvt_pk_bf16(float lo, float hi) { f32x2 v = {lo, hi}; bf16x2_t b = __builtin_convertvector(v, bf16x2_t); return __builtin_bit_cast(unsigned, b); }
; __device__ __forceinline__ f32x2 gelu_pk(f32x2 v) {
;     const f32x2 av = __builtin_elementwise_abs(v), d = av * 0.2316418882f + 1.0f;
;     f32x2 t; t.x = __builtin_amdgcn_rcpf(d.x); t.y = __builtin_amdgcn_rcpf(d.y);
;     f32x2 q = t * 0.5307027145f + (-0.7265760135f); q = q * t + 0.7107068705f; q = q * t + (-0.142248368f); q = q * t + 0.127414796f; q = q * t;
;     const f32x2 s = (v * v) * (-0.72134752044f);
;     f32x2 e; e.x = __builtin_amdgcn_exp2f(s.x); e.y = __builtin_amdgcn_exp2f(s.y);
;     const f32x2 m = v * (q * e), r = v - m;
;     f32x2 o; o.x = v.x < 0.f ? m.x : r.x; o.y = v.y < 0.f ? m.y : r.y; return o;
; }
; __device__ __forceinline__ f32x4 gelu4(f32x4 v) { f32x2 a = gelu_pk((f32x2){v[0], v[1]}), b = gelu_pk((f32x2){v[2], v[3]}); return (f32x4){a.x, a.y, b.x, b.y}; }
;     __device__ __forceinline__ void operator()(const AccT& acc, const pg8::Unit& u, int wr, int wc, int fr, int fq) const {
;     ...
;                 for (int m = 0; m < 4; ++m) { const int row = row0 + ai * 128 + m * 16; float s = 0.f, q = 0.f;
; #pragma unroll
;                     for (int bj = 0; bj < 2; ++bj) { const f32x4 v0 = gelu4(acc[ai][bj][m][0]), v1 = gelu4(acc[ai][bj][m][1]);
;                         s += (v0[0] + v0[1]) + (v0[2] + v0[3]) + (v1[0] + v1[1]) + (v1[2] + v1[3]);
;                         q += (v0[0] * v0[0] + v0[1] * v0[1]) + (v0[2] * v0[2] + v0[3] * v0[3]) + (v1[0] * v1[0] + v1[1] * v1[1]) + (v1[2] * v1[2] + v1[3] * v1[3]);
;                         u32x4 w; w.x = cvt_pk_bf16(v0[0], v0[1]); w.y = cvt_pk_bf16(v0[2], v0[3]); w.z = cvt_pk_bf16(v1[0], v1[1]); w.w = cvt_pk_bf16(v1[2], v1[3]);
;                         *(u32x4*)(dst + (size_t)row * GW + col0 + bj * 128) = w; }
;                     if (pn >= 4) { s += __shfl_xor(s, 16); s += __shfl_xor(s, 32); q += __shfl_xor(q, 16); q += __shfl_xor(q, 32);
;                         if (fq == 0) *(f32x2*)(vstat + (size_t)row * 32 + ((pn - 4) * 4 + wc) * 2) = (f32x2){s, q}; } }
	v_pk_mul_f32 v[104:105], v[122:123], v[104:105]
	s_nop 0
	v_pk_mul_f32 v[104:105], v[106:107], v[104:105]
	s_nop 0
	v_pk_mul_f32 v[106:107], v[88:89], v[104:105]
	v_pk_fma_f32 v[122:123], v[88:89], v[104:105], v[88:89] neg_lo:[1,0,0] neg_hi:[1,0,0]
	v_and_b32_e32 v105, 0x7fffffff, v83
	v_and_b32_e32 v104, 0x7fffffff, v82
	v_pk_fma_f32 v[104:105], v[104:105], s[28:29], 1.0 op_sel_hi:[1,0,0]
	s_nop 0
	v_rcp_f32_e32 v126, v104
	v_rcp_f32_e32 v127, v105
	v_cndmask_b32_e32 v105, v122, v106, vcc
	v_cmp_gt_f32_e32 vcc, 0, v89
	s_nop 1
	v_cndmask_b32_e32 v89, v123, v107, vcc
	v_pk_mul_f32 v[122:123], v[82:83], v[82:83]
	v_pk_fma_f32 v[106:107], v[126:127], s[30:31], v[102:103] op_sel_hi:[1,0,0]
	v_pk_mul_f32 v[122:123], v[122:123], s[42:43] op_sel_hi:[1,0]
	v_pk_fma_f32 v[106:107], v[126:127], v[106:107], s[36:37] op_sel_hi:[1,1,0]
	v_exp_f32_e32 v122, v122
	v_exp_f32_e32 v123, v123
	v_pk_fma_f32 v[106:107], v[126:127], v[106:107], s[38:39] op_sel_hi:[1,1,0]
	v_cmp_gt_f32_e32 vcc, 0, v94
	v_pk_fma_f32 v[106:107], v[126:127], v[106:107], s[40:41] op_sel_hi:[1,1,0]
	s_nop 0
	v_pk_mul_f32 v[106:107], v[126:127], v[106:107]
	v_pk_mul_f32 v[126:127], v[84:85], v[84:85]
	v_pk_mul_f32 v[106:107], v[122:123], v[106:107]
	s_nop 0
	v_pk_mul_f32 v[122:123], v[82:83], v[106:107]
	v_pk_fma_f32 v[128:129], v[82:83], v[106:107], v[82:83] neg_lo:[1,0,0] neg_hi:[1,0,0]
	v_cndmask_b32_e32 v106, v114, v108, vcc
	v_cmp_gt_f32_e32 vcc, 0, v86
	v_and_b32_e32 v114, 0x7fffffff, v84
	s_nop 0
	v_cndmask_b32_e32 v107, v124, v120, vcc
	v_cmp_gt_f32_e32 vcc, 0, v95
	s_nop 1
	v_cndmask_b32_e32 v108, v115, v109, vcc
	v_cmp_gt_f32_e32 vcc, 0, v96
	v_and_b32_e32 v115, 0x7fffffff, v85
	v_pk_fma_f32 v[114:115], v[114:115], s[28:29], 1.0 op_sel_hi:[1,0,0]
	v_cndmask_b32_e32 v94, v118, v116, vcc
	v_cmp_gt_f32_e32 vcc, 0, v87
	v_rcp_f32_e32 v114, v114
	v_rcp_f32_e32 v115, v115
	v_cndmask_b32_e32 v95, v125, v121, vcc
	v_cmp_gt_f32_e32 vcc, 0, v97
	v_cvt_pk_bf16_f32 v110, v106, v108
	v_pk_fma_f32 v[102:103], v[114:115], s[30:31], v[102:103] op_sel_hi:[1,0,0]
	v_cndmask_b32_e32 v96, v119, v117, vcc
	v_cmp_gt_f32_e32 vcc, 0, v82
	v_pk_fma_f32 v[102:103], v[114:115], v[102:103], s[36:37] op_sel_hi:[1,1,0]
	s_nop 0
	v_cndmask_b32_e32 v86, v128, v122, vcc
	v_cmp_gt_f32_e32 vcc, 0, v93
	v_pk_fma_f32 v[102:103], v[114:115], v[102:103], s[38:39] op_sel_hi:[1,1,0]
	s_nop 0
	v_cndmask_b32_e32 v87, v113, v111, vcc
	v_cvt_pk_bf16_f32 v111, v94, v96
	v_cvt_pk_bf16_f32 v113, v92, v87
	global_store_dwordx4 v[100:101], v[110:113], off nt
	v_pk_fma_f32 v[102:103], v[114:115], v[102:103], s[40:41] op_sel_hi:[1,1,0]
	v_cmp_gt_f32_e32 vcc, 0, v83
	v_pk_mul_f32 v[110:111], v[126:127], s[42:43] op_sel_hi:[1,0]
	v_pk_mul_f32 v[102:103], v[114:115], v[102:103]
	v_exp_f32_e32 v110, v110
	v_exp_f32_e32 v111, v111
	v_cndmask_b32_e32 v82, v129, v123, vcc
	v_cmp_gt_f32_e32 vcc, 0, v85
	v_cvt_pk_bf16_f32 v112, v86, v82
	v_pk_mul_f32 v[102:103], v[110:111], v[102:103]
	s_nop 0
	v_pk_mul_f32 v[110:111], v[84:85], v[102:103]
	v_pk_fma_f32 v[102:103], v[84:85], v[102:103], v[84:85] neg_lo:[1,0,0] neg_hi:[1,0,0]
	s_nop 0
	v_cndmask_b32_e32 v85, v103, v111, vcc
	v_cmp_gt_f32_e32 vcc, 0, v84
	v_cvt_pk_bf16_f32 v111, v105, v89
	s_nop 0
	v_cndmask_b32_e32 v84, v102, v110, vcc
	v_cvt_pk_bf16_f32 v110, v107, v95
	v_cvt_pk_bf16_f32 v113, v84, v85
	s_and_b64 vcc, exec, s[10:11]
	global_store_dwordx4 v[100:101], v[110:113], off offset:256 nt
	s_cbranch_vccnz .LBB0_258
	v_mov_b32_e32 v109, v107
	v_mov_b32_e32 v83, v87
	v_mov_b32_e32 v97, v95
	v_pk_add_f32 v[100:101], v[86:87], v[82:83]
	v_pk_mul_f32 v[102:103], v[86:87], v[82:83]
	v_mov_b32_e32 v110, v108
	v_pk_add_f32 v[114:115], v[106:107], v[108:109]
	v_pk_mul_f32 v[108:109], v[106:107], v[108:109]
	v_mov_b32_e32 v101, v103
	v_mov_b32_e32 v103, v94
	v_mov_b32_e32 v111, v96
	v_mov_b32_e32 v115, v109
	v_pk_add_f32 v[108:109], v[94:95], v[96:97]
	v_pk_mul_f32 v[96:97], v[94:95], v[96:97]
	v_and_b32_e32 v94, 64, v169
	v_xor_b32_e32 v93, 16, v169
	v_add_u32_e32 v94, 64, v94
	v_mov_b32_e32 v102, v106
	v_pk_mul_f32 v[110:111], v[110:111], v[110:111]
	v_mul_f32_e32 v88, v90, v90
	v_cmp_lt_i32_e32 vcc, v93, v94
	v_pk_fma_f32 v[102:103], v[102:103], v[102:103], v[110:111]
	v_pk_fma_f32 v[110:111], v[90:91], v[90:91], v[88:89] op_sel_hi:[1,1,0]
	v_mul_f32_e32 v88, v84, v84
	v_mov_b32_e32 v109, v97
	v_mul_f32_e32 v97, v105, v105
	v_mul_f32_e32 v117, v89, v89
	v_pk_mul_f32 v[118:119], v[86:87], v[86:87]
	v_pk_mul_f32 v[82:83], v[82:83], v[82:83]
	v_cndmask_b32_e32 v93, v169, v93, vcc
	v_mov_b32_e32 v96, v90
	v_mov_b32_e32 v116, v91
	v_pk_fma_f32 v[112:113], v[84:85], v[84:85], v[88:89] op_sel_hi:[1,1,0]
	v_mov_b32_e32 v104, v107
	v_mov_b32_e32 v88, v95
	v_lshlrev_b32_e32 v95, 2, v93
	v_mov_b32_e32 v93, v118
	v_pk_mov_b32 v[82:83], v[86:87], v[82:83] op_sel:[1,0]
	v_pk_add_f32 v[86:87], v[114:115], v[108:109]
	v_pk_add_f32 v[90:91], v[96:97], v[116:117]
	v_pk_add_f32 v[88:89], v[104:105], v[88:89]
	v_pk_add_f32 v[82:83], v[92:93], v[82:83]
	v_pk_add_f32 v[86:87], v[86:87], v[90:91]
	v_mul_f32_e32 v120, v92, v92
	v_pk_add_f32 v[102:103], v[102:103], v[102:103] op_sel_hi:[0,1]
	v_pk_add_f32 v[82:83], v[86:87], v[82:83]
	v_pk_add_f32 v[86:87], v[88:89], v[88:89] op_sel:[0,1] op_sel_hi:[1,0]
	v_mov_b32_e32 v102, v84
	v_mov_b32_e32 v110, v85
	v_mov_b32_e32 v87, v120
	v_mov_b32_e32 v112, v131
	v_pk_add_f32 v[84:85], v[102:103], v[110:111]
	v_pk_add_f32 v[86:87], v[86:87], v[100:101]
	v_pk_add_f32 v[82:83], v[82:83], v[112:113]
	v_pk_add_f32 v[84:85], v[86:87], v[84:85]
	v_xor_b32_e32 v86, 32, v169
	v_pk_add_f32 v[82:83], v[84:85], v[82:83]
	ds_bpermute_b32 v84, v95, v82
	ds_bpermute_b32 v85, v95, v83
	v_cmp_lt_i32_e32 vcc, v86, v94
	s_waitcnt lgkmcnt(0)
	v_pk_add_f32 v[82:83], v[82:83], v[84:85]
	v_cndmask_b32_e32 v86, v169, v86, vcc
	v_lshlrev_b32_e32 v86, 2, v86
	ds_bpermute_b32 v84, v86, v82
	ds_bpermute_b32 v85, v86, v83
	s_and_saveexec_b64 s[0:1], s[6:7]
	s_cbranch_execz .LBB0_257
	s_waitcnt lgkmcnt(0)
	v_pk_add_f32 v[82:83], v[82:83], v[84:85]
	v_lshlrev_b64 v[84:85], 7, v[98:99]
	v_lshl_add_u64 v[84:85], s[12:13], 0, v[84:85]
	global_store_dwordx2 v[84:85], v[82:83], off nt

; __device__ __forceinline__ unsigned cvt_pk_bf16(float lo, float hi) { f32x2 v = {lo, hi}; bf16x2_t b = __builtin_convertvector(v, bf16x2_t); return __builtin_bit_cast(unsigned, b); }
; __device__ __forceinline__ f32x2 gelu_pk(f32x2 v) {
;     const f32x2 av = __builtin_elementwise_abs(v), d = av * 0.2316418882f + 1.0f;
;     f32x2 t; t.x = __builtin_amdgcn_rcpf(d.x); t.y = __builtin_amdgcn_rcpf(d.y);
;     f32x2 q = t * 0.5307027145f + (-0.7265760135f); q = q * t + 0.7107068705f; q = q * t + (-0.142248368f); q = q * t + 0.127414796f; q = q * t;
;     const f32x2 s = (v * v) * (-0.72134752044f);
;     f32x2 e; e.x = __builtin_amdgcn_exp2f(s.x); e.y = __builtin_amdgcn_exp2f(s.y);
;     const f32x2 m = v * (q * e), r = v - m;
;     f32x2 o; o.x = v.x < 0.f ? m.x : r.x; o.y = v.y < 0.f ? m.y : r.y; return o;
; }
; __device__ __forceinline__ f32x4 gelu4(f32x4 v) { f32x2 a = gelu_pk((f32x2){v[0], v[1]}), b = gelu_pk((f32x2){v[2], v[3]}); return (f32x4){a.x, a.y, b.x, b.y}; }
;     __device__ __forceinline__ void operator()(const AccT& acc, const pg8::Unit& u, int wr, int wc, int fr, int fq) const {
;     ...
;                 for (int m = 0; m < 4; ++m) { const int row = row0 + ai * 128 + m * 16; float s = 0.f, q = 0.f;
; #pragma unroll
;                     for (int bj = 0; bj < 2; ++bj) { const f32x4 v0 = gelu4(acc[ai][bj][m][0]), v1 = gelu4(acc[ai][bj][m][1]);
;                         s += (v0[0] + v0[1]) + (v0[2] + v0[3]) + (v1[0] + v1[1]) + (v1[2] + v1[3]);
;                         q += (v0[0] * v0[0] + v0[1] * v0[1]) + (v0[2] * v0[2] + v0[3] * v0[3]) + (v1[0] * v1[0] + v1[1] * v1[1]) + (v1[2] * v1[2] + v1[3] * v1[3]);
;                         u32x4 w; w.x = cvt_pk_bf16(v0[0], v0[1]); w.y = cvt_pk_bf16(v0[2], v0[3]); w.z = cvt_pk_bf16(v1[0], v1[1]); w.w = cvt_pk_bf16(v1[2], v1[3]);
;                         *(u32x4*)(dst + (size_t)row * GW + col0 + bj * 128) = w; }
.LBB0_258:
	s_waitcnt lgkmcnt(0)
	v_and_b32_e32 v85, 0x7fffffff, v79
	v_and_b32_e32 v84, 0x7fffffff, v78
	v_pk_fma_f32 v[84:85], v[84:85], s[28:29], 1.0 op_sel_hi:[1,0,0]
	v_mov_b64_e32 v[86:87], s[34:35]
	v_rcp_f32_e32 v88, v84
	v_rcp_f32_e32 v89, v85
	v_pk_mul_f32 v[92:93], v[78:79], v[78:79]
	v_and_b32_e32 v95, 0x7fffffff, v81
	v_pk_mul_f32 v[92:93], v[92:93], s[42:43] op_sel_hi:[1,0]
	v_pk_fma_f32 v[90:91], v[88:89], s[30:31], v[86:87] op_sel_hi:[1,0,0]
	v_and_b32_e32 v94, 0x7fffffff, v80
	v_pk_fma_f32 v[90:91], v[88:89], v[90:91], s[36:37] op_sel_hi:[1,1,0]
	v_exp_f32_e32 v92, v92
	v_exp_f32_e32 v93, v93
	v_pk_fma_f32 v[94:95], v[94:95], s[28:29], 1.0 op_sel_hi:[1,0,0]
	v_pk_fma_f32 v[90:91], v[88:89], v[90:91], s[38:39] op_sel_hi:[1,1,0]
	v_rcp_f32_e32 v94, v94
	v_rcp_f32_e32 v95, v95
	v_pk_fma_f32 v[90:91], v[88:89], v[90:91], s[40:41] op_sel_hi:[1,1,0]
	v_and_b32_e32 v97, 0x7fffffff, v77
	v_pk_mul_f32 v[88:89], v[88:89], v[90:91]
	v_pk_mul_f32 v[90:91], v[80:81], v[80:81]
	v_pk_mul_f32 v[88:89], v[92:93], v[88:89]
	v_pk_mul_f32 v[90:91], v[90:91], s[42:43] op_sel_hi:[1,0]
	v_pk_mul_f32 v[92:93], v[78:79], v[88:89]
	v_pk_fma_f32 v[98:99], v[78:79], v[88:89], v[78:79] neg_lo:[1,0,0] neg_hi:[1,0,0]
	v_pk_fma_f32 v[88:89], v[94:95], s[30:31], v[86:87] op_sel_hi:[1,0,0]
	v_exp_f32_e32 v90, v90
	v_pk_fma_f32 v[88:89], v[94:95], v[88:89], s[36:37] op_sel_hi:[1,1,0]
	v_exp_f32_e32 v91, v91
	v_pk_fma_f32 v[88:89], v[94:95], v[88:89], s[38:39] op_sel_hi:[1,1,0]
	v_and_b32_e32 v96, 0x7fffffff, v76
	v_pk_fma_f32 v[88:89], v[94:95], v[88:89], s[40:41] op_sel_hi:[1,1,0]
	v_pk_fma_f32 v[96:97], v[96:97], s[28:29], 1.0 op_sel_hi:[1,0,0]
	v_pk_mul_f32 v[88:89], v[94:95], v[88:89]
	v_and_b32_e32 v95, 0x7fffffff, v75
	v_and_b32_e32 v94, 0x7fffffff, v74
	v_pk_fma_f32 v[94:95], v[94:95], s[28:29], 1.0 op_sel_hi:[1,0,0]
	v_pk_mul_f32 v[88:89], v[90:91], v[88:89]
	v_rcp_f32_e32 v94, v94
	v_rcp_f32_e32 v95, v95
	v_pk_mul_f32 v[90:91], v[74:75], v[74:75]
	v_pk_mul_f32 v[100:101], v[80:81], v[88:89]
	v_pk_fma_f32 v[102:103], v[80:81], v[88:89], v[80:81] neg_lo:[1,0,0] neg_hi:[1,0,0]
	v_pk_fma_f32 v[88:89], v[94:95], s[30:31], v[86:87] op_sel_hi:[1,0,0]
	v_pk_mul_f32 v[90:91], v[90:91], s[42:43] op_sel_hi:[1,0]
	v_pk_fma_f32 v[88:89], v[94:95], v[88:89], s[36:37] op_sel_hi:[1,1,0]
	v_exp_f32_e32 v90, v90
	v_exp_f32_e32 v91, v91
	v_pk_fma_f32 v[88:89], v[94:95], v[88:89], s[38:39] op_sel_hi:[1,1,0]
	v_rcp_f32_e32 v96, v96
	v_pk_fma_f32 v[88:89], v[94:95], v[88:89], s[40:41] op_sel_hi:[1,1,0]
	v_rcp_f32_e32 v97, v97
	v_pk_mul_f32 v[88:89], v[94:95], v[88:89]
	v_cmp_gt_f32_e32 vcc, 0, v75
	v_pk_mul_f32 v[88:89], v[90:91], v[88:89]
	v_pk_mul_f32 v[94:95], v[76:77], v[76:77]
	v_pk_mul_f32 v[90:91], v[74:75], v[88:89]
	v_pk_fma_f32 v[88:89], v[74:75], v[88:89], v[74:75] neg_lo:[1,0,0] neg_hi:[1,0,0]
	v_pk_mul_f32 v[104:105], v[70:71], v[70:71]
	v_cndmask_b32_e32 v75, v89, v91, vcc
	v_cmp_gt_f32_e32 vcc, 0, v74
	v_pk_mul_f32 v[104:105], v[104:105], s[42:43] op_sel_hi:[1,0]
	v_and_b32_e32 v107, 0x7fffffff, v73
	v_cndmask_b32_e32 v74, v88, v90, vcc
	v_pk_fma_f32 v[88:89], v[96:97], s[30:31], v[86:87] op_sel_hi:[1,0,0]
	v_pk_mul_f32 v[90:91], v[94:95], s[42:43] op_sel_hi:[1,0]
	v_pk_fma_f32 v[88:89], v[96:97], v[88:89], s[36:37] op_sel_hi:[1,1,0]
	v_exp_f32_e32 v90, v90
	v_exp_f32_e32 v91, v91
	v_pk_fma_f32 v[88:89], v[96:97], v[88:89], s[38:39] op_sel_hi:[1,1,0]
	v_and_b32_e32 v106, 0x7fffffff, v72
	v_pk_fma_f32 v[88:89], v[96:97], v[88:89], s[40:41] op_sel_hi:[1,1,0]
	v_exp_f32_e32 v104, v104
	v_pk_mul_f32 v[88:89], v[96:97], v[88:89]
	v_exp_f32_e32 v105, v105
	v_pk_mul_f32 v[88:89], v[90:91], v[88:89]
	v_pk_fma_f32 v[106:107], v[106:107], s[28:29], 1.0 op_sel_hi:[1,0,0]
	v_pk_mul_f32 v[94:95], v[76:77], v[88:89]
	v_pk_fma_f32 v[96:97], v[76:77], v[88:89], v[76:77] neg_lo:[1,0,0] neg_hi:[1,0,0]
	v_and_b32_e32 v89, 0x7fffffff, v71
	v_and_b32_e32 v88, 0x7fffffff, v70
	v_pk_fma_f32 v[88:89], v[88:89], s[28:29], 1.0 op_sel_hi:[1,0,0]
	v_rcp_f32_e32 v106, v106
	v_rcp_f32_e32 v88, v88
	v_rcp_f32_e32 v89, v89
	v_rcp_f32_e32 v107, v107
	v_cmp_gt_f32_e32 vcc, 0, v76
	v_or_b32_e32 v82, 48, v142
	v_pk_fma_f32 v[90:91], v[88:89], s[30:31], v[86:87] op_sel_hi:[1,0,0]
	v_cndmask_b32_e32 v76, v96, v94, vcc
	v_pk_fma_f32 v[90:91], v[88:89], v[90:91], s[36:37] op_sel_hi:[1,1,0]
	v_cmp_gt_f32_e32 vcc, 0, v72
	v_pk_fma_f32 v[90:91], v[88:89], v[90:91], s[38:39] op_sel_hi:[1,1,0]
	v_ashrrev_i32_e32 v83, 31, v82
	v_pk_fma_f32 v[90:91], v[88:89], v[90:91], s[40:41] op_sel_hi:[1,1,0]
	v_lshlrev_b64 v[84:85], 11, v[82:83]
	v_pk_mul_f32 v[88:89], v[88:89], v[90:91]
	v_pk_mul_f32 v[90:91], v[72:73], v[72:73]
	v_pk_mul_f32 v[88:89], v[104:105], v[88:89]
	v_pk_mul_f32 v[90:91], v[90:91], s[42:43] op_sel_hi:[1,0]
	v_pk_mul_f32 v[104:105], v[70:71], v[88:89]
	v_pk_fma_f32 v[108:109], v[70:71], v[88:89], v[70:71] neg_lo:[1,0,0] neg_hi:[1,0,0]
	v_pk_fma_f32 v[88:89], v[106:107], s[30:31], v[86:87] op_sel_hi:[1,0,0]
	v_exp_f32_e32 v90, v90
	v_pk_fma_f32 v[88:89], v[106:107], v[88:89], s[36:37] op_sel_hi:[1,1,0]
	v_exp_f32_e32 v91, v91
	v_pk_fma_f32 v[88:89], v[106:107], v[88:89], s[38:39] op_sel_hi:[1,1,0]
	v_lshl_add_u64 v[84:85], v[144:145], 0, v[84:85]
	v_pk_fma_f32 v[88:89], v[106:107], v[88:89], s[40:41] op_sel_hi:[1,1,0]
	v_cvt_pk_bf16_f32 v96, v74, v75
	v_pk_mul_f32 v[88:89], v[106:107], v[88:89]
	s_nop 0
	v_pk_mul_f32 v[88:89], v[90:91], v[88:89]
	s_nop 0
	v_pk_mul_f32 v[90:91], v[72:73], v[88:89]
	v_pk_fma_f32 v[106:107], v[72:73], v[88:89], v[72:73] neg_lo:[1,0,0] neg_hi:[1,0,0]
	v_and_b32_e32 v89, 0x7fffffff, v67
	v_and_b32_e32 v88, 0x7fffffff, v66
; __device__ __forceinline__ unsigned cvt_pk_bf16(float lo, float hi) { f32x2 v = {lo, hi}; bf16x2_t b = __builtin_convertvector(v, bf16x2_t); return __builtin_bit_cast(unsigned, b); }
; __device__ __forceinline__ f32x2 gelu_pk(f32x2 v) {
;     const f32x2 av = __builtin_elementwise_abs(v), d = av * 0.2316418882f + 1.0f;
;     f32x2 t; t.x = __builtin_amdgcn_rcpf(d.x); t.y = __builtin_amdgcn_rcpf(d.y);
;     f32x2 q = t * 0.5307027145f + (-0.7265760135f); q = q * t + 0.7107068705f; q = q * t + (-0.142248368f); q = q * t + 0.127414796f; q = q * t;
;     const f32x2 s = (v * v) * (-0.72134752044f);
;     f32x2 e; e.x = __builtin_amdgcn_exp2f(s.x); e.y = __builtin_amdgcn_exp2f(s.y);
;     const f32x2 m = v * (q * e), r = v - m;
;     f32x2 o; o.x = v.x < 0.f ? m.x : r.x; o.y = v.y < 0.f ? m.y : r.y; return o;
; }
; __device__ __forceinline__ f32x4 gelu4(f32x4 v) { f32x2 a = gelu_pk((f32x2){v[0], v[1]}), b = gelu_pk((f32x2){v[2], v[3]}); return (f32x4){a.x, a.y, b.x, b.y}; }
;     __device__ __forceinline__ void operator()(const AccT& acc, const pg8::Unit& u, int wr, int wc, int fr, int fq) const {
;     ...
;                 for (int m = 0; m < 4; ++m) { const int row = row0 + ai * 128 + m * 16; float s = 0.f, q = 0.f;
; #pragma unroll
;                     for (int bj = 0; bj < 2; ++bj) { const f32x4 v0 = gelu4(acc[ai][bj][m][0]), v1 = gelu4(acc[ai][bj][m][1]);
;                         s += (v0[0] + v0[1]) + (v0[2] + v0[3]) + (v1[0] + v1[1]) + (v1[2] + v1[3]);
;                         q += (v0[0] * v0[0] + v0[1] * v0[1]) + (v0[2] * v0[2] + v0[3] * v0[3]) + (v1[0] * v1[0] + v1[1] * v1[1]) + (v1[2] * v1[2] + v1[3] * v1[3]);
;                         u32x4 w; w.x = cvt_pk_bf16(v0[0], v0[1]); w.y = cvt_pk_bf16(v0[2], v0[3]); w.z = cvt_pk_bf16(v1[0], v1[1]); w.w = cvt_pk_bf16(v1[2], v1[3]);
;                         *(u32x4*)(dst + (size_t)row * GW + col0 + bj * 128) = w; }
;                     if (pn >= 4) { s += __shfl_xor(s, 16); s += __shfl_xor(s, 32); q += __shfl_xor(q, 16); q += __shfl_xor(q, 32);
;                         if (fq == 0) *(f32x2*)(vstat + (size_t)row * 32 + ((pn - 4) * 4 + wc) * 2) = (f32x2){s, q}; } }
	v_pk_fma_f32 v[88:89], v[88:89], s[28:29], 1.0 op_sel_hi:[1,0,0]
	s_nop 0
	v_rcp_f32_e32 v110, v88
	v_rcp_f32_e32 v111, v89
	v_cndmask_b32_e32 v89, v106, v90, vcc
	v_cmp_gt_f32_e32 vcc, 0, v73
	s_nop 1
	v_cndmask_b32_e32 v73, v107, v91, vcc
	v_pk_mul_f32 v[106:107], v[66:67], v[66:67]
	v_pk_fma_f32 v[90:91], v[110:111], s[30:31], v[86:87] op_sel_hi:[1,0,0]
	v_pk_mul_f32 v[106:107], v[106:107], s[42:43] op_sel_hi:[1,0]
	v_pk_fma_f32 v[90:91], v[110:111], v[90:91], s[36:37] op_sel_hi:[1,1,0]
	v_exp_f32_e32 v106, v106
	v_exp_f32_e32 v107, v107
	v_pk_fma_f32 v[90:91], v[110:111], v[90:91], s[38:39] op_sel_hi:[1,1,0]
	v_cmp_gt_f32_e32 vcc, 0, v78
	v_pk_fma_f32 v[90:91], v[110:111], v[90:91], s[40:41] op_sel_hi:[1,1,0]
	s_nop 0
	v_pk_mul_f32 v[90:91], v[110:111], v[90:91]
	v_pk_mul_f32 v[110:111], v[68:69], v[68:69]
	v_pk_mul_f32 v[90:91], v[106:107], v[90:91]
	s_nop 0
	v_pk_mul_f32 v[106:107], v[66:67], v[90:91]
	v_pk_fma_f32 v[112:113], v[66:67], v[90:91], v[66:67] neg_lo:[1,0,0] neg_hi:[1,0,0]
	v_cndmask_b32_e32 v90, v98, v92, vcc
	v_cmp_gt_f32_e32 vcc, 0, v70
	v_and_b32_e32 v98, 0x7fffffff, v68
	s_nop 0
	v_cndmask_b32_e32 v91, v108, v104, vcc
	v_cmp_gt_f32_e32 vcc, 0, v79
	s_nop 1
	v_cndmask_b32_e32 v92, v99, v93, vcc
	v_cmp_gt_f32_e32 vcc, 0, v80
	v_and_b32_e32 v99, 0x7fffffff, v69
	v_pk_fma_f32 v[98:99], v[98:99], s[28:29], 1.0 op_sel_hi:[1,0,0]
	v_cndmask_b32_e32 v78, v102, v100, vcc
	v_cmp_gt_f32_e32 vcc, 0, v71
	v_rcp_f32_e32 v98, v98
	v_rcp_f32_e32 v99, v99
	v_cndmask_b32_e32 v79, v109, v105, vcc
	v_cmp_gt_f32_e32 vcc, 0, v81
	v_cvt_pk_bf16_f32 v94, v90, v92
	v_pk_fma_f32 v[86:87], v[98:99], s[30:31], v[86:87] op_sel_hi:[1,0,0]
	v_cndmask_b32_e32 v80, v103, v101, vcc
	v_cmp_gt_f32_e32 vcc, 0, v66
	v_pk_fma_f32 v[86:87], v[98:99], v[86:87], s[36:37] op_sel_hi:[1,1,0]
	s_nop 0
	v_cndmask_b32_e32 v70, v112, v106, vcc
	v_cmp_gt_f32_e32 vcc, 0, v77
	v_pk_fma_f32 v[86:87], v[98:99], v[86:87], s[38:39] op_sel_hi:[1,1,0]
	s_nop 0
	v_cndmask_b32_e32 v71, v97, v95, vcc
	v_cvt_pk_bf16_f32 v95, v78, v80
	v_cvt_pk_bf16_f32 v97, v76, v71
	global_store_dwordx4 v[84:85], v[94:97], off nt
	v_pk_fma_f32 v[86:87], v[98:99], v[86:87], s[40:41] op_sel_hi:[1,1,0]
	v_cmp_gt_f32_e32 vcc, 0, v67
	v_pk_mul_f32 v[94:95], v[110:111], s[42:43] op_sel_hi:[1,0]
	v_pk_mul_f32 v[86:87], v[98:99], v[86:87]
	v_exp_f32_e32 v94, v94
	v_exp_f32_e32 v95, v95
	v_cndmask_b32_e32 v66, v113, v107, vcc
	v_cmp_gt_f32_e32 vcc, 0, v69
	v_cvt_pk_bf16_f32 v96, v70, v66
	v_pk_mul_f32 v[86:87], v[94:95], v[86:87]
	s_nop 0
	v_pk_mul_f32 v[94:95], v[68:69], v[86:87]
	v_pk_fma_f32 v[86:87], v[68:69], v[86:87], v[68:69] neg_lo:[1,0,0] neg_hi:[1,0,0]
	s_nop 0
	v_cndmask_b32_e32 v69, v87, v95, vcc
	v_cmp_gt_f32_e32 vcc, 0, v68
	v_cvt_pk_bf16_f32 v95, v89, v73
	s_nop 0
	v_cndmask_b32_e32 v68, v86, v94, vcc
	v_cvt_pk_bf16_f32 v94, v91, v79
	v_cvt_pk_bf16_f32 v97, v68, v69
	s_and_b64 vcc, exec, s[10:11]
	global_store_dwordx4 v[84:85], v[94:97], off offset:256 nt
	s_cbranch_vccnz .LBB0_262
	v_mov_b32_e32 v93, v91
	v_mov_b32_e32 v67, v71
	v_mov_b32_e32 v81, v79
	v_pk_add_f32 v[84:85], v[70:71], v[66:67]
	v_pk_mul_f32 v[86:87], v[70:71], v[66:67]
	v_mov_b32_e32 v94, v92
	v_pk_add_f32 v[98:99], v[90:91], v[92:93]
	v_pk_mul_f32 v[92:93], v[90:91], v[92:93]
	v_mov_b32_e32 v85, v87
	v_mov_b32_e32 v87, v78
	v_mov_b32_e32 v95, v80
	v_mov_b32_e32 v99, v93
	v_pk_add_f32 v[92:93], v[78:79], v[80:81]
	v_pk_mul_f32 v[80:81], v[78:79], v[80:81]
	v_and_b32_e32 v78, 64, v169
	v_xor_b32_e32 v77, 16, v169
	v_add_u32_e32 v78, 64, v78
	v_mov_b32_e32 v86, v90
	v_pk_mul_f32 v[94:95], v[94:95], v[94:95]
	v_mul_f32_e32 v72, v74, v74
	v_cmp_lt_i32_e32 vcc, v77, v78
	v_pk_fma_f32 v[86:87], v[86:87], v[86:87], v[94:95]
	v_pk_fma_f32 v[94:95], v[74:75], v[74:75], v[72:73] op_sel_hi:[1,1,0]
	v_mul_f32_e32 v72, v68, v68
	v_mov_b32_e32 v93, v81
	v_mul_f32_e32 v81, v89, v89
	v_mul_f32_e32 v101, v73, v73
	v_pk_mul_f32 v[102:103], v[70:71], v[70:71]
	v_pk_mul_f32 v[66:67], v[66:67], v[66:67]
	v_cndmask_b32_e32 v77, v169, v77, vcc
	v_mov_b32_e32 v80, v74
	v_mov_b32_e32 v100, v75
	v_pk_fma_f32 v[96:97], v[68:69], v[68:69], v[72:73] op_sel_hi:[1,1,0]
	v_mov_b32_e32 v88, v91
	v_mov_b32_e32 v72, v79
	v_lshlrev_b32_e32 v79, 2, v77
	v_mov_b32_e32 v77, v102
	v_pk_mov_b32 v[66:67], v[70:71], v[66:67] op_sel:[1,0]
	v_pk_add_f32 v[70:71], v[98:99], v[92:93]
	v_pk_add_f32 v[74:75], v[80:81], v[100:101]
	v_pk_add_f32 v[72:73], v[88:89], v[72:73]
	v_pk_add_f32 v[66:67], v[76:77], v[66:67]
	v_pk_add_f32 v[70:71], v[70:71], v[74:75]
	v_mul_f32_e32 v104, v76, v76
	v_pk_add_f32 v[86:87], v[86:87], v[86:87] op_sel_hi:[0,1]
	v_pk_add_f32 v[66:67], v[70:71], v[66:67]
	v_pk_add_f32 v[70:71], v[72:73], v[72:73] op_sel:[0,1] op_sel_hi:[1,0]
	v_mov_b32_e32 v86, v68
	v_mov_b32_e32 v94, v69
	v_mov_b32_e32 v71, v104
	v_mov_b32_e32 v96, v131
	v_pk_add_f32 v[68:69], v[86:87], v[94:95]
	v_pk_add_f32 v[70:71], v[70:71], v[84:85]
	v_pk_add_f32 v[66:67], v[66:67], v[96:97]
	v_pk_add_f32 v[68:69], v[70:71], v[68:69]
	v_xor_b32_e32 v70, 32, v169
	v_pk_add_f32 v[66:67], v[68:69], v[66:67]
	ds_bpermute_b32 v68, v79, v66
	ds_bpermute_b32 v69, v79, v67
	v_cmp_lt_i32_e32 vcc, v70, v78
	s_waitcnt lgkmcnt(0)
	v_pk_add_f32 v[66:67], v[66:67], v[68:69]
	v_cndmask_b32_e32 v70, v169, v70, vcc
	v_lshlrev_b32_e32 v70, 2, v70
	ds_bpermute_b32 v68, v70, v66
	ds_bpermute_b32 v69, v70, v67
	s_and_saveexec_b64 s[0:1], s[6:7]
	s_cbranch_execz .LBB0_261
	s_waitcnt lgkmcnt(0)
	v_pk_add_f32 v[66:67], v[66:67], v[68:69]
	v_lshlrev_b64 v[68:69], 7, v[82:83]
	v_lshl_add_u64 v[68:69], s[12:13], 0, v[68:69]
	global_store_dwordx2 v[68:69], v[66:67], off nt

; __device__ __forceinline__ unsigned cvt_pk_bf16(float lo, float hi) { f32x2 v = {lo, hi}; bf16x2_t b = __builtin_convertvector(v, bf16x2_t); return __builtin_bit_cast(unsigned, b); }
; __device__ __forceinline__ f32x2 gelu_pk(f32x2 v) {
;     const f32x2 av = __builtin_elementwise_abs(v), d = av * 0.2316418882f + 1.0f;
;     f32x2 t; t.x = __builtin_amdgcn_rcpf(d.x); t.y = __builtin_amdgcn_rcpf(d.y);
;     f32x2 q = t * 0.5307027145f + (-0.7265760135f); q = q * t + 0.7107068705f; q = q * t + (-0.142248368f); q = q * t + 0.127414796f; q = q * t;
;     const f32x2 s = (v * v) * (-0.72134752044f);
;     f32x2 e; e.x = __builtin_amdgcn_exp2f(s.x); e.y = __builtin_amdgcn_exp2f(s.y);
;     const f32x2 m = v * (q * e), r = v - m;
;     f32x2 o; o.x = v.x < 0.f ? m.x : r.x; o.y = v.y < 0.f ? m.y : r.y; return o;
; }
; __device__ __forceinline__ f32x4 gelu4(f32x4 v) { f32x2 a = gelu_pk((f32x2){v[0], v[1]}), b = gelu_pk((f32x2){v[2], v[3]}); return (f32x4){a.x, a.y, b.x, b.y}; }
;     __device__ __forceinline__ void operator()(const AccT& acc, const pg8::Unit& u, int wr, int wc, int fr, int fq) const {
;     ...
;                 for (int m = 0; m < 4; ++m) { const int row = row0 + ai * 128 + m * 16; float s = 0.f, q = 0.f;
; #pragma unroll
;                     for (int bj = 0; bj < 2; ++bj) { const f32x4 v0 = gelu4(acc[ai][bj][m][0]), v1 = gelu4(acc[ai][bj][m][1]);
;                         s += (v0[0] + v0[1]) + (v0[2] + v0[3]) + (v1[0] + v1[1]) + (v1[2] + v1[3]);
;                         q += (v0[0] * v0[0] + v0[1] * v0[1]) + (v0[2] * v0[2] + v0[3] * v0[3]) + (v1[0] * v1[0] + v1[1] * v1[1]) + (v1[2] * v1[2] + v1[3] * v1[3]);
;                         u32x4 w; w.x = cvt_pk_bf16(v0[0], v0[1]); w.y = cvt_pk_bf16(v0[2], v0[3]); w.z = cvt_pk_bf16(v1[0], v1[1]); w.w = cvt_pk_bf16(v1[2], v1[3]);
;                         *(u32x4*)(dst + (size_t)row * GW + col0 + bj * 128) = w; }
.LBB0_262:
	s_waitcnt lgkmcnt(0)
	v_and_b32_e32 v69, 0x7fffffff, v63
	v_and_b32_e32 v68, 0x7fffffff, v62
	v_pk_fma_f32 v[68:69], v[68:69], s[28:29], 1.0 op_sel_hi:[1,0,0]
	v_mov_b64_e32 v[70:71], s[34:35]
	v_rcp_f32_e32 v72, v68
	v_rcp_f32_e32 v73, v69
	v_pk_mul_f32 v[76:77], v[62:63], v[62:63]
	v_and_b32_e32 v79, 0x7fffffff, v65
	v_pk_mul_f32 v[76:77], v[76:77], s[42:43] op_sel_hi:[1,0]
	v_pk_fma_f32 v[74:75], v[72:73], s[30:31], v[70:71] op_sel_hi:[1,0,0]
	v_and_b32_e32 v78, 0x7fffffff, v64
	v_pk_fma_f32 v[74:75], v[72:73], v[74:75], s[36:37] op_sel_hi:[1,1,0]
	v_exp_f32_e32 v76, v76
	v_exp_f32_e32 v77, v77
	v_pk_fma_f32 v[78:79], v[78:79], s[28:29], 1.0 op_sel_hi:[1,0,0]
	v_pk_fma_f32 v[74:75], v[72:73], v[74:75], s[38:39] op_sel_hi:[1,1,0]
	v_rcp_f32_e32 v78, v78
	v_rcp_f32_e32 v79, v79
	v_pk_fma_f32 v[74:75], v[72:73], v[74:75], s[40:41] op_sel_hi:[1,1,0]
	v_and_b32_e32 v81, 0x7fffffff, v61
	v_pk_mul_f32 v[72:73], v[72:73], v[74:75]
	v_pk_mul_f32 v[74:75], v[64:65], v[64:65]
	v_pk_mul_f32 v[72:73], v[76:77], v[72:73]
	v_pk_mul_f32 v[74:75], v[74:75], s[42:43] op_sel_hi:[1,0]
	v_pk_mul_f32 v[76:77], v[62:63], v[72:73]
	v_pk_fma_f32 v[82:83], v[62:63], v[72:73], v[62:63] neg_lo:[1,0,0] neg_hi:[1,0,0]
	v_pk_fma_f32 v[72:73], v[78:79], s[30:31], v[70:71] op_sel_hi:[1,0,0]
	v_exp_f32_e32 v74, v74
	v_pk_fma_f32 v[72:73], v[78:79], v[72:73], s[36:37] op_sel_hi:[1,1,0]
	v_exp_f32_e32 v75, v75
	v_pk_fma_f32 v[72:73], v[78:79], v[72:73], s[38:39] op_sel_hi:[1,1,0]
	v_and_b32_e32 v80, 0x7fffffff, v60
	v_pk_fma_f32 v[72:73], v[78:79], v[72:73], s[40:41] op_sel_hi:[1,1,0]
	v_pk_fma_f32 v[80:81], v[80:81], s[28:29], 1.0 op_sel_hi:[1,0,0]
	v_pk_mul_f32 v[72:73], v[78:79], v[72:73]
	v_and_b32_e32 v79, 0x7fffffff, v59
	v_and_b32_e32 v78, 0x7fffffff, v58
	v_pk_fma_f32 v[78:79], v[78:79], s[28:29], 1.0 op_sel_hi:[1,0,0]
	v_pk_mul_f32 v[72:73], v[74:75], v[72:73]
	v_rcp_f32_e32 v78, v78
	v_rcp_f32_e32 v79, v79
	v_pk_mul_f32 v[74:75], v[58:59], v[58:59]
	v_pk_mul_f32 v[84:85], v[64:65], v[72:73]
	v_pk_fma_f32 v[86:87], v[64:65], v[72:73], v[64:65] neg_lo:[1,0,0] neg_hi:[1,0,0]
	v_pk_fma_f32 v[72:73], v[78:79], s[30:31], v[70:71] op_sel_hi:[1,0,0]
	v_pk_mul_f32 v[74:75], v[74:75], s[42:43] op_sel_hi:[1,0]
	v_pk_fma_f32 v[72:73], v[78:79], v[72:73], s[36:37] op_sel_hi:[1,1,0]
	v_exp_f32_e32 v74, v74
	v_exp_f32_e32 v75, v75
	v_pk_fma_f32 v[72:73], v[78:79], v[72:73], s[38:39] op_sel_hi:[1,1,0]
	v_rcp_f32_e32 v80, v80
	v_pk_fma_f32 v[72:73], v[78:79], v[72:73], s[40:41] op_sel_hi:[1,1,0]
	v_rcp_f32_e32 v81, v81
	v_pk_mul_f32 v[72:73], v[78:79], v[72:73]
	v_cmp_gt_f32_e32 vcc, 0, v59
	v_pk_mul_f32 v[72:73], v[74:75], v[72:73]
	v_pk_mul_f32 v[78:79], v[60:61], v[60:61]
	v_pk_mul_f32 v[74:75], v[58:59], v[72:73]
	v_pk_fma_f32 v[72:73], v[58:59], v[72:73], v[58:59] neg_lo:[1,0,0] neg_hi:[1,0,0]
	v_pk_mul_f32 v[88:89], v[54:55], v[54:55]
	v_cndmask_b32_e32 v59, v73, v75, vcc
	v_cmp_gt_f32_e32 vcc, 0, v58
	v_pk_mul_f32 v[88:89], v[88:89], s[42:43] op_sel_hi:[1,0]
	v_and_b32_e32 v91, 0x7fffffff, v57
	v_cndmask_b32_e32 v58, v72, v74, vcc
	v_pk_fma_f32 v[72:73], v[80:81], s[30:31], v[70:71] op_sel_hi:[1,0,0]
	v_pk_mul_f32 v[74:75], v[78:79], s[42:43] op_sel_hi:[1,0]
	v_pk_fma_f32 v[72:73], v[80:81], v[72:73], s[36:37] op_sel_hi:[1,1,0]
	v_exp_f32_e32 v74, v74
	v_exp_f32_e32 v75, v75
	v_pk_fma_f32 v[72:73], v[80:81], v[72:73], s[38:39] op_sel_hi:[1,1,0]
	v_and_b32_e32 v90, 0x7fffffff, v56
	v_pk_fma_f32 v[72:73], v[80:81], v[72:73], s[40:41] op_sel_hi:[1,1,0]
	v_exp_f32_e32 v88, v88
	v_pk_mul_f32 v[72:73], v[80:81], v[72:73]
	v_exp_f32_e32 v89, v89
	v_pk_mul_f32 v[72:73], v[74:75], v[72:73]
	v_pk_fma_f32 v[90:91], v[90:91], s[28:29], 1.0 op_sel_hi:[1,0,0]
	v_pk_mul_f32 v[78:79], v[60:61], v[72:73]
	v_pk_fma_f32 v[80:81], v[60:61], v[72:73], v[60:61] neg_lo:[1,0,0] neg_hi:[1,0,0]
	v_and_b32_e32 v73, 0x7fffffff, v55
	v_and_b32_e32 v72, 0x7fffffff, v54
	v_pk_fma_f32 v[72:73], v[72:73], s[28:29], 1.0 op_sel_hi:[1,0,0]
	v_rcp_f32_e32 v90, v90
	v_rcp_f32_e32 v72, v72
	v_rcp_f32_e32 v73, v73
	v_rcp_f32_e32 v91, v91
	v_cmp_gt_f32_e32 vcc, 0, v60
	v_add_u32_e32 v66, 0x80, v142
	v_pk_fma_f32 v[74:75], v[72:73], s[30:31], v[70:71] op_sel_hi:[1,0,0]
	v_cndmask_b32_e32 v60, v80, v78, vcc
	v_pk_fma_f32 v[74:75], v[72:73], v[74:75], s[36:37] op_sel_hi:[1,1,0]
	v_cmp_gt_f32_e32 vcc, 0, v56
	v_pk_fma_f32 v[74:75], v[72:73], v[74:75], s[38:39] op_sel_hi:[1,1,0]
	v_ashrrev_i32_e32 v67, 31, v66
	v_pk_fma_f32 v[74:75], v[72:73], v[74:75], s[40:41] op_sel_hi:[1,1,0]
	v_lshlrev_b64 v[68:69], 11, v[66:67]
	v_pk_mul_f32 v[72:73], v[72:73], v[74:75]
	v_pk_mul_f32 v[74:75], v[56:57], v[56:57]
	v_pk_mul_f32 v[72:73], v[88:89], v[72:73]
	v_pk_mul_f32 v[74:75], v[74:75], s[42:43] op_sel_hi:[1,0]
	v_pk_mul_f32 v[88:89], v[54:55], v[72:73]
	v_pk_fma_f32 v[92:93], v[54:55], v[72:73], v[54:55] neg_lo:[1,0,0] neg_hi:[1,0,0]
	v_pk_fma_f32 v[72:73], v[90:91], s[30:31], v[70:71] op_sel_hi:[1,0,0]
	v_exp_f32_e32 v74, v74
	v_pk_fma_f32 v[72:73], v[90:91], v[72:73], s[36:37] op_sel_hi:[1,1,0]
	v_exp_f32_e32 v75, v75
	v_pk_fma_f32 v[72:73], v[90:91], v[72:73], s[38:39] op_sel_hi:[1,1,0]
	v_lshl_add_u64 v[68:69], v[144:145], 0, v[68:69]
	v_pk_fma_f32 v[72:73], v[90:91], v[72:73], s[40:41] op_sel_hi:[1,1,0]
	v_cvt_pk_bf16_f32 v80, v58, v59
	v_pk_mul_f32 v[72:73], v[90:91], v[72:73]
	s_nop 0
	v_pk_mul_f32 v[72:73], v[74:75], v[72:73]
	s_nop 0
	v_pk_mul_f32 v[74:75], v[56:57], v[72:73]
	v_pk_fma_f32 v[90:91], v[56:57], v[72:73], v[56:57] neg_lo:[1,0,0] neg_hi:[1,0,0]
	v_and_b32_e32 v73, 0x7fffffff, v51
	v_and_b32_e32 v72, 0x7fffffff, v50
; __device__ __forceinline__ unsigned cvt_pk_bf16(float lo, float hi) { f32x2 v = {lo, hi}; bf16x2_t b = __builtin_convertvector(v, bf16x2_t); return __builtin_bit_cast(unsigned, b); }
; __device__ __forceinline__ f32x2 gelu_pk(f32x2 v) {
;     const f32x2 av = __builtin_elementwise_abs(v), d = av * 0.2316418882f + 1.0f;
;     f32x2 t; t.x = __builtin_amdgcn_rcpf(d.x); t.y = __builtin_amdgcn_rcpf(d.y);
;     f32x2 q = t * 0.5307027145f + (-0.7265760135f); q = q * t + 0.7107068705f; q = q * t + (-0.142248368f); q = q * t + 0.127414796f; q = q * t;
;     const f32x2 s = (v * v) * (-0.72134752044f);
;     f32x2 e; e.x = __builtin_amdgcn_exp2f(s.x); e.y = __builtin_amdgcn_exp2f(s.y);
;     const f32x2 m = v * (q * e), r = v - m;
;     f32x2 o; o.x = v.x < 0.f ? m.x : r.x; o.y = v.y < 0.f ? m.y : r.y; return o;
; }
; __device__ __forceinline__ f32x4 gelu4(f32x4 v) { f32x2 a = gelu_pk((f32x2){v[0], v[1]}), b = gelu_pk((f32x2){v[2], v[3]}); return (f32x4){a.x, a.y, b.x, b.y}; }
;     __device__ __forceinline__ void operator()(const AccT& acc, const pg8::Unit& u, int wr, int wc, int fr, int fq) const {
;     ...
;                 for (int m = 0; m < 4; ++m) { const int row = row0 + ai * 128 + m * 16; float s = 0.f, q = 0.f;
; #pragma unroll
;                     for (int bj = 0; bj < 2; ++bj) { const f32x4 v0 = gelu4(acc[ai][bj][m][0]), v1 = gelu4(acc[ai][bj][m][1]);
;                         s += (v0[0] + v0[1]) + (v0[2] + v0[3]) + (v1[0] + v1[1]) + (v1[2] + v1[3]);
;                         q += (v0[0] * v0[0] + v0[1] * v0[1]) + (v0[2] * v0[2] + v0[3] * v0[3]) + (v1[0] * v1[0] + v1[1] * v1[1]) + (v1[2] * v1[2] + v1[3] * v1[3]);
;                         u32x4 w; w.x = cvt_pk_bf16(v0[0], v0[1]); w.y = cvt_pk_bf16(v0[2], v0[3]); w.z = cvt_pk_bf16(v1[0], v1[1]); w.w = cvt_pk_bf16(v1[2], v1[3]);
;                         *(u32x4*)(dst + (size_t)row * GW + col0 + bj * 128) = w; }
;                     if (pn >= 4) { s += __shfl_xor(s, 16); s += __shfl_xor(s, 32); q += __shfl_xor(q, 16); q += __shfl_xor(q, 32);
;                         if (fq == 0) *(f32x2*)(vstat + (size_t)row * 32 + ((pn - 4) * 4 + wc) * 2) = (f32x2){s, q}; } }
	v_pk_fma_f32 v[72:73], v[72:73], s[28:29], 1.0 op_sel_hi:[1,0,0]
	s_nop 0
	v_rcp_f32_e32 v94, v72
	v_rcp_f32_e32 v95, v73
	v_cndmask_b32_e32 v73, v90, v74, vcc
	v_cmp_gt_f32_e32 vcc, 0, v57
	s_nop 1
	v_cndmask_b32_e32 v57, v91, v75, vcc
	v_pk_mul_f32 v[90:91], v[50:51], v[50:51]
	v_pk_fma_f32 v[74:75], v[94:95], s[30:31], v[70:71] op_sel_hi:[1,0,0]
	v_pk_mul_f32 v[90:91], v[90:91], s[42:43] op_sel_hi:[1,0]
	v_pk_fma_f32 v[74:75], v[94:95], v[74:75], s[36:37] op_sel_hi:[1,1,0]
	v_exp_f32_e32 v90, v90
	v_exp_f32_e32 v91, v91
	v_pk_fma_f32 v[74:75], v[94:95], v[74:75], s[38:39] op_sel_hi:[1,1,0]
	v_cmp_gt_f32_e32 vcc, 0, v62
	v_pk_fma_f32 v[74:75], v[94:95], v[74:75], s[40:41] op_sel_hi:[1,1,0]
	s_nop 0
	v_pk_mul_f32 v[74:75], v[94:95], v[74:75]
	v_pk_mul_f32 v[94:95], v[52:53], v[52:53]
	v_pk_mul_f32 v[74:75], v[90:91], v[74:75]
	s_nop 0
	v_pk_mul_f32 v[90:91], v[50:51], v[74:75]
	v_pk_fma_f32 v[96:97], v[50:51], v[74:75], v[50:51] neg_lo:[1,0,0] neg_hi:[1,0,0]
	v_cndmask_b32_e32 v74, v82, v76, vcc
	v_cmp_gt_f32_e32 vcc, 0, v54
	v_and_b32_e32 v82, 0x7fffffff, v52
	s_nop 0
	v_cndmask_b32_e32 v75, v92, v88, vcc
	v_cmp_gt_f32_e32 vcc, 0, v63
	s_nop 1
	v_cndmask_b32_e32 v76, v83, v77, vcc
	v_cmp_gt_f32_e32 vcc, 0, v64
	v_and_b32_e32 v83, 0x7fffffff, v53
	v_pk_fma_f32 v[82:83], v[82:83], s[28:29], 1.0 op_sel_hi:[1,0,0]
	v_cndmask_b32_e32 v62, v86, v84, vcc
	v_cmp_gt_f32_e32 vcc, 0, v55
	v_rcp_f32_e32 v82, v82
	v_rcp_f32_e32 v83, v83
	v_cndmask_b32_e32 v63, v93, v89, vcc
	v_cmp_gt_f32_e32 vcc, 0, v65
	v_cvt_pk_bf16_f32 v78, v74, v76
	v_pk_fma_f32 v[70:71], v[82:83], s[30:31], v[70:71] op_sel_hi:[1,0,0]
	v_cndmask_b32_e32 v64, v87, v85, vcc
	v_cmp_gt_f32_e32 vcc, 0, v50
	v_pk_fma_f32 v[70:71], v[82:83], v[70:71], s[36:37] op_sel_hi:[1,1,0]
	s_nop 0
	v_cndmask_b32_e32 v54, v96, v90, vcc
	v_cmp_gt_f32_e32 vcc, 0, v61
	v_pk_fma_f32 v[70:71], v[82:83], v[70:71], s[38:39] op_sel_hi:[1,1,0]
	s_nop 0
	v_cndmask_b32_e32 v55, v81, v79, vcc
	v_cvt_pk_bf16_f32 v79, v62, v64
	v_cvt_pk_bf16_f32 v81, v60, v55
	global_store_dwordx4 v[68:69], v[78:81], off nt
	v_pk_fma_f32 v[70:71], v[82:83], v[70:71], s[40:41] op_sel_hi:[1,1,0]
	v_cmp_gt_f32_e32 vcc, 0, v51
	v_pk_mul_f32 v[78:79], v[94:95], s[42:43] op_sel_hi:[1,0]
	v_pk_mul_f32 v[70:71], v[82:83], v[70:71]
	v_exp_f32_e32 v78, v78
	v_exp_f32_e32 v79, v79
	v_cndmask_b32_e32 v50, v97, v91, vcc
	v_cmp_gt_f32_e32 vcc, 0, v53
	v_cvt_pk_bf16_f32 v80, v54, v50
	v_pk_mul_f32 v[70:71], v[78:79], v[70:71]
	s_nop 0
	v_pk_mul_f32 v[78:79], v[52:53], v[70:71]
	v_pk_fma_f32 v[70:71], v[52:53], v[70:71], v[52:53] neg_lo:[1,0,0] neg_hi:[1,0,0]
	s_nop 0
	v_cndmask_b32_e32 v53, v71, v79, vcc
	v_cmp_gt_f32_e32 vcc, 0, v52
	v_cvt_pk_bf16_f32 v79, v73, v57
	s_nop 0
	v_cndmask_b32_e32 v52, v70, v78, vcc
	v_cvt_pk_bf16_f32 v78, v75, v63
	v_cvt_pk_bf16_f32 v81, v52, v53
	s_and_b64 vcc, exec, s[10:11]
	global_store_dwordx4 v[68:69], v[78:81], off offset:256 nt
	s_cbranch_vccnz .LBB0_266
	v_mov_b32_e32 v77, v75
	v_mov_b32_e32 v51, v55
	v_mov_b32_e32 v65, v63
	v_pk_add_f32 v[68:69], v[54:55], v[50:51]
	v_pk_mul_f32 v[70:71], v[54:55], v[50:51]
	v_mov_b32_e32 v78, v76
	v_pk_add_f32 v[82:83], v[74:75], v[76:77]
	v_pk_mul_f32 v[76:77], v[74:75], v[76:77]
	v_mov_b32_e32 v69, v71
	v_mov_b32_e32 v71, v62
	v_mov_b32_e32 v79, v64
	v_mov_b32_e32 v83, v77
	v_pk_add_f32 v[76:77], v[62:63], v[64:65]
	v_pk_mul_f32 v[64:65], v[62:63], v[64:65]
	v_and_b32_e32 v62, 64, v169
	v_xor_b32_e32 v61, 16, v169
	v_add_u32_e32 v62, 64, v62
	v_mov_b32_e32 v70, v74
	v_pk_mul_f32 v[78:79], v[78:79], v[78:79]
	v_mul_f32_e32 v56, v58, v58
	v_cmp_lt_i32_e32 vcc, v61, v62
	v_pk_fma_f32 v[70:71], v[70:71], v[70:71], v[78:79]
	v_pk_fma_f32 v[78:79], v[58:59], v[58:59], v[56:57] op_sel_hi:[1,1,0]
	v_mul_f32_e32 v56, v52, v52
	v_mov_b32_e32 v77, v65
	v_mul_f32_e32 v65, v73, v73
	v_mul_f32_e32 v85, v57, v57
	v_pk_mul_f32 v[86:87], v[54:55], v[54:55]
	v_pk_mul_f32 v[50:51], v[50:51], v[50:51]
	v_cndmask_b32_e32 v61, v169, v61, vcc
	v_mov_b32_e32 v64, v58
	v_mov_b32_e32 v84, v59
	v_pk_fma_f32 v[80:81], v[52:53], v[52:53], v[56:57] op_sel_hi:[1,1,0]
	v_mov_b32_e32 v72, v75
	v_mov_b32_e32 v56, v63
	v_lshlrev_b32_e32 v63, 2, v61
	v_mov_b32_e32 v61, v86
	v_pk_mov_b32 v[50:51], v[54:55], v[50:51] op_sel:[1,0]
	v_pk_add_f32 v[54:55], v[82:83], v[76:77]
	v_pk_add_f32 v[58:59], v[64:65], v[84:85]
	v_pk_add_f32 v[56:57], v[72:73], v[56:57]
	v_pk_add_f32 v[50:51], v[60:61], v[50:51]
	v_pk_add_f32 v[54:55], v[54:55], v[58:59]
	v_mul_f32_e32 v88, v60, v60
	v_pk_add_f32 v[70:71], v[70:71], v[70:71] op_sel_hi:[0,1]
	v_pk_add_f32 v[50:51], v[54:55], v[50:51]
	v_pk_add_f32 v[54:55], v[56:57], v[56:57] op_sel:[0,1] op_sel_hi:[1,0]
	v_mov_b32_e32 v70, v52
	v_mov_b32_e32 v78, v53
	v_mov_b32_e32 v55, v88
	v_mov_b32_e32 v80, v131
	v_pk_add_f32 v[52:53], v[70:71], v[78:79]
	v_pk_add_f32 v[54:55], v[54:55], v[68:69]
	v_pk_add_f32 v[50:51], v[50:51], v[80:81]
	v_pk_add_f32 v[52:53], v[54:55], v[52:53]
	v_xor_b32_e32 v54, 32, v169
	v_pk_add_f32 v[50:51], v[52:53], v[50:51]
	ds_bpermute_b32 v52, v63, v50
	ds_bpermute_b32 v53, v63, v51
	v_cmp_lt_i32_e32 vcc, v54, v62
	s_waitcnt lgkmcnt(0)
	v_pk_add_f32 v[50:51], v[50:51], v[52:53]
	v_cndmask_b32_e32 v54, v169, v54, vcc
	v_lshlrev_b32_e32 v54, 2, v54
	ds_bpermute_b32 v52, v54, v50
	ds_bpermute_b32 v53, v54, v51
	s_and_saveexec_b64 s[0:1], s[6:7]
	s_cbranch_execz .LBB0_265
	s_waitcnt lgkmcnt(0)
	v_pk_add_f32 v[50:51], v[50:51], v[52:53]
	v_lshlrev_b64 v[52:53], 7, v[66:67]
	v_lshl_add_u64 v[52:53], s[12:13], 0, v[52:53]
	global_store_dwordx2 v[52:53], v[50:51], off nt

; __device__ __forceinline__ unsigned cvt_pk_bf16(float lo, float hi) { f32x2 v = {lo, hi}; bf16x2_t b = __builtin_convertvector(v, bf16x2_t); return __builtin_bit_cast(unsigned, b); }
; __device__ __forceinline__ f32x2 gelu_pk(f32x2 v) {
;     const f32x2 av = __builtin_elementwise_abs(v), d = av * 0.2316418882f + 1.0f;
;     f32x2 t; t.x = __builtin_amdgcn_rcpf(d.x); t.y = __builtin_amdgcn_rcpf(d.y);
;     f32x2 q = t * 0.5307027145f + (-0.7265760135f); q = q * t + 0.7107068705f; q = q * t + (-0.142248368f); q = q * t + 0.127414796f; q = q * t;
;     const f32x2 s = (v * v) * (-0.72134752044f);
;     f32x2 e; e.x = __builtin_amdgcn_exp2f(s.x); e.y = __builtin_amdgcn_exp2f(s.y);
;     const f32x2 m = v * (q * e), r = v - m;
;     f32x2 o; o.x = v.x < 0.f ? m.x : r.x; o.y = v.y < 0.f ? m.y : r.y; return o;
; }
; __device__ __forceinline__ f32x4 gelu4(f32x4 v) { f32x2 a = gelu_pk((f32x2){v[0], v[1]}), b = gelu_pk((f32x2){v[2], v[3]}); return (f32x4){a.x, a.y, b.x, b.y}; }
;     __device__ __forceinline__ void operator()(const AccT& acc, const pg8::Unit& u, int wr, int wc, int fr, int fq) const {
;     ...
;                 for (int m = 0; m < 4; ++m) { const int row = row0 + ai * 128 + m * 16; float s = 0.f, q = 0.f;
; #pragma unroll
;                     for (int bj = 0; bj < 2; ++bj) { const f32x4 v0 = gelu4(acc[ai][bj][m][0]), v1 = gelu4(acc[ai][bj][m][1]);
;                         s += (v0[0] + v0[1]) + (v0[2] + v0[3]) + (v1[0] + v1[1]) + (v1[2] + v1[3]);
;                         q += (v0[0] * v0[0] + v0[1] * v0[1]) + (v0[2] * v0[2] + v0[3] * v0[3]) + (v1[0] * v1[0] + v1[1] * v1[1]) + (v1[2] * v1[2] + v1[3] * v1[3]);
;                         u32x4 w; w.x = cvt_pk_bf16(v0[0], v0[1]); w.y = cvt_pk_bf16(v0[2], v0[3]); w.z = cvt_pk_bf16(v1[0], v1[1]); w.w = cvt_pk_bf16(v1[2], v1[3]);
;                         *(u32x4*)(dst + (size_t)row * GW + col0 + bj * 128) = w; }
.LBB0_266:
	s_waitcnt lgkmcnt(0)
	v_and_b32_e32 v53, 0x7fffffff, v47
	v_and_b32_e32 v52, 0x7fffffff, v46
	v_pk_fma_f32 v[52:53], v[52:53], s[28:29], 1.0 op_sel_hi:[1,0,0]
	v_mov_b64_e32 v[54:55], s[34:35]
	v_rcp_f32_e32 v56, v52
	v_rcp_f32_e32 v57, v53
	v_pk_mul_f32 v[60:61], v[46:47], v[46:47]
	v_and_b32_e32 v63, 0x7fffffff, v49
	v_pk_mul_f32 v[60:61], v[60:61], s[42:43] op_sel_hi:[1,0]
	v_pk_fma_f32 v[58:59], v[56:57], s[30:31], v[54:55] op_sel_hi:[1,0,0]
	v_and_b32_e32 v62, 0x7fffffff, v48
	v_pk_fma_f32 v[58:59], v[56:57], v[58:59], s[36:37] op_sel_hi:[1,1,0]
	v_exp_f32_e32 v60, v60
	v_exp_f32_e32 v61, v61
	v_pk_fma_f32 v[62:63], v[62:63], s[28:29], 1.0 op_sel_hi:[1,0,0]
	v_pk_fma_f32 v[58:59], v[56:57], v[58:59], s[38:39] op_sel_hi:[1,1,0]
	v_rcp_f32_e32 v62, v62
	v_rcp_f32_e32 v63, v63
	v_pk_fma_f32 v[58:59], v[56:57], v[58:59], s[40:41] op_sel_hi:[1,1,0]
	v_and_b32_e32 v65, 0x7fffffff, v45
	v_pk_mul_f32 v[56:57], v[56:57], v[58:59]
	v_pk_mul_f32 v[58:59], v[48:49], v[48:49]
	v_pk_mul_f32 v[56:57], v[60:61], v[56:57]
	v_pk_mul_f32 v[58:59], v[58:59], s[42:43] op_sel_hi:[1,0]
	v_pk_mul_f32 v[60:61], v[46:47], v[56:57]
	v_pk_fma_f32 v[66:67], v[46:47], v[56:57], v[46:47] neg_lo:[1,0,0] neg_hi:[1,0,0]
	v_pk_fma_f32 v[56:57], v[62:63], s[30:31], v[54:55] op_sel_hi:[1,0,0]
	v_exp_f32_e32 v58, v58
	v_pk_fma_f32 v[56:57], v[62:63], v[56:57], s[36:37] op_sel_hi:[1,1,0]
	v_exp_f32_e32 v59, v59
	v_pk_fma_f32 v[56:57], v[62:63], v[56:57], s[38:39] op_sel_hi:[1,1,0]
	v_and_b32_e32 v64, 0x7fffffff, v44
	v_pk_fma_f32 v[56:57], v[62:63], v[56:57], s[40:41] op_sel_hi:[1,1,0]
	v_pk_fma_f32 v[64:65], v[64:65], s[28:29], 1.0 op_sel_hi:[1,0,0]
	v_pk_mul_f32 v[56:57], v[62:63], v[56:57]
	v_and_b32_e32 v63, 0x7fffffff, v43
	v_and_b32_e32 v62, 0x7fffffff, v42
	v_pk_fma_f32 v[62:63], v[62:63], s[28:29], 1.0 op_sel_hi:[1,0,0]
	v_pk_mul_f32 v[56:57], v[58:59], v[56:57]
	v_rcp_f32_e32 v62, v62
	v_rcp_f32_e32 v63, v63
	v_pk_mul_f32 v[58:59], v[42:43], v[42:43]
	v_pk_mul_f32 v[68:69], v[48:49], v[56:57]
	v_pk_fma_f32 v[70:71], v[48:49], v[56:57], v[48:49] neg_lo:[1,0,0] neg_hi:[1,0,0]
	v_pk_fma_f32 v[56:57], v[62:63], s[30:31], v[54:55] op_sel_hi:[1,0,0]
	v_pk_mul_f32 v[58:59], v[58:59], s[42:43] op_sel_hi:[1,0]
	v_pk_fma_f32 v[56:57], v[62:63], v[56:57], s[36:37] op_sel_hi:[1,1,0]
	v_exp_f32_e32 v58, v58
	v_exp_f32_e32 v59, v59
	v_pk_fma_f32 v[56:57], v[62:63], v[56:57], s[38:39] op_sel_hi:[1,1,0]
	v_rcp_f32_e32 v64, v64
	v_pk_fma_f32 v[56:57], v[62:63], v[56:57], s[40:41] op_sel_hi:[1,1,0]
	v_rcp_f32_e32 v65, v65
	v_pk_mul_f32 v[56:57], v[62:63], v[56:57]
	v_cmp_gt_f32_e32 vcc, 0, v43
	v_pk_mul_f32 v[56:57], v[58:59], v[56:57]
	v_pk_mul_f32 v[62:63], v[44:45], v[44:45]
	v_pk_mul_f32 v[58:59], v[42:43], v[56:57]
	v_pk_fma_f32 v[56:57], v[42:43], v[56:57], v[42:43] neg_lo:[1,0,0] neg_hi:[1,0,0]
	v_pk_mul_f32 v[72:73], v[38:39], v[38:39]
	v_cndmask_b32_e32 v43, v57, v59, vcc
	v_cmp_gt_f32_e32 vcc, 0, v42
	v_pk_mul_f32 v[72:73], v[72:73], s[42:43] op_sel_hi:[1,0]
	v_and_b32_e32 v75, 0x7fffffff, v41
	v_cndmask_b32_e32 v42, v56, v58, vcc
	v_pk_fma_f32 v[56:57], v[64:65], s[30:31], v[54:55] op_sel_hi:[1,0,0]
	v_pk_mul_f32 v[58:59], v[62:63], s[42:43] op_sel_hi:[1,0]
	v_pk_fma_f32 v[56:57], v[64:65], v[56:57], s[36:37] op_sel_hi:[1,1,0]
	v_exp_f32_e32 v58, v58
	v_exp_f32_e32 v59, v59
	v_pk_fma_f32 v[56:57], v[64:65], v[56:57], s[38:39] op_sel_hi:[1,1,0]
	v_and_b32_e32 v74, 0x7fffffff, v40
	v_pk_fma_f32 v[56:57], v[64:65], v[56:57], s[40:41] op_sel_hi:[1,1,0]
	v_exp_f32_e32 v72, v72
	v_pk_mul_f32 v[56:57], v[64:65], v[56:57]
	v_exp_f32_e32 v73, v73
	v_pk_mul_f32 v[56:57], v[58:59], v[56:57]
	v_pk_fma_f32 v[74:75], v[74:75], s[28:29], 1.0 op_sel_hi:[1,0,0]
	v_pk_mul_f32 v[62:63], v[44:45], v[56:57]
	v_pk_fma_f32 v[64:65], v[44:45], v[56:57], v[44:45] neg_lo:[1,0,0] neg_hi:[1,0,0]
	v_and_b32_e32 v57, 0x7fffffff, v39
	v_and_b32_e32 v56, 0x7fffffff, v38
	v_pk_fma_f32 v[56:57], v[56:57], s[28:29], 1.0 op_sel_hi:[1,0,0]
	v_rcp_f32_e32 v74, v74
	v_rcp_f32_e32 v56, v56
	v_rcp_f32_e32 v57, v57
	v_rcp_f32_e32 v75, v75
	v_cmp_gt_f32_e32 vcc, 0, v44
	v_add_u32_e32 v50, 0x90, v142
	v_pk_fma_f32 v[58:59], v[56:57], s[30:31], v[54:55] op_sel_hi:[1,0,0]
	v_cndmask_b32_e32 v44, v64, v62, vcc
	v_pk_fma_f32 v[58:59], v[56:57], v[58:59], s[36:37] op_sel_hi:[1,1,0]
	v_cmp_gt_f32_e32 vcc, 0, v40
	v_pk_fma_f32 v[58:59], v[56:57], v[58:59], s[38:39] op_sel_hi:[1,1,0]
	v_ashrrev_i32_e32 v51, 31, v50
	v_pk_fma_f32 v[58:59], v[56:57], v[58:59], s[40:41] op_sel_hi:[1,1,0]
	v_lshlrev_b64 v[52:53], 11, v[50:51]
	v_pk_mul_f32 v[56:57], v[56:57], v[58:59]
	v_pk_mul_f32 v[58:59], v[40:41], v[40:41]
	v_pk_mul_f32 v[56:57], v[72:73], v[56:57]
	v_pk_mul_f32 v[58:59], v[58:59], s[42:43] op_sel_hi:[1,0]
	v_pk_mul_f32 v[72:73], v[38:39], v[56:57]
	v_pk_fma_f32 v[76:77], v[38:39], v[56:57], v[38:39] neg_lo:[1,0,0] neg_hi:[1,0,0]
	v_pk_fma_f32 v[56:57], v[74:75], s[30:31], v[54:55] op_sel_hi:[1,0,0]
	v_exp_f32_e32 v58, v58
	v_pk_fma_f32 v[56:57], v[74:75], v[56:57], s[36:37] op_sel_hi:[1,1,0]
	v_exp_f32_e32 v59, v59
	v_pk_fma_f32 v[56:57], v[74:75], v[56:57], s[38:39] op_sel_hi:[1,1,0]
	v_lshl_add_u64 v[52:53], v[144:145], 0, v[52:53]
	v_pk_fma_f32 v[56:57], v[74:75], v[56:57], s[40:41] op_sel_hi:[1,1,0]
	v_cvt_pk_bf16_f32 v64, v42, v43
	v_pk_mul_f32 v[56:57], v[74:75], v[56:57]
	s_nop 0
	v_pk_mul_f32 v[56:57], v[58:59], v[56:57]
	s_nop 0
	v_pk_mul_f32 v[58:59], v[40:41], v[56:57]
	v_pk_fma_f32 v[74:75], v[40:41], v[56:57], v[40:41] neg_lo:[1,0,0] neg_hi:[1,0,0]
	v_and_b32_e32 v57, 0x7fffffff, v35
	v_and_b32_e32 v56, 0x7fffffff, v34
; __device__ __forceinline__ unsigned cvt_pk_bf16(float lo, float hi) { f32x2 v = {lo, hi}; bf16x2_t b = __builtin_convertvector(v, bf16x2_t); return __builtin_bit_cast(unsigned, b); }
; __device__ __forceinline__ f32x2 gelu_pk(f32x2 v) {
;     const f32x2 av = __builtin_elementwise_abs(v), d = av * 0.2316418882f + 1.0f;
;     f32x2 t; t.x = __builtin_amdgcn_rcpf(d.x); t.y = __builtin_amdgcn_rcpf(d.y);
;     f32x2 q = t * 0.5307027145f + (-0.7265760135f); q = q * t + 0.7107068705f; q = q * t + (-0.142248368f); q = q * t + 0.127414796f; q = q * t;
;     const f32x2 s = (v * v) * (-0.72134752044f);
;     f32x2 e; e.x = __builtin_amdgcn_exp2f(s.x); e.y = __builtin_amdgcn_exp2f(s.y);
;     const f32x2 m = v * (q * e), r = v - m;
;     f32x2 o; o.x = v.x < 0.f ? m.x : r.x; o.y = v.y < 0.f ? m.y : r.y; return o;
; }
; __device__ __forceinline__ f32x4 gelu4(f32x4 v) { f32x2 a = gelu_pk((f32x2){v[0], v[1]}), b = gelu_pk((f32x2){v[2], v[3]}); return (f32x4){a.x, a.y, b.x, b.y}; }
;     __device__ __forceinline__ void operator()(const AccT& acc, const pg8::Unit& u, int wr, int wc, int fr, int fq) const {
;     ...
;                 for (int m = 0; m < 4; ++m) { const int row = row0 + ai * 128 + m * 16; float s = 0.f, q = 0.f;
; #pragma unroll
;                     for (int bj = 0; bj < 2; ++bj) { const f32x4 v0 = gelu4(acc[ai][bj][m][0]), v1 = gelu4(acc[ai][bj][m][1]);
;                         s += (v0[0] + v0[1]) + (v0[2] + v0[3]) + (v1[0] + v1[1]) + (v1[2] + v1[3]);
;                         q += (v0[0] * v0[0] + v0[1] * v0[1]) + (v0[2] * v0[2] + v0[3] * v0[3]) + (v1[0] * v1[0] + v1[1] * v1[1]) + (v1[2] * v1[2] + v1[3] * v1[3]);
;                         u32x4 w; w.x = cvt_pk_bf16(v0[0], v0[1]); w.y = cvt_pk_bf16(v0[2], v0[3]); w.z = cvt_pk_bf16(v1[0], v1[1]); w.w = cvt_pk_bf16(v1[2], v1[3]);
;                         *(u32x4*)(dst + (size_t)row * GW + col0 + bj * 128) = w; }
;                     if (pn >= 4) { s += __shfl_xor(s, 16); s += __shfl_xor(s, 32); q += __shfl_xor(q, 16); q += __shfl_xor(q, 32);
;                         if (fq == 0) *(f32x2*)(vstat + (size_t)row * 32 + ((pn - 4) * 4 + wc) * 2) = (f32x2){s, q}; } }
	v_pk_fma_f32 v[56:57], v[56:57], s[28:29], 1.0 op_sel_hi:[1,0,0]
	s_nop 0
	v_rcp_f32_e32 v78, v56
	v_rcp_f32_e32 v79, v57
	v_cndmask_b32_e32 v57, v74, v58, vcc
	v_cmp_gt_f32_e32 vcc, 0, v41
	s_nop 1
	v_cndmask_b32_e32 v41, v75, v59, vcc
	v_pk_mul_f32 v[74:75], v[34:35], v[34:35]
	v_pk_fma_f32 v[58:59], v[78:79], s[30:31], v[54:55] op_sel_hi:[1,0,0]
	v_pk_mul_f32 v[74:75], v[74:75], s[42:43] op_sel_hi:[1,0]
	v_pk_fma_f32 v[58:59], v[78:79], v[58:59], s[36:37] op_sel_hi:[1,1,0]
	v_exp_f32_e32 v74, v74
	v_exp_f32_e32 v75, v75
	v_pk_fma_f32 v[58:59], v[78:79], v[58:59], s[38:39] op_sel_hi:[1,1,0]
	v_cmp_gt_f32_e32 vcc, 0, v46
	v_pk_fma_f32 v[58:59], v[78:79], v[58:59], s[40:41] op_sel_hi:[1,1,0]
	s_nop 0
	v_pk_mul_f32 v[58:59], v[78:79], v[58:59]
	v_pk_mul_f32 v[78:79], v[36:37], v[36:37]
	v_pk_mul_f32 v[58:59], v[74:75], v[58:59]
	s_nop 0
	v_pk_mul_f32 v[74:75], v[34:35], v[58:59]
	v_pk_fma_f32 v[80:81], v[34:35], v[58:59], v[34:35] neg_lo:[1,0,0] neg_hi:[1,0,0]
	v_cndmask_b32_e32 v58, v66, v60, vcc
	v_cmp_gt_f32_e32 vcc, 0, v38
	v_and_b32_e32 v66, 0x7fffffff, v36
	s_nop 0
	v_cndmask_b32_e32 v59, v76, v72, vcc
	v_cmp_gt_f32_e32 vcc, 0, v47
	s_nop 1
	v_cndmask_b32_e32 v60, v67, v61, vcc
	v_cmp_gt_f32_e32 vcc, 0, v48
	v_and_b32_e32 v67, 0x7fffffff, v37
	v_pk_fma_f32 v[66:67], v[66:67], s[28:29], 1.0 op_sel_hi:[1,0,0]
	v_cndmask_b32_e32 v46, v70, v68, vcc
	v_cmp_gt_f32_e32 vcc, 0, v39
	v_rcp_f32_e32 v66, v66
	v_rcp_f32_e32 v67, v67
	v_cndmask_b32_e32 v47, v77, v73, vcc
	v_cmp_gt_f32_e32 vcc, 0, v49
	v_cvt_pk_bf16_f32 v62, v58, v60
	v_pk_fma_f32 v[54:55], v[66:67], s[30:31], v[54:55] op_sel_hi:[1,0,0]
	v_cndmask_b32_e32 v48, v71, v69, vcc
	v_cmp_gt_f32_e32 vcc, 0, v34
	v_pk_fma_f32 v[54:55], v[66:67], v[54:55], s[36:37] op_sel_hi:[1,1,0]
	s_nop 0
	v_cndmask_b32_e32 v38, v80, v74, vcc
	v_cmp_gt_f32_e32 vcc, 0, v45
	v_pk_fma_f32 v[54:55], v[66:67], v[54:55], s[38:39] op_sel_hi:[1,1,0]
	s_nop 0
	v_cndmask_b32_e32 v39, v65, v63, vcc
	v_cvt_pk_bf16_f32 v63, v46, v48
	v_cvt_pk_bf16_f32 v65, v44, v39
	global_store_dwordx4 v[52:53], v[62:65], off nt
	v_pk_fma_f32 v[54:55], v[66:67], v[54:55], s[40:41] op_sel_hi:[1,1,0]
	v_cmp_gt_f32_e32 vcc, 0, v35
	v_pk_mul_f32 v[62:63], v[78:79], s[42:43] op_sel_hi:[1,0]
	v_pk_mul_f32 v[54:55], v[66:67], v[54:55]
	v_exp_f32_e32 v62, v62
	v_exp_f32_e32 v63, v63
	v_cndmask_b32_e32 v34, v81, v75, vcc
	v_cmp_gt_f32_e32 vcc, 0, v37
	v_cvt_pk_bf16_f32 v64, v38, v34
	v_pk_mul_f32 v[54:55], v[62:63], v[54:55]
	s_nop 0
	v_pk_mul_f32 v[62:63], v[36:37], v[54:55]
	v_pk_fma_f32 v[54:55], v[36:37], v[54:55], v[36:37] neg_lo:[1,0,0] neg_hi:[1,0,0]
	s_nop 0
	v_cndmask_b32_e32 v37, v55, v63, vcc
	v_cmp_gt_f32_e32 vcc, 0, v36
	v_cvt_pk_bf16_f32 v63, v57, v41
	s_nop 0
	v_cndmask_b32_e32 v36, v54, v62, vcc
	v_cvt_pk_bf16_f32 v62, v59, v47
	v_cvt_pk_bf16_f32 v65, v36, v37
	s_and_b64 vcc, exec, s[10:11]
	global_store_dwordx4 v[52:53], v[62:65], off offset:256 nt
	s_cbranch_vccnz .LBB0_270
	v_mov_b32_e32 v61, v59
	v_mov_b32_e32 v35, v39
	v_mov_b32_e32 v49, v47
	v_pk_add_f32 v[52:53], v[38:39], v[34:35]
	v_pk_mul_f32 v[54:55], v[38:39], v[34:35]
	v_mov_b32_e32 v62, v60
	v_pk_add_f32 v[66:67], v[58:59], v[60:61]
	v_pk_mul_f32 v[60:61], v[58:59], v[60:61]
	v_mov_b32_e32 v53, v55
	v_mov_b32_e32 v55, v46
	v_mov_b32_e32 v63, v48
	v_mov_b32_e32 v67, v61
	v_pk_add_f32 v[60:61], v[46:47], v[48:49]
	v_pk_mul_f32 v[48:49], v[46:47], v[48:49]
	v_and_b32_e32 v46, 64, v169
	v_xor_b32_e32 v45, 16, v169
	v_add_u32_e32 v46, 64, v46
	v_mov_b32_e32 v54, v58
	v_pk_mul_f32 v[62:63], v[62:63], v[62:63]
	v_mul_f32_e32 v40, v42, v42
	v_cmp_lt_i32_e32 vcc, v45, v46
	v_pk_fma_f32 v[54:55], v[54:55], v[54:55], v[62:63]
	v_pk_fma_f32 v[62:63], v[42:43], v[42:43], v[40:41] op_sel_hi:[1,1,0]
	v_mul_f32_e32 v40, v36, v36
	v_mov_b32_e32 v61, v49
	v_mul_f32_e32 v49, v57, v57
	v_mul_f32_e32 v69, v41, v41
	v_pk_mul_f32 v[70:71], v[38:39], v[38:39]
	v_pk_mul_f32 v[34:35], v[34:35], v[34:35]
	v_cndmask_b32_e32 v45, v169, v45, vcc
	v_mov_b32_e32 v48, v42
	v_mov_b32_e32 v68, v43
	v_pk_fma_f32 v[64:65], v[36:37], v[36:37], v[40:41] op_sel_hi:[1,1,0]
	v_mov_b32_e32 v56, v59
	v_mov_b32_e32 v40, v47
	v_lshlrev_b32_e32 v47, 2, v45
	v_mov_b32_e32 v45, v70
	v_pk_mov_b32 v[34:35], v[38:39], v[34:35] op_sel:[1,0]
	v_pk_add_f32 v[38:39], v[66:67], v[60:61]
	v_pk_add_f32 v[42:43], v[48:49], v[68:69]
	v_pk_add_f32 v[40:41], v[56:57], v[40:41]
	v_pk_add_f32 v[34:35], v[44:45], v[34:35]
	v_pk_add_f32 v[38:39], v[38:39], v[42:43]
	v_mul_f32_e32 v72, v44, v44
	v_pk_add_f32 v[54:55], v[54:55], v[54:55] op_sel_hi:[0,1]
	v_pk_add_f32 v[34:35], v[38:39], v[34:35]
	v_pk_add_f32 v[38:39], v[40:41], v[40:41] op_sel:[0,1] op_sel_hi:[1,0]
	v_mov_b32_e32 v54, v36
	v_mov_b32_e32 v62, v37
	v_mov_b32_e32 v39, v72
	v_mov_b32_e32 v64, v131
	v_pk_add_f32 v[36:37], v[54:55], v[62:63]
	v_pk_add_f32 v[38:39], v[38:39], v[52:53]
	v_pk_add_f32 v[34:35], v[34:35], v[64:65]
	v_pk_add_f32 v[36:37], v[38:39], v[36:37]
	v_xor_b32_e32 v38, 32, v169
	v_pk_add_f32 v[34:35], v[36:37], v[34:35]
	ds_bpermute_b32 v36, v47, v34
	ds_bpermute_b32 v37, v47, v35
	v_cmp_lt_i32_e32 vcc, v38, v46
	s_waitcnt lgkmcnt(0)
	v_pk_add_f32 v[34:35], v[34:35], v[36:37]
	v_cndmask_b32_e32 v38, v169, v38, vcc
	v_lshlrev_b32_e32 v38, 2, v38
	ds_bpermute_b32 v36, v38, v34
	ds_bpermute_b32 v37, v38, v35
	s_and_saveexec_b64 s[0:1], s[6:7]
	s_cbranch_execz .LBB0_269
	s_waitcnt lgkmcnt(0)
	v_pk_add_f32 v[34:35], v[34:35], v[36:37]
	v_lshlrev_b64 v[36:37], 7, v[50:51]
	v_lshl_add_u64 v[36:37], s[12:13], 0, v[36:37]
	global_store_dwordx2 v[36:37], v[34:35], off nt

; __device__ __forceinline__ unsigned cvt_pk_bf16(float lo, float hi) { f32x2 v = {lo, hi}; bf16x2_t b = __builtin_convertvector(v, bf16x2_t); return __builtin_bit_cast(unsigned, b); }
; __device__ __forceinline__ f32x2 gelu_pk(f32x2 v) {
;     const f32x2 av = __builtin_elementwise_abs(v), d = av * 0.2316418882f + 1.0f;
;     f32x2 t; t.x = __builtin_amdgcn_rcpf(d.x); t.y = __builtin_amdgcn_rcpf(d.y);
;     f32x2 q = t * 0.5307027145f + (-0.7265760135f); q = q * t + 0.7107068705f; q = q * t + (-0.142248368f); q = q * t + 0.127414796f; q = q * t;
;     const f32x2 s = (v * v) * (-0.72134752044f);
;     f32x2 e; e.x = __builtin_amdgcn_exp2f(s.x); e.y = __builtin_amdgcn_exp2f(s.y);
;     const f32x2 m = v * (q * e), r = v - m;
;     f32x2 o; o.x = v.x < 0.f ? m.x : r.x; o.y = v.y < 0.f ? m.y : r.y; return o;
; }
; __device__ __forceinline__ f32x4 gelu4(f32x4 v) { f32x2 a = gelu_pk((f32x2){v[0], v[1]}), b = gelu_pk((f32x2){v[2], v[3]}); return (f32x4){a.x, a.y, b.x, b.y}; }
;     __device__ __forceinline__ void operator()(const AccT& acc, const pg8::Unit& u, int wr, int wc, int fr, int fq) const {
;     ...
;                 for (int m = 0; m < 4; ++m) { const int row = row0 + ai * 128 + m * 16; float s = 0.f, q = 0.f;
; #pragma unroll
;                     for (int bj = 0; bj < 2; ++bj) { const f32x4 v0 = gelu4(acc[ai][bj][m][0]), v1 = gelu4(acc[ai][bj][m][1]);
;                         s += (v0[0] + v0[1]) + (v0[2] + v0[3]) + (v1[0] + v1[1]) + (v1[2] + v1[3]);
;                         q += (v0[0] * v0[0] + v0[1] * v0[1]) + (v0[2] * v0[2] + v0[3] * v0[3]) + (v1[0] * v1[0] + v1[1] * v1[1]) + (v1[2] * v1[2] + v1[3] * v1[3]);
;                         u32x4 w; w.x = cvt_pk_bf16(v0[0], v0[1]); w.y = cvt_pk_bf16(v0[2], v0[3]); w.z = cvt_pk_bf16(v1[0], v1[1]); w.w = cvt_pk_bf16(v1[2], v1[3]);
;                         *(u32x4*)(dst + (size_t)row * GW + col0 + bj * 128) = w; }
.LBB0_270:
	s_waitcnt lgkmcnt(0)
	v_and_b32_e32 v37, 0x7fffffff, v31
	v_and_b32_e32 v36, 0x7fffffff, v30
	v_pk_fma_f32 v[36:37], v[36:37], s[28:29], 1.0 op_sel_hi:[1,0,0]
	v_mov_b64_e32 v[38:39], s[34:35]
	v_rcp_f32_e32 v40, v36
	v_rcp_f32_e32 v41, v37
	v_pk_mul_f32 v[44:45], v[30:31], v[30:31]
	v_and_b32_e32 v47, 0x7fffffff, v33
	v_pk_mul_f32 v[44:45], v[44:45], s[42:43] op_sel_hi:[1,0]
	v_pk_fma_f32 v[42:43], v[40:41], s[30:31], v[38:39] op_sel_hi:[1,0,0]
	v_and_b32_e32 v46, 0x7fffffff, v32
	v_pk_fma_f32 v[42:43], v[40:41], v[42:43], s[36:37] op_sel_hi:[1,1,0]
	v_exp_f32_e32 v44, v44
	v_exp_f32_e32 v45, v45
	v_pk_fma_f32 v[46:47], v[46:47], s[28:29], 1.0 op_sel_hi:[1,0,0]
	v_pk_fma_f32 v[42:43], v[40:41], v[42:43], s[38:39] op_sel_hi:[1,1,0]
	v_rcp_f32_e32 v46, v46
	v_rcp_f32_e32 v47, v47
	v_pk_fma_f32 v[42:43], v[40:41], v[42:43], s[40:41] op_sel_hi:[1,1,0]
	v_and_b32_e32 v49, 0x7fffffff, v29
	v_pk_mul_f32 v[40:41], v[40:41], v[42:43]
	v_pk_mul_f32 v[42:43], v[32:33], v[32:33]
	v_pk_mul_f32 v[40:41], v[44:45], v[40:41]
	v_pk_mul_f32 v[42:43], v[42:43], s[42:43] op_sel_hi:[1,0]
	v_pk_mul_f32 v[44:45], v[30:31], v[40:41]
	v_pk_fma_f32 v[50:51], v[30:31], v[40:41], v[30:31] neg_lo:[1,0,0] neg_hi:[1,0,0]
	v_pk_fma_f32 v[40:41], v[46:47], s[30:31], v[38:39] op_sel_hi:[1,0,0]
	v_exp_f32_e32 v42, v42
	v_pk_fma_f32 v[40:41], v[46:47], v[40:41], s[36:37] op_sel_hi:[1,1,0]
	v_exp_f32_e32 v43, v43
	v_pk_fma_f32 v[40:41], v[46:47], v[40:41], s[38:39] op_sel_hi:[1,1,0]
	v_and_b32_e32 v48, 0x7fffffff, v28
	v_pk_fma_f32 v[40:41], v[46:47], v[40:41], s[40:41] op_sel_hi:[1,1,0]
	v_pk_fma_f32 v[48:49], v[48:49], s[28:29], 1.0 op_sel_hi:[1,0,0]
	v_pk_mul_f32 v[40:41], v[46:47], v[40:41]
	v_and_b32_e32 v47, 0x7fffffff, v27
	v_and_b32_e32 v46, 0x7fffffff, v26
	v_pk_fma_f32 v[46:47], v[46:47], s[28:29], 1.0 op_sel_hi:[1,0,0]
	v_pk_mul_f32 v[40:41], v[42:43], v[40:41]
	v_rcp_f32_e32 v46, v46
	v_rcp_f32_e32 v47, v47
	v_pk_mul_f32 v[42:43], v[26:27], v[26:27]
	v_pk_mul_f32 v[52:53], v[32:33], v[40:41]
	v_pk_fma_f32 v[54:55], v[32:33], v[40:41], v[32:33] neg_lo:[1,0,0] neg_hi:[1,0,0]
	v_pk_fma_f32 v[40:41], v[46:47], s[30:31], v[38:39] op_sel_hi:[1,0,0]
	v_pk_mul_f32 v[42:43], v[42:43], s[42:43] op_sel_hi:[1,0]
	v_pk_fma_f32 v[40:41], v[46:47], v[40:41], s[36:37] op_sel_hi:[1,1,0]
	v_exp_f32_e32 v42, v42
	v_exp_f32_e32 v43, v43
	v_pk_fma_f32 v[40:41], v[46:47], v[40:41], s[38:39] op_sel_hi:[1,1,0]
	v_rcp_f32_e32 v48, v48
	v_pk_fma_f32 v[40:41], v[46:47], v[40:41], s[40:41] op_sel_hi:[1,1,0]
	v_rcp_f32_e32 v49, v49
	v_pk_mul_f32 v[40:41], v[46:47], v[40:41]
	v_cmp_gt_f32_e32 vcc, 0, v27
	v_pk_mul_f32 v[40:41], v[42:43], v[40:41]
	v_pk_mul_f32 v[46:47], v[28:29], v[28:29]
	v_pk_mul_f32 v[42:43], v[26:27], v[40:41]
	v_pk_fma_f32 v[40:41], v[26:27], v[40:41], v[26:27] neg_lo:[1,0,0] neg_hi:[1,0,0]
	v_pk_mul_f32 v[56:57], v[22:23], v[22:23]
	v_cndmask_b32_e32 v27, v41, v43, vcc
	v_cmp_gt_f32_e32 vcc, 0, v26
	v_pk_mul_f32 v[56:57], v[56:57], s[42:43] op_sel_hi:[1,0]
	v_and_b32_e32 v59, 0x7fffffff, v25
	v_cndmask_b32_e32 v26, v40, v42, vcc
	v_pk_fma_f32 v[40:41], v[48:49], s[30:31], v[38:39] op_sel_hi:[1,0,0]
	v_pk_mul_f32 v[42:43], v[46:47], s[42:43] op_sel_hi:[1,0]
	v_pk_fma_f32 v[40:41], v[48:49], v[40:41], s[36:37] op_sel_hi:[1,1,0]
	v_exp_f32_e32 v42, v42
	v_exp_f32_e32 v43, v43
	v_pk_fma_f32 v[40:41], v[48:49], v[40:41], s[38:39] op_sel_hi:[1,1,0]
	v_and_b32_e32 v58, 0x7fffffff, v24
	v_pk_fma_f32 v[40:41], v[48:49], v[40:41], s[40:41] op_sel_hi:[1,1,0]
	v_exp_f32_e32 v56, v56
	v_pk_mul_f32 v[40:41], v[48:49], v[40:41]
	v_exp_f32_e32 v57, v57
	v_pk_mul_f32 v[40:41], v[42:43], v[40:41]
	v_pk_fma_f32 v[58:59], v[58:59], s[28:29], 1.0 op_sel_hi:[1,0,0]
	v_pk_mul_f32 v[46:47], v[28:29], v[40:41]
	v_pk_fma_f32 v[48:49], v[28:29], v[40:41], v[28:29] neg_lo:[1,0,0] neg_hi:[1,0,0]
	v_and_b32_e32 v41, 0x7fffffff, v23
	v_and_b32_e32 v40, 0x7fffffff, v22
	v_pk_fma_f32 v[40:41], v[40:41], s[28:29], 1.0 op_sel_hi:[1,0,0]
	v_rcp_f32_e32 v58, v58
	v_rcp_f32_e32 v40, v40
	v_rcp_f32_e32 v41, v41
	v_rcp_f32_e32 v59, v59
	v_cmp_gt_f32_e32 vcc, 0, v28
	v_add_u32_e32 v34, 0xa0, v142
	v_pk_fma_f32 v[42:43], v[40:41], s[30:31], v[38:39] op_sel_hi:[1,0,0]
	v_cndmask_b32_e32 v28, v48, v46, vcc
	v_pk_fma_f32 v[42:43], v[40:41], v[42:43], s[36:37] op_sel_hi:[1,1,0]
	v_cmp_gt_f32_e32 vcc, 0, v24
	v_pk_fma_f32 v[42:43], v[40:41], v[42:43], s[38:39] op_sel_hi:[1,1,0]
	v_ashrrev_i32_e32 v35, 31, v34
	v_pk_fma_f32 v[42:43], v[40:41], v[42:43], s[40:41] op_sel_hi:[1,1,0]
	v_lshlrev_b64 v[36:37], 11, v[34:35]
	v_pk_mul_f32 v[40:41], v[40:41], v[42:43]
	v_pk_mul_f32 v[42:43], v[24:25], v[24:25]
	v_pk_mul_f32 v[40:41], v[56:57], v[40:41]
	v_pk_mul_f32 v[42:43], v[42:43], s[42:43] op_sel_hi:[1,0]
	v_pk_mul_f32 v[56:57], v[22:23], v[40:41]
	v_pk_fma_f32 v[60:61], v[22:23], v[40:41], v[22:23] neg_lo:[1,0,0] neg_hi:[1,0,0]
	v_pk_fma_f32 v[40:41], v[58:59], s[30:31], v[38:39] op_sel_hi:[1,0,0]
	v_exp_f32_e32 v42, v42
	v_pk_fma_f32 v[40:41], v[58:59], v[40:41], s[36:37] op_sel_hi:[1,1,0]
	v_exp_f32_e32 v43, v43
	v_pk_fma_f32 v[40:41], v[58:59], v[40:41], s[38:39] op_sel_hi:[1,1,0]
	v_lshl_add_u64 v[36:37], v[144:145], 0, v[36:37]
	v_pk_fma_f32 v[40:41], v[58:59], v[40:41], s[40:41] op_sel_hi:[1,1,0]
	v_cvt_pk_bf16_f32 v48, v26, v27
	v_pk_mul_f32 v[40:41], v[58:59], v[40:41]
	s_nop 0
	v_pk_mul_f32 v[40:41], v[42:43], v[40:41]
	s_nop 0
	v_pk_mul_f32 v[42:43], v[24:25], v[40:41]
	v_pk_fma_f32 v[58:59], v[24:25], v[40:41], v[24:25] neg_lo:[1,0,0] neg_hi:[1,0,0]
	v_and_b32_e32 v41, 0x7fffffff, v19
	v_and_b32_e32 v40, 0x7fffffff, v18
; __device__ __forceinline__ unsigned cvt_pk_bf16(float lo, float hi) { f32x2 v = {lo, hi}; bf16x2_t b = __builtin_convertvector(v, bf16x2_t); return __builtin_bit_cast(unsigned, b); }
; __device__ __forceinline__ f32x2 gelu_pk(f32x2 v) {
;     const f32x2 av = __builtin_elementwise_abs(v), d = av * 0.2316418882f + 1.0f;
;     f32x2 t; t.x = __builtin_amdgcn_rcpf(d.x); t.y = __builtin_amdgcn_rcpf(d.y);
;     f32x2 q = t * 0.5307027145f + (-0.7265760135f); q = q * t + 0.7107068705f; q = q * t + (-0.142248368f); q = q * t + 0.127414796f; q = q * t;
;     const f32x2 s = (v * v) * (-0.72134752044f);
;     f32x2 e; e.x = __builtin_amdgcn_exp2f(s.x); e.y = __builtin_amdgcn_exp2f(s.y);
;     const f32x2 m = v * (q * e), r = v - m;
;     f32x2 o; o.x = v.x < 0.f ? m.x : r.x; o.y = v.y < 0.f ? m.y : r.y; return o;
; }
; __device__ __forceinline__ f32x4 gelu4(f32x4 v) { f32x2 a = gelu_pk((f32x2){v[0], v[1]}), b = gelu_pk((f32x2){v[2], v[3]}); return (f32x4){a.x, a.y, b.x, b.y}; }
;     __device__ __forceinline__ void operator()(const AccT& acc, const pg8::Unit& u, int wr, int wc, int fr, int fq) const {
;     ...
;                 for (int m = 0; m < 4; ++m) { const int row = row0 + ai * 128 + m * 16; float s = 0.f, q = 0.f;
; #pragma unroll
;                     for (int bj = 0; bj < 2; ++bj) { const f32x4 v0 = gelu4(acc[ai][bj][m][0]), v1 = gelu4(acc[ai][bj][m][1]);
;                         s += (v0[0] + v0[1]) + (v0[2] + v0[3]) + (v1[0] + v1[1]) + (v1[2] + v1[3]);
;                         q += (v0[0] * v0[0] + v0[1] * v0[1]) + (v0[2] * v0[2] + v0[3] * v0[3]) + (v1[0] * v1[0] + v1[1] * v1[1]) + (v1[2] * v1[2] + v1[3] * v1[3]);
;                         u32x4 w; w.x = cvt_pk_bf16(v0[0], v0[1]); w.y = cvt_pk_bf16(v0[2], v0[3]); w.z = cvt_pk_bf16(v1[0], v1[1]); w.w = cvt_pk_bf16(v1[2], v1[3]);
;                         *(u32x4*)(dst + (size_t)row * GW + col0 + bj * 128) = w; }
;                     if (pn >= 4) { s += __shfl_xor(s, 16); s += __shfl_xor(s, 32); q += __shfl_xor(q, 16); q += __shfl_xor(q, 32);
;                         if (fq == 0) *(f32x2*)(vstat + (size_t)row * 32 + ((pn - 4) * 4 + wc) * 2) = (f32x2){s, q}; } }
	v_pk_fma_f32 v[40:41], v[40:41], s[28:29], 1.0 op_sel_hi:[1,0,0]
	s_nop 0
	v_rcp_f32_e32 v62, v40
	v_rcp_f32_e32 v63, v41
	v_cndmask_b32_e32 v41, v58, v42, vcc
	v_cmp_gt_f32_e32 vcc, 0, v25
	s_nop 1
	v_cndmask_b32_e32 v25, v59, v43, vcc
	v_pk_mul_f32 v[58:59], v[18:19], v[18:19]
	v_pk_fma_f32 v[42:43], v[62:63], s[30:31], v[38:39] op_sel_hi:[1,0,0]
	v_pk_mul_f32 v[58:59], v[58:59], s[42:43] op_sel_hi:[1,0]
	v_pk_fma_f32 v[42:43], v[62:63], v[42:43], s[36:37] op_sel_hi:[1,1,0]
	v_exp_f32_e32 v58, v58
	v_exp_f32_e32 v59, v59
	v_pk_fma_f32 v[42:43], v[62:63], v[42:43], s[38:39] op_sel_hi:[1,1,0]
	v_cmp_gt_f32_e32 vcc, 0, v30
	v_pk_fma_f32 v[42:43], v[62:63], v[42:43], s[40:41] op_sel_hi:[1,1,0]
	s_nop 0
	v_pk_mul_f32 v[42:43], v[62:63], v[42:43]
	v_pk_mul_f32 v[62:63], v[20:21], v[20:21]
	v_pk_mul_f32 v[42:43], v[58:59], v[42:43]
	s_nop 0
	v_pk_mul_f32 v[58:59], v[18:19], v[42:43]
	v_pk_fma_f32 v[64:65], v[18:19], v[42:43], v[18:19] neg_lo:[1,0,0] neg_hi:[1,0,0]
	v_cndmask_b32_e32 v42, v50, v44, vcc
	v_cmp_gt_f32_e32 vcc, 0, v22
	v_and_b32_e32 v50, 0x7fffffff, v20
	s_nop 0
	v_cndmask_b32_e32 v43, v60, v56, vcc
	v_cmp_gt_f32_e32 vcc, 0, v31
	s_nop 1
	v_cndmask_b32_e32 v44, v51, v45, vcc
	v_cmp_gt_f32_e32 vcc, 0, v32
	v_and_b32_e32 v51, 0x7fffffff, v21
	v_pk_fma_f32 v[50:51], v[50:51], s[28:29], 1.0 op_sel_hi:[1,0,0]
	v_cndmask_b32_e32 v30, v54, v52, vcc
	v_cmp_gt_f32_e32 vcc, 0, v23
	v_rcp_f32_e32 v50, v50
	v_rcp_f32_e32 v51, v51
	v_cndmask_b32_e32 v31, v61, v57, vcc
	v_cmp_gt_f32_e32 vcc, 0, v33
	v_cvt_pk_bf16_f32 v46, v42, v44
	v_pk_fma_f32 v[38:39], v[50:51], s[30:31], v[38:39] op_sel_hi:[1,0,0]
	v_cndmask_b32_e32 v32, v55, v53, vcc
	v_cmp_gt_f32_e32 vcc, 0, v18
	v_pk_fma_f32 v[38:39], v[50:51], v[38:39], s[36:37] op_sel_hi:[1,1,0]
	s_nop 0
	v_cndmask_b32_e32 v22, v64, v58, vcc
	v_cmp_gt_f32_e32 vcc, 0, v29
	v_pk_fma_f32 v[38:39], v[50:51], v[38:39], s[38:39] op_sel_hi:[1,1,0]
	s_nop 0
	v_cndmask_b32_e32 v23, v49, v47, vcc
	v_cvt_pk_bf16_f32 v47, v30, v32
	v_cvt_pk_bf16_f32 v49, v28, v23
	global_store_dwordx4 v[36:37], v[46:49], off nt
	v_pk_fma_f32 v[38:39], v[50:51], v[38:39], s[40:41] op_sel_hi:[1,1,0]
	v_cmp_gt_f32_e32 vcc, 0, v19
	v_pk_mul_f32 v[46:47], v[62:63], s[42:43] op_sel_hi:[1,0]
	v_pk_mul_f32 v[38:39], v[50:51], v[38:39]
	v_exp_f32_e32 v46, v46
	v_exp_f32_e32 v47, v47
	v_cndmask_b32_e32 v18, v65, v59, vcc
	v_cmp_gt_f32_e32 vcc, 0, v21
	v_cvt_pk_bf16_f32 v48, v22, v18
	v_pk_mul_f32 v[38:39], v[46:47], v[38:39]
	s_nop 0
	v_pk_mul_f32 v[46:47], v[20:21], v[38:39]
	v_pk_fma_f32 v[38:39], v[20:21], v[38:39], v[20:21] neg_lo:[1,0,0] neg_hi:[1,0,0]
	s_nop 0
	v_cndmask_b32_e32 v21, v39, v47, vcc
	v_cmp_gt_f32_e32 vcc, 0, v20
	v_cvt_pk_bf16_f32 v47, v41, v25
	s_nop 0
	v_cndmask_b32_e32 v20, v38, v46, vcc
	v_cvt_pk_bf16_f32 v46, v43, v31
	v_cvt_pk_bf16_f32 v49, v20, v21
	s_and_b64 vcc, exec, s[10:11]
	global_store_dwordx4 v[36:37], v[46:49], off offset:256 nt
	s_cbranch_vccnz .LBB0_274
	v_mov_b32_e32 v45, v43
	v_mov_b32_e32 v19, v23
	v_mov_b32_e32 v33, v31
	v_pk_add_f32 v[36:37], v[22:23], v[18:19]
	v_pk_mul_f32 v[38:39], v[22:23], v[18:19]
	v_mov_b32_e32 v46, v44
	v_pk_add_f32 v[50:51], v[42:43], v[44:45]
	v_pk_mul_f32 v[44:45], v[42:43], v[44:45]
	v_mov_b32_e32 v37, v39
	v_mov_b32_e32 v39, v30
	v_mov_b32_e32 v47, v32
	v_mov_b32_e32 v51, v45
	v_pk_add_f32 v[44:45], v[30:31], v[32:33]
	v_pk_mul_f32 v[32:33], v[30:31], v[32:33]
	v_and_b32_e32 v30, 64, v169
	v_xor_b32_e32 v29, 16, v169
	v_add_u32_e32 v30, 64, v30
	v_mov_b32_e32 v38, v42
	v_pk_mul_f32 v[46:47], v[46:47], v[46:47]
	v_mul_f32_e32 v24, v26, v26
	v_cmp_lt_i32_e32 vcc, v29, v30
	v_pk_fma_f32 v[38:39], v[38:39], v[38:39], v[46:47]
	v_pk_fma_f32 v[46:47], v[26:27], v[26:27], v[24:25] op_sel_hi:[1,1,0]
	v_mul_f32_e32 v24, v20, v20
	v_mov_b32_e32 v45, v33
	v_mul_f32_e32 v33, v41, v41
	v_mul_f32_e32 v53, v25, v25
	v_pk_mul_f32 v[54:55], v[22:23], v[22:23]
	v_pk_mul_f32 v[18:19], v[18:19], v[18:19]
	v_cndmask_b32_e32 v29, v169, v29, vcc
	v_mov_b32_e32 v32, v26
	v_mov_b32_e32 v52, v27
	v_pk_fma_f32 v[48:49], v[20:21], v[20:21], v[24:25] op_sel_hi:[1,1,0]
	v_mov_b32_e32 v40, v43
	v_mov_b32_e32 v24, v31
	v_lshlrev_b32_e32 v31, 2, v29
	v_mov_b32_e32 v29, v54
	v_pk_mov_b32 v[18:19], v[22:23], v[18:19] op_sel:[1,0]
	v_pk_add_f32 v[22:23], v[50:51], v[44:45]
	v_pk_add_f32 v[26:27], v[32:33], v[52:53]
	v_pk_add_f32 v[24:25], v[40:41], v[24:25]
	v_pk_add_f32 v[18:19], v[28:29], v[18:19]
	v_pk_add_f32 v[22:23], v[22:23], v[26:27]
	v_mul_f32_e32 v56, v28, v28
	v_pk_add_f32 v[38:39], v[38:39], v[38:39] op_sel_hi:[0,1]
	v_pk_add_f32 v[18:19], v[22:23], v[18:19]
	v_pk_add_f32 v[22:23], v[24:25], v[24:25] op_sel:[0,1] op_sel_hi:[1,0]
	v_mov_b32_e32 v38, v20
	v_mov_b32_e32 v46, v21
	v_mov_b32_e32 v23, v56
	v_mov_b32_e32 v48, v131
	v_pk_add_f32 v[20:21], v[38:39], v[46:47]
	v_pk_add_f32 v[22:23], v[22:23], v[36:37]
	v_pk_add_f32 v[18:19], v[18:19], v[48:49]
	v_pk_add_f32 v[20:21], v[22:23], v[20:21]
	v_xor_b32_e32 v22, 32, v169
	v_pk_add_f32 v[18:19], v[20:21], v[18:19]
	ds_bpermute_b32 v20, v31, v18
	ds_bpermute_b32 v21, v31, v19
	v_cmp_lt_i32_e32 vcc, v22, v30
	s_waitcnt lgkmcnt(0)
	v_pk_add_f32 v[18:19], v[18:19], v[20:21]
	v_cndmask_b32_e32 v22, v169, v22, vcc
	v_lshlrev_b32_e32 v22, 2, v22
	ds_bpermute_b32 v20, v22, v18
	ds_bpermute_b32 v21, v22, v19
	s_and_saveexec_b64 s[0:1], s[6:7]
	s_cbranch_execz .LBB0_273
	s_waitcnt lgkmcnt(0)
	v_pk_add_f32 v[18:19], v[18:19], v[20:21]
	v_lshlrev_b64 v[20:21], 7, v[34:35]
	v_lshl_add_u64 v[20:21], s[12:13], 0, v[20:21]
	global_store_dwordx2 v[20:21], v[18:19], off nt

; __device__ __forceinline__ unsigned cvt_pk_bf16(float lo, float hi) { f32x2 v = {lo, hi}; bf16x2_t b = __builtin_convertvector(v, bf16x2_t); return __builtin_bit_cast(unsigned, b); }
; __device__ __forceinline__ f32x2 gelu_pk(f32x2 v) {
;     const f32x2 av = __builtin_elementwise_abs(v), d = av * 0.2316418882f + 1.0f;
;     f32x2 t; t.x = __builtin_amdgcn_rcpf(d.x); t.y = __builtin_amdgcn_rcpf(d.y);
;     f32x2 q = t * 0.5307027145f + (-0.7265760135f); q = q * t + 0.7107068705f; q = q * t + (-0.142248368f); q = q * t + 0.127414796f; q = q * t;
;     const f32x2 s = (v * v) * (-0.72134752044f);
;     f32x2 e; e.x = __builtin_amdgcn_exp2f(s.x); e.y = __builtin_amdgcn_exp2f(s.y);
;     const f32x2 m = v * (q * e), r = v - m;
;     f32x2 o; o.x = v.x < 0.f ? m.x : r.x; o.y = v.y < 0.f ? m.y : r.y; return o;
; }
; __device__ __forceinline__ f32x4 gelu4(f32x4 v) { f32x2 a = gelu_pk((f32x2){v[0], v[1]}), b = gelu_pk((f32x2){v[2], v[3]}); return (f32x4){a.x, a.y, b.x, b.y}; }
;     __device__ __forceinline__ void operator()(const AccT& acc, const pg8::Unit& u, int wr, int wc, int fr, int fq) const {
;     ...
;                 for (int m = 0; m < 4; ++m) { const int row = row0 + ai * 128 + m * 16; float s = 0.f, q = 0.f;
; #pragma unroll
;                     for (int bj = 0; bj < 2; ++bj) { const f32x4 v0 = gelu4(acc[ai][bj][m][0]), v1 = gelu4(acc[ai][bj][m][1]);
;                         s += (v0[0] + v0[1]) + (v0[2] + v0[3]) + (v1[0] + v1[1]) + (v1[2] + v1[3]);
;                         q += (v0[0] * v0[0] + v0[1] * v0[1]) + (v0[2] * v0[2] + v0[3] * v0[3]) + (v1[0] * v1[0] + v1[1] * v1[1]) + (v1[2] * v1[2] + v1[3] * v1[3]);
;                         u32x4 w; w.x = cvt_pk_bf16(v0[0], v0[1]); w.y = cvt_pk_bf16(v0[2], v0[3]); w.z = cvt_pk_bf16(v1[0], v1[1]); w.w = cvt_pk_bf16(v1[2], v1[3]);
;                         *(u32x4*)(dst + (size_t)row * GW + col0 + bj * 128) = w; }
.LBB0_274:
	s_waitcnt lgkmcnt(0)
	v_and_b32_e32 v21, 0x7fffffff, v15
	v_and_b32_e32 v20, 0x7fffffff, v14
	v_pk_fma_f32 v[20:21], v[20:21], s[28:29], 1.0 op_sel_hi:[1,0,0]
	v_mov_b64_e32 v[22:23], s[34:35]
	v_rcp_f32_e32 v24, v20
	v_rcp_f32_e32 v25, v21
	v_pk_mul_f32 v[28:29], v[14:15], v[14:15]
	v_and_b32_e32 v31, 0x7fffffff, v17
	v_pk_mul_f32 v[28:29], v[28:29], s[42:43] op_sel_hi:[1,0]
	v_pk_fma_f32 v[26:27], v[24:25], s[30:31], v[22:23] op_sel_hi:[1,0,0]
	v_and_b32_e32 v30, 0x7fffffff, v16
	v_pk_fma_f32 v[26:27], v[24:25], v[26:27], s[36:37] op_sel_hi:[1,1,0]
	v_exp_f32_e32 v28, v28
	v_exp_f32_e32 v29, v29
	v_pk_fma_f32 v[30:31], v[30:31], s[28:29], 1.0 op_sel_hi:[1,0,0]
	v_pk_fma_f32 v[26:27], v[24:25], v[26:27], s[38:39] op_sel_hi:[1,1,0]
	v_rcp_f32_e32 v30, v30
	v_rcp_f32_e32 v31, v31
	v_pk_fma_f32 v[26:27], v[24:25], v[26:27], s[40:41] op_sel_hi:[1,1,0]
	v_and_b32_e32 v33, 0x7fffffff, v13
	v_pk_mul_f32 v[24:25], v[24:25], v[26:27]
	v_pk_mul_f32 v[26:27], v[16:17], v[16:17]
	v_pk_mul_f32 v[24:25], v[28:29], v[24:25]
	v_pk_mul_f32 v[26:27], v[26:27], s[42:43] op_sel_hi:[1,0]
	v_pk_mul_f32 v[28:29], v[14:15], v[24:25]
	v_pk_fma_f32 v[34:35], v[14:15], v[24:25], v[14:15] neg_lo:[1,0,0] neg_hi:[1,0,0]
	v_pk_fma_f32 v[24:25], v[30:31], s[30:31], v[22:23] op_sel_hi:[1,0,0]
	v_exp_f32_e32 v26, v26
	v_pk_fma_f32 v[24:25], v[30:31], v[24:25], s[36:37] op_sel_hi:[1,1,0]
	v_exp_f32_e32 v27, v27
	v_pk_fma_f32 v[24:25], v[30:31], v[24:25], s[38:39] op_sel_hi:[1,1,0]
	v_and_b32_e32 v32, 0x7fffffff, v12
	v_pk_fma_f32 v[24:25], v[30:31], v[24:25], s[40:41] op_sel_hi:[1,1,0]
	v_pk_fma_f32 v[32:33], v[32:33], s[28:29], 1.0 op_sel_hi:[1,0,0]
	v_pk_mul_f32 v[24:25], v[30:31], v[24:25]
	v_and_b32_e32 v31, 0x7fffffff, v11
	v_and_b32_e32 v30, 0x7fffffff, v10
	v_pk_fma_f32 v[30:31], v[30:31], s[28:29], 1.0 op_sel_hi:[1,0,0]
	v_pk_mul_f32 v[24:25], v[26:27], v[24:25]
	v_rcp_f32_e32 v30, v30
	v_rcp_f32_e32 v31, v31
	v_pk_mul_f32 v[26:27], v[10:11], v[10:11]
	v_pk_mul_f32 v[36:37], v[16:17], v[24:25]
	v_pk_fma_f32 v[38:39], v[16:17], v[24:25], v[16:17] neg_lo:[1,0,0] neg_hi:[1,0,0]
	v_pk_fma_f32 v[24:25], v[30:31], s[30:31], v[22:23] op_sel_hi:[1,0,0]
	v_pk_mul_f32 v[26:27], v[26:27], s[42:43] op_sel_hi:[1,0]
	v_pk_fma_f32 v[24:25], v[30:31], v[24:25], s[36:37] op_sel_hi:[1,1,0]
	v_exp_f32_e32 v26, v26
	v_exp_f32_e32 v27, v27
	v_pk_fma_f32 v[24:25], v[30:31], v[24:25], s[38:39] op_sel_hi:[1,1,0]
	v_rcp_f32_e32 v32, v32
	v_pk_fma_f32 v[24:25], v[30:31], v[24:25], s[40:41] op_sel_hi:[1,1,0]
	v_rcp_f32_e32 v33, v33
	v_pk_mul_f32 v[24:25], v[30:31], v[24:25]
	v_cmp_gt_f32_e32 vcc, 0, v11
	v_pk_mul_f32 v[24:25], v[26:27], v[24:25]
	v_pk_mul_f32 v[30:31], v[12:13], v[12:13]
	v_pk_mul_f32 v[26:27], v[10:11], v[24:25]
	v_pk_fma_f32 v[24:25], v[10:11], v[24:25], v[10:11] neg_lo:[1,0,0] neg_hi:[1,0,0]
	v_pk_mul_f32 v[40:41], v[6:7], v[6:7]
	v_cndmask_b32_e32 v11, v25, v27, vcc
	v_cmp_gt_f32_e32 vcc, 0, v10
	v_pk_mul_f32 v[40:41], v[40:41], s[42:43] op_sel_hi:[1,0]
	v_and_b32_e32 v43, 0x7fffffff, v9
	v_cndmask_b32_e32 v10, v24, v26, vcc
	v_pk_fma_f32 v[24:25], v[32:33], s[30:31], v[22:23] op_sel_hi:[1,0,0]
	v_pk_mul_f32 v[26:27], v[30:31], s[42:43] op_sel_hi:[1,0]
	v_pk_fma_f32 v[24:25], v[32:33], v[24:25], s[36:37] op_sel_hi:[1,1,0]
	v_exp_f32_e32 v26, v26
	v_exp_f32_e32 v27, v27
	v_pk_fma_f32 v[24:25], v[32:33], v[24:25], s[38:39] op_sel_hi:[1,1,0]
	v_and_b32_e32 v42, 0x7fffffff, v8
	v_pk_fma_f32 v[24:25], v[32:33], v[24:25], s[40:41] op_sel_hi:[1,1,0]
	v_exp_f32_e32 v40, v40
	v_pk_mul_f32 v[24:25], v[32:33], v[24:25]
	v_exp_f32_e32 v41, v41
	v_pk_mul_f32 v[24:25], v[26:27], v[24:25]
	v_pk_fma_f32 v[42:43], v[42:43], s[28:29], 1.0 op_sel_hi:[1,0,0]
	v_pk_mul_f32 v[30:31], v[12:13], v[24:25]
	v_pk_fma_f32 v[32:33], v[12:13], v[24:25], v[12:13] neg_lo:[1,0,0] neg_hi:[1,0,0]
	v_and_b32_e32 v25, 0x7fffffff, v7
	v_and_b32_e32 v24, 0x7fffffff, v6
	v_pk_fma_f32 v[24:25], v[24:25], s[28:29], 1.0 op_sel_hi:[1,0,0]
	v_rcp_f32_e32 v42, v42
	v_rcp_f32_e32 v24, v24
	v_rcp_f32_e32 v25, v25
	v_rcp_f32_e32 v43, v43
	v_cmp_gt_f32_e32 vcc, 0, v12
	v_add_u32_e32 v18, 0xb0, v142
	v_pk_fma_f32 v[26:27], v[24:25], s[30:31], v[22:23] op_sel_hi:[1,0,0]
	v_cndmask_b32_e32 v12, v32, v30, vcc
	v_pk_fma_f32 v[26:27], v[24:25], v[26:27], s[36:37] op_sel_hi:[1,1,0]
	v_cmp_gt_f32_e32 vcc, 0, v8
	v_pk_fma_f32 v[26:27], v[24:25], v[26:27], s[38:39] op_sel_hi:[1,1,0]
	v_ashrrev_i32_e32 v19, 31, v18
	v_pk_fma_f32 v[26:27], v[24:25], v[26:27], s[40:41] op_sel_hi:[1,1,0]
	v_lshlrev_b64 v[20:21], 11, v[18:19]
	v_pk_mul_f32 v[24:25], v[24:25], v[26:27]
	v_pk_mul_f32 v[26:27], v[8:9], v[8:9]
	v_pk_mul_f32 v[24:25], v[40:41], v[24:25]
	v_pk_mul_f32 v[26:27], v[26:27], s[42:43] op_sel_hi:[1,0]
	v_pk_mul_f32 v[40:41], v[6:7], v[24:25]
	v_pk_fma_f32 v[44:45], v[6:7], v[24:25], v[6:7] neg_lo:[1,0,0] neg_hi:[1,0,0]
	v_pk_fma_f32 v[24:25], v[42:43], s[30:31], v[22:23] op_sel_hi:[1,0,0]
	v_exp_f32_e32 v26, v26
	v_pk_fma_f32 v[24:25], v[42:43], v[24:25], s[36:37] op_sel_hi:[1,1,0]
	v_exp_f32_e32 v27, v27
	v_pk_fma_f32 v[24:25], v[42:43], v[24:25], s[38:39] op_sel_hi:[1,1,0]
	v_lshl_add_u64 v[20:21], v[144:145], 0, v[20:21]
	v_pk_fma_f32 v[24:25], v[42:43], v[24:25], s[40:41] op_sel_hi:[1,1,0]
	v_cvt_pk_bf16_f32 v32, v10, v11
	v_pk_mul_f32 v[24:25], v[42:43], v[24:25]
	s_nop 0
	v_pk_mul_f32 v[24:25], v[26:27], v[24:25]
	s_nop 0
	v_pk_mul_f32 v[26:27], v[8:9], v[24:25]
	v_pk_fma_f32 v[42:43], v[8:9], v[24:25], v[8:9] neg_lo:[1,0,0] neg_hi:[1,0,0]
; __device__ __forceinline__ unsigned cvt_pk_bf16(float lo, float hi) { f32x2 v = {lo, hi}; bf16x2_t b = __builtin_convertvector(v, bf16x2_t); return __builtin_bit_cast(unsigned, b); }
; __device__ __forceinline__ f32x2 gelu_pk(f32x2 v) {
;     const f32x2 av = __builtin_elementwise_abs(v), d = av * 0.2316418882f + 1.0f;
;     f32x2 t; t.x = __builtin_amdgcn_rcpf(d.x); t.y = __builtin_amdgcn_rcpf(d.y);
;     f32x2 q = t * 0.5307027145f + (-0.7265760135f); q = q * t + 0.7107068705f; q = q * t + (-0.142248368f); q = q * t + 0.127414796f; q = q * t;
;     const f32x2 s = (v * v) * (-0.72134752044f);
;     f32x2 e; e.x = __builtin_amdgcn_exp2f(s.x); e.y = __builtin_amdgcn_exp2f(s.y);
;     const f32x2 m = v * (q * e), r = v - m;
;     f32x2 o; o.x = v.x < 0.f ? m.x : r.x; o.y = v.y < 0.f ? m.y : r.y; return o;
; }
; __device__ __forceinline__ f32x4 gelu4(f32x4 v) { f32x2 a = gelu_pk((f32x2){v[0], v[1]}), b = gelu_pk((f32x2){v[2], v[3]}); return (f32x4){a.x, a.y, b.x, b.y}; }
;     __device__ __forceinline__ void operator()(const AccT& acc, const pg8::Unit& u, int wr, int wc, int fr, int fq) const {
;     ...
;                 for (int m = 0; m < 4; ++m) { const int row = row0 + ai * 128 + m * 16; float s = 0.f, q = 0.f;
; #pragma unroll
;                     for (int bj = 0; bj < 2; ++bj) { const f32x4 v0 = gelu4(acc[ai][bj][m][0]), v1 = gelu4(acc[ai][bj][m][1]);
;                         s += (v0[0] + v0[1]) + (v0[2] + v0[3]) + (v1[0] + v1[1]) + (v1[2] + v1[3]);
;                         q += (v0[0] * v0[0] + v0[1] * v0[1]) + (v0[2] * v0[2] + v0[3] * v0[3]) + (v1[0] * v1[0] + v1[1] * v1[1]) + (v1[2] * v1[2] + v1[3] * v1[3]);
;                         u32x4 w; w.x = cvt_pk_bf16(v0[0], v0[1]); w.y = cvt_pk_bf16(v0[2], v0[3]); w.z = cvt_pk_bf16(v1[0], v1[1]); w.w = cvt_pk_bf16(v1[2], v1[3]);
;                         *(u32x4*)(dst + (size_t)row * GW + col0 + bj * 128) = w; }
;                     if (pn >= 4) { s += __shfl_xor(s, 16); s += __shfl_xor(s, 32); q += __shfl_xor(q, 16); q += __shfl_xor(q, 32);
;                         if (fq == 0) *(f32x2*)(vstat + (size_t)row * 32 + ((pn - 4) * 4 + wc) * 2) = (f32x2){s, q}; } }
	v_and_b32_e32 v25, 0x7fffffff, v3
	v_and_b32_e32 v24, 0x7fffffff, v2
	v_pk_fma_f32 v[24:25], v[24:25], s[28:29], 1.0 op_sel_hi:[1,0,0]
	s_nop 0
	v_rcp_f32_e32 v46, v24
	v_rcp_f32_e32 v47, v25
	v_cndmask_b32_e32 v25, v42, v26, vcc
	v_cmp_gt_f32_e32 vcc, 0, v9
	s_nop 1
	v_cndmask_b32_e32 v9, v43, v27, vcc
	v_pk_mul_f32 v[42:43], v[2:3], v[2:3]
	v_pk_fma_f32 v[26:27], v[46:47], s[30:31], v[22:23] op_sel_hi:[1,0,0]
	v_pk_mul_f32 v[42:43], v[42:43], s[42:43] op_sel_hi:[1,0]
	v_pk_fma_f32 v[26:27], v[46:47], v[26:27], s[36:37] op_sel_hi:[1,1,0]
	v_exp_f32_e32 v42, v42
	v_exp_f32_e32 v43, v43
	v_pk_fma_f32 v[26:27], v[46:47], v[26:27], s[38:39] op_sel_hi:[1,1,0]
	v_cmp_gt_f32_e32 vcc, 0, v14
	v_pk_fma_f32 v[26:27], v[46:47], v[26:27], s[40:41] op_sel_hi:[1,1,0]
	s_nop 0
	v_pk_mul_f32 v[26:27], v[46:47], v[26:27]
	v_pk_mul_f32 v[46:47], v[4:5], v[4:5]
	v_pk_mul_f32 v[26:27], v[42:43], v[26:27]
	s_nop 0
	v_pk_mul_f32 v[42:43], v[2:3], v[26:27]
	v_pk_fma_f32 v[48:49], v[2:3], v[26:27], v[2:3] neg_lo:[1,0,0] neg_hi:[1,0,0]
	v_cndmask_b32_e32 v26, v34, v28, vcc
	v_cmp_gt_f32_e32 vcc, 0, v6
	v_and_b32_e32 v34, 0x7fffffff, v4
	s_nop 0
	v_cndmask_b32_e32 v27, v44, v40, vcc
	v_cmp_gt_f32_e32 vcc, 0, v15
	s_nop 1
	v_cndmask_b32_e32 v28, v35, v29, vcc
	v_cmp_gt_f32_e32 vcc, 0, v16
	v_and_b32_e32 v35, 0x7fffffff, v5
	v_pk_fma_f32 v[34:35], v[34:35], s[28:29], 1.0 op_sel_hi:[1,0,0]
	v_cndmask_b32_e32 v14, v38, v36, vcc
	v_cmp_gt_f32_e32 vcc, 0, v7
	v_rcp_f32_e32 v34, v34
	v_rcp_f32_e32 v35, v35
	v_cndmask_b32_e32 v15, v45, v41, vcc
	v_cmp_gt_f32_e32 vcc, 0, v17
	v_cvt_pk_bf16_f32 v30, v26, v28
	v_pk_fma_f32 v[22:23], v[34:35], s[30:31], v[22:23] op_sel_hi:[1,0,0]
	v_cndmask_b32_e32 v16, v39, v37, vcc
	v_cmp_gt_f32_e32 vcc, 0, v2
	v_pk_fma_f32 v[22:23], v[34:35], v[22:23], s[36:37] op_sel_hi:[1,1,0]
	s_nop 0
	v_cndmask_b32_e32 v6, v48, v42, vcc
	v_cmp_gt_f32_e32 vcc, 0, v13
	v_pk_fma_f32 v[22:23], v[34:35], v[22:23], s[38:39] op_sel_hi:[1,1,0]
	s_nop 0
	v_cndmask_b32_e32 v7, v33, v31, vcc
	v_cvt_pk_bf16_f32 v31, v14, v16
	v_cvt_pk_bf16_f32 v33, v12, v7
	global_store_dwordx4 v[20:21], v[30:33], off nt
	v_pk_fma_f32 v[22:23], v[34:35], v[22:23], s[40:41] op_sel_hi:[1,1,0]
	v_cmp_gt_f32_e32 vcc, 0, v3
	v_pk_mul_f32 v[30:31], v[46:47], s[42:43] op_sel_hi:[1,0]
	v_pk_mul_f32 v[22:23], v[34:35], v[22:23]
	v_exp_f32_e32 v30, v30
	v_exp_f32_e32 v31, v31
	v_cndmask_b32_e32 v2, v49, v43, vcc
	v_cmp_gt_f32_e32 vcc, 0, v5
	v_cvt_pk_bf16_f32 v32, v6, v2
	v_pk_mul_f32 v[22:23], v[30:31], v[22:23]
	s_nop 0
	v_pk_mul_f32 v[30:31], v[4:5], v[22:23]
	v_pk_fma_f32 v[22:23], v[4:5], v[22:23], v[4:5] neg_lo:[1,0,0] neg_hi:[1,0,0]
	s_nop 0
	v_cndmask_b32_e32 v5, v23, v31, vcc
	v_cmp_gt_f32_e32 vcc, 0, v4
	v_cvt_pk_bf16_f32 v31, v25, v9
	s_nop 0
	v_cndmask_b32_e32 v4, v22, v30, vcc
	v_cvt_pk_bf16_f32 v30, v27, v15
	v_cvt_pk_bf16_f32 v33, v4, v5
	s_and_b64 vcc, exec, s[10:11]
	global_store_dwordx4 v[20:21], v[30:33], off offset:256 nt
	s_cbranch_vccnz .LBB0_278
	v_mov_b32_e32 v29, v27
	v_mov_b32_e32 v3, v7
	v_mov_b32_e32 v17, v15
	v_pk_add_f32 v[20:21], v[6:7], v[2:3]
	v_pk_mul_f32 v[22:23], v[6:7], v[2:3]
	v_mov_b32_e32 v30, v28
	v_pk_add_f32 v[34:35], v[26:27], v[28:29]
	v_pk_mul_f32 v[28:29], v[26:27], v[28:29]
	v_mov_b32_e32 v21, v23
	v_mov_b32_e32 v23, v14
	v_mov_b32_e32 v31, v16
	v_mov_b32_e32 v35, v29
	v_pk_add_f32 v[28:29], v[14:15], v[16:17]
	v_pk_mul_f32 v[16:17], v[14:15], v[16:17]
	v_and_b32_e32 v14, 64, v169
	v_xor_b32_e32 v13, 16, v169
	v_add_u32_e32 v14, 64, v14
	v_mov_b32_e32 v22, v26
	v_pk_mul_f32 v[30:31], v[30:31], v[30:31]
	v_mul_f32_e32 v8, v10, v10
	v_cmp_lt_i32_e32 vcc, v13, v14
	v_pk_fma_f32 v[22:23], v[22:23], v[22:23], v[30:31]
	v_pk_fma_f32 v[30:31], v[10:11], v[10:11], v[8:9] op_sel_hi:[1,1,0]
	v_mul_f32_e32 v8, v4, v4
	v_mov_b32_e32 v29, v17
	v_mul_f32_e32 v17, v25, v25
	v_mul_f32_e32 v37, v9, v9
	v_pk_mul_f32 v[38:39], v[6:7], v[6:7]
	v_pk_mul_f32 v[2:3], v[2:3], v[2:3]
	v_cndmask_b32_e32 v13, v169, v13, vcc
	v_mov_b32_e32 v16, v10
	v_mov_b32_e32 v36, v11
	v_pk_fma_f32 v[32:33], v[4:5], v[4:5], v[8:9] op_sel_hi:[1,1,0]
	v_mov_b32_e32 v24, v27
	v_mov_b32_e32 v8, v15
	v_lshlrev_b32_e32 v15, 2, v13
	v_mov_b32_e32 v13, v38
	v_pk_mov_b32 v[2:3], v[6:7], v[2:3] op_sel:[1,0]
	v_pk_add_f32 v[6:7], v[34:35], v[28:29]
	v_pk_add_f32 v[10:11], v[16:17], v[36:37]
	v_pk_add_f32 v[8:9], v[24:25], v[8:9]
	v_pk_add_f32 v[2:3], v[12:13], v[2:3]
	v_pk_add_f32 v[6:7], v[6:7], v[10:11]
	v_mul_f32_e32 v40, v12, v12
	v_pk_add_f32 v[22:23], v[22:23], v[22:23] op_sel_hi:[0,1]
	v_pk_add_f32 v[2:3], v[6:7], v[2:3]
	v_pk_add_f32 v[6:7], v[8:9], v[8:9] op_sel:[0,1] op_sel_hi:[1,0]
	v_mov_b32_e32 v22, v4
	v_mov_b32_e32 v30, v5
	v_mov_b32_e32 v7, v40
	v_mov_b32_e32 v32, v131
	v_pk_add_f32 v[4:5], v[22:23], v[30:31]
	v_pk_add_f32 v[6:7], v[6:7], v[20:21]
	v_pk_add_f32 v[2:3], v[2:3], v[32:33]
	v_pk_add_f32 v[4:5], v[6:7], v[4:5]
	v_xor_b32_e32 v6, 32, v169
	v_pk_add_f32 v[2:3], v[4:5], v[2:3]
	ds_bpermute_b32 v4, v15, v2
	ds_bpermute_b32 v5, v15, v3
	v_cmp_lt_i32_e32 vcc, v6, v14
	s_waitcnt lgkmcnt(0)
	v_pk_add_f32 v[2:3], v[2:3], v[4:5]
	v_cndmask_b32_e32 v6, v169, v6, vcc
	v_lshlrev_b32_e32 v6, 2, v6
	ds_bpermute_b32 v4, v6, v2
	ds_bpermute_b32 v5, v6, v3
	s_and_saveexec_b64 s[0:1], s[6:7]
	s_cbranch_execz .LBB0_277
	s_waitcnt lgkmcnt(0)
	v_pk_add_f32 v[2:3], v[2:3], v[4:5]
	v_lshlrev_b64 v[4:5], 7, v[18:19]
	v_lshl_add_u64 v[4:5], s[12:13], 0, v[4:5]
	global_store_dwordx2 v[4:5], v[2:3], off nt
